# P3 prep: cumulative gate loop re-paired via interleaved LDS tile (576 v_mov removed, steps 0..47); dtype comment added
# speedup vs baseline: 1.0575x; 1.0072x over previous
; #define LAS __attribute__((address_space(3)))
; __device__ __forceinline__ void prep_item(const Args& a, LAS unsigned char* lds, int tid, int dir, int b, int ch) {
;     ...
;     if (tid < 256) { const int i = tid >> 2, r4 = (tid & 3) * 4; const int row = scan_row(b, dir, ch * 64 + i);
;         *(LAS f32x4*)(alr + i * 16 + r4) = *(const f32x4*)(ALR + (size_t)row * 32 + dir * 16 + r4); }
;     { v4u kr[8], qr[8];
; #pragma unroll
;       for (int q = 0; q < 8; ++q) { const int p = tid + 512 * q, i = p >> 6, c8 = (p & 63) * 8; const int row = scan_row(b, dir, ch * 64 + i);
;           kr[q] = *(const v4u*)(Kb + (size_t)row * 512 + c8); if (lat) qr[q] = *(const v4u*)(Q + (size_t)row * 512 + c8); }
.LBB0_320:
	s_and_b32 s9, s59, 31
	s_add_i32 s16, s9, 4
	s_bfe_u32 s17, s59, 0x30005
	s_ashr_i32 s18, s59, 8
	v_readfirstlane_b32 s8, v66
	s_lshl_b32 s19, s16, 6
	s_and_saveexec_b64 s[2:3], s[0:1]
	s_cbranch_execz .LBB0_326
	v_add_u32_e32 v9, s19, v82
	v_cmp_lt_i32_e32 vcc, s20, v9
	s_and_saveexec_b64 s[4:5], vcc
	s_xor_b64 s[4:5], exec, s[4:5]
	s_cmpk_lt_u32 s59, 0x100
	v_add_u32_e32 v8, 0xffffff00, v9
	v_sub_u32_e32 v9, 0x8ff, v9
	s_cselect_b64 vcc, -1, 0
	v_cndmask_b32_e32 v8, v9, v8, vcc
	v_lshl_add_u32 v8, s17, 11, v8
	s_andn2_saveexec_b64 s[4:5], s[4:5]
	s_cmpk_lt_u32 s59, 0x100
	v_sub_u32_e32 v8, 0xff, v9
	s_cselect_b64 vcc, -1, 0
	v_cndmask_b32_e32 v8, v8, v9, vcc
	v_lshl_add_u32 v8, s17, 8, v8
	v_add_u32_e32 v8, 0x4000, v8
	s_or_b64 exec, exec, s[4:5]
	v_ashrrev_i32_e32 v9, 31, v8
	v_lshlrev_b64 v[8:9], 7, v[8:9]
	s_lshl_b32 s4, s18, 4
	v_lshl_add_u64 v[8:9], s[10:11], 0, v[8:9]
	s_ashr_i32 s5, s4, 31
	v_lshl_add_u64 v[8:9], s[4:5], 2, v[8:9]
	v_lshl_add_u64 v[8:9], v[8:9], 0, v[68:69]
	global_load_dwordx4 v[8:11], v[8:9], off
	s_waitcnt vmcnt(0)
	v_sub_u32_e32 v25, v83, v68
	v_and_b32_e32 v24, 16, v68
	v_lshrrev_b32_e32 v12, 5, v68
	v_lshlrev_b32_e32 v24, 1, v24
	v_lshl_add_u32 v24, v12, 2, v24
	v_add_u32_e32 v24, v24, v25
	s_mov_b64 s[100:101], exec
	v_cmp_gt_u32_e32 vcc, 0xc00, v25
	s_and_b64 exec, s[100:101], vcc
	ds_write2_b32 v24, v8, v9 offset1:2
	ds_write2_b32 v24, v10, v11 offset0:4 offset1:6
	s_andn2_b64 exec, s[100:101], vcc
	ds_write_b128 v83, v[8:11]
	s_mov_b64 exec, s[100:101]
.LBB0_326:
	s_or_b64 exec, exec, s[2:3]
	s_lshl_b32 s3, s17, 8
	v_add_u32_e32 v8, s19, v84
	s_lshl_b32 s2, s17, 11
	s_bitset1_b32 s3, 14
	v_cmp_gt_i32_e32 vcc, s21, v8
	s_cmpk_lt_u32 s59, 0x100
	v_add_u32_e32 v9, 0xffffff00, v8
	v_cndmask_b32_e32 v10, v43, v44, vcc
	v_mov_b32_e32 v12, s2
	v_mov_b32_e32 v13, s3
	v_cndmask_b32_e32 v9, v9, v8, vcc
	v_cndmask_b32_e32 v11, v12, v13, vcc
	v_sub_u32_e32 v8, v10, v8
	s_cselect_b64 vcc, -1, 0
	v_cndmask_b32_e32 v8, v8, v9, vcc
	v_add_u32_e32 v8, v8, v11
	v_ashrrev_i32_e32 v9, 31, v8
	v_lshlrev_b64 v[8:9], 10, v[8:9]
	v_lshl_add_u64 v[10:11], v[70:71], 0, v[8:9]
	v_lshl_add_u64 v[8:9], v[72:73], 0, v[8:9]
	global_load_dwordx4 v[24:27], v[10:11], off
	global_load_dwordx4 v[28:31], v[8:9], off
	v_add_u32_e32 v8, s19, v85
	v_cmp_gt_i32_e64 s[4:5], s21, v8
	v_add_u32_e32 v9, 0xffffff00, v8
	v_readlane_b32 s36, v246, 3
	v_cndmask_b32_e64 v10, v43, v44, s[4:5]
	v_cndmask_b32_e64 v9, v9, v8, s[4:5]
	v_sub_u32_e32 v8, v10, v8
	v_cndmask_b32_e64 v11, v12, v13, s[4:5]
	v_cndmask_b32_e32 v8, v8, v9, vcc
	v_add_u32_e32 v8, v8, v11
	v_ashrrev_i32_e32 v9, 31, v8
	v_lshlrev_b64 v[8:9], 10, v[8:9]
	v_lshl_add_u64 v[10:11], v[70:71], 0, v[8:9]
	v_lshl_add_u64 v[8:9], v[72:73], 0, v[8:9]
	global_load_dwordx4 v[32:35], v[10:11], off
	global_load_dwordx4 v[36:39], v[8:9], off
	v_add_u32_e32 v8, s19, v86
	v_cmp_gt_i32_e64 s[4:5], s21, v8
	v_add_u32_e32 v9, 0xffffff00, v8
	s_and_b64 s[2:3], vcc, exec
	v_cndmask_b32_e64 v10, v43, v44, s[4:5]
	v_cndmask_b32_e64 v9, v9, v8, s[4:5]
	v_sub_u32_e32 v8, v10, v8
	v_cndmask_b32_e64 v11, v12, v13, s[4:5]
	v_cndmask_b32_e32 v8, v8, v9, vcc
	v_add_u32_e32 v8, v8, v11
	v_ashrrev_i32_e32 v9, 31, v8
	v_lshlrev_b64 v[8:9], 10, v[8:9]
	v_lshl_add_u64 v[10:11], v[70:71], 0, v[8:9]
	v_lshl_add_u64 v[8:9], v[72:73], 0, v[8:9]
	global_load_dwordx4 v[50:53], v[10:11], off
	global_load_dwordx4 v[54:57], v[8:9], off
	v_add_u32_e32 v8, s19, v87
	v_cmp_gt_i32_e64 s[4:5], s21, v8
	v_add_u32_e32 v9, 0xffffff00, v8
	v_readlane_b32 s42, v246, 9
	v_cndmask_b32_e64 v10, v43, v44, s[4:5]
	v_cndmask_b32_e64 v9, v9, v8, s[4:5]
	v_sub_u32_e32 v8, v10, v8
	v_cndmask_b32_e64 v11, v12, v13, s[4:5]
	v_cndmask_b32_e32 v8, v8, v9, vcc
	v_add_u32_e32 v8, v8, v11
	v_ashrrev_i32_e32 v9, 31, v8
	v_lshlrev_b64 v[8:9], 10, v[8:9]
	v_lshl_add_u64 v[10:11], v[70:71], 0, v[8:9]
	v_lshl_add_u64 v[8:9], v[72:73], 0, v[8:9]
	global_load_dwordx4 v[58:61], v[10:11], off
	global_load_dwordx4 v[62:65], v[8:9], off
	v_add_u32_e32 v8, s19, v88
	v_cmp_gt_i32_e64 s[4:5], s21, v8
	v_add_u32_e32 v9, 0xffffff00, v8
	v_readlane_b32 s43, v246, 10
	v_cndmask_b32_e64 v10, v43, v44, s[4:5]
	v_cndmask_b32_e64 v9, v9, v8, s[4:5]
	v_sub_u32_e32 v8, v10, v8
	v_cndmask_b32_e64 v11, v12, v13, s[4:5]
	v_cndmask_b32_e32 v8, v8, v9, vcc
	v_add_u32_e32 v8, v8, v11
	v_ashrrev_i32_e32 v9, 31, v8
	v_lshlrev_b64 v[8:9], 10, v[8:9]
	v_lshl_add_u64 v[10:11], v[70:71], 0, v[8:9]
	v_lshl_add_u64 v[8:9], v[72:73], 0, v[8:9]
	global_load_dwordx4 v[196:199], v[10:11], off
	global_load_dwordx4 v[200:203], v[8:9], off
	v_add_u32_e32 v8, s19, v89
	v_cmp_gt_i32_e64 s[4:5], s21, v8
	v_add_u32_e32 v9, 0xffffff00, v8
	v_readlane_b32 s46, v246, 13
	v_cndmask_b32_e64 v10, v43, v44, s[4:5]
	v_cndmask_b32_e64 v9, v9, v8, s[4:5]
	v_sub_u32_e32 v8, v10, v8
	v_cndmask_b32_e64 v11, v12, v13, s[4:5]
	v_cndmask_b32_e32 v8, v8, v9, vcc
	v_add_u32_e32 v8, v8, v11
	v_ashrrev_i32_e32 v9, 31, v8
	v_lshlrev_b64 v[8:9], 10, v[8:9]
	v_lshl_add_u64 v[10:11], v[70:71], 0, v[8:9]
	v_lshl_add_u64 v[8:9], v[72:73], 0, v[8:9]
	global_load_dwordx4 v[204:207], v[10:11], off
	global_load_dwordx4 v[208:211], v[8:9], off
	v_add_u32_e32 v8, s19, v90
	v_cmp_gt_i32_e64 s[4:5], s21, v8
	v_add_u32_e32 v9, 0xffffff00, v8
	v_readlane_b32 s47, v246, 14
	v_cndmask_b32_e64 v10, v43, v44, s[4:5]
	v_cndmask_b32_e64 v9, v9, v8, s[4:5]
	v_sub_u32_e32 v8, v10, v8
	v_cndmask_b32_e64 v11, v12, v13, s[4:5]
	v_cndmask_b32_e32 v8, v8, v9, vcc
	v_add_u32_e32 v8, v8, v11
	v_ashrrev_i32_e32 v9, 31, v8
	v_lshlrev_b64 v[8:9], 10, v[8:9]
	v_lshl_add_u64 v[10:11], v[70:71], 0, v[8:9]
	v_lshl_add_u64 v[8:9], v[72:73], 0, v[8:9]
; #define LAS __attribute__((address_space(3)))
; #define LDS_BARRIER() do { asm volatile("s_waitcnt lgkmcnt(0)" ::: "memory"); __builtin_amdgcn_s_barrier(); asm volatile("" ::: "memory"); } while (0)
; __device__ __forceinline__ void prep_item(const Args& a, LAS unsigned char* lds, int tid, int dir, int b, int ch) {
;     ...
;       for (int q = 0; q < 8; ++q) { const int p = tid + 512 * q, i = p >> 6, c8 = (p & 63) * 8; const int row = scan_row(b, dir, ch * 64 + i);
;           kr[q] = *(const v4u*)(Kb + (size_t)row * 512 + c8); if (lat) qr[q] = *(const v4u*)(Q + (size_t)row * 512 + c8); }
; #pragma unroll
;       for (int q = 0; q < 8; ++q) { const int p = tid + 512 * q, i = p >> 6, c8 = (p & 63) * 8; *(LAS v4u*)(Kt + i * TS + c8) = kr[q]; if (lat) *(LAS v4u*)(Qt + i * TS + c8) = qr[q]; } }
;     const float* wa2 = dir ? a.in[13] : a.in[11]; const float bia = (dir ? a.in[14] : a.in[12])[col];
;     float w[16];
; #pragma unroll
;     for (int r = 0; r < 16; ++r) w[r] = wa2[r * 512 + col];
;     LDS_BARRIER();
;     float Gv[64]; float Gc = 0.f;
; #pragma unroll
;     for (int i = 0; i < 64; ++i) { float zp[4];
; #pragma unroll
;         for (int r4 = 0; r4 < 4; ++r4) { const f32x4 x = *(const LAS f32x4*)(alr + i * 16 + 4 * r4); zp[r4] = x[0] * w[4 * r4] + x[1] * w[4 * r4 + 1] + x[2] * w[4 * r4 + 2] + x[3] * w[4 * r4 + 3]; }
;         const float z = bia + ((zp[0] + zp[1]) + (zp[2] + zp[3]));
	global_load_dwordx4 v[212:215], v[10:11], off
	global_load_dwordx4 v[216:219], v[8:9], off
	v_add_u32_e32 v8, s19, v91
	v_cmp_gt_i32_e64 s[4:5], s21, v8
	v_add_u32_e32 v9, 0xffffff00, v8
	s_cselect_b32 s3, s43, s47
	v_cndmask_b32_e64 v10, v43, v44, s[4:5]
	v_cndmask_b32_e64 v9, v9, v8, s[4:5]
	v_sub_u32_e32 v8, v10, v8
	v_cndmask_b32_e64 v11, v12, v13, s[4:5]
	v_cndmask_b32_e32 v8, v8, v9, vcc
	v_add_u32_e32 v8, v8, v11
	v_ashrrev_i32_e32 v9, 31, v8
	v_lshlrev_b64 v[8:9], 10, v[8:9]
	s_cselect_b32 s2, s42, s46
	v_lshl_add_u64 v[10:11], v[70:71], 0, v[8:9]
	v_lshl_add_u64 v[8:9], v[72:73], 0, v[8:9]
	v_lshl_add_u64 v[16:17], s[2:3], 0, v[4:5]
	global_load_dwordx4 v[220:223], v[10:11], off
	global_load_dwordx4 v[228:231], v[8:9], off
	v_add_co_u32_e32 v8, vcc, s23, v16
	v_readlane_b32 s44, v246, 11
	s_nop 0
	v_addc_co_u32_e32 v9, vcc, 0, v17, vcc
	v_add_co_u32_e32 v18, vcc, s27, v16
	v_readlane_b32 s45, v246, 12
	s_nop 0
	v_addc_co_u32_e32 v19, vcc, 0, v17, vcc
	v_add_co_u32_e32 v46, vcc, s28, v16
	v_readlane_b32 s48, v246, 15
	s_nop 0
	v_addc_co_u32_e32 v47, vcc, 0, v17, vcc
	v_add_co_u32_e32 v48, vcc, s22, v16
	v_readlane_b32 s49, v246, 16
	s_nop 0
	v_addc_co_u32_e32 v49, vcc, 0, v17, vcc
	v_add_co_u32_e32 v12, vcc, s29, v16
	global_load_dword v11, v[48:49], off
	global_load_dword v15, v[48:49], off offset:2048
	v_addc_co_u32_e32 v13, vcc, 0, v17, vcc
	v_add_co_u32_e32 v78, vcc, s30, v16
	s_cselect_b32 s5, s45, s49
	s_nop 0
	v_addc_co_u32_e32 v79, vcc, 0, v17, vcc
	global_load_dword v10, v[16:17], off
	global_load_dword v14, v[16:17], off offset:2048
	global_load_dword v22, v[18:19], off offset:-4096
	global_load_dword v20, v[8:9], off offset:2048
	global_load_dword v21, v[12:13], off offset:2048
	global_load_dword v23, v[78:79], off offset:-4096
	s_nop 0
	global_load_dword v12, v[18:19], off
	s_nop 0
	global_load_dword v18, v[18:19], off offset:2048
	s_nop 0
	global_load_dword v8, v[48:49], off offset:-4096
	global_load_dword v13, v[78:79], off
	global_load_dword v19, v[78:79], off offset:2048
	v_add_co_u32_e32 v48, vcc, s31, v16
	s_cselect_b32 s4, s44, s48
	s_nop 0
	v_addc_co_u32_e32 v49, vcc, 0, v17, vcc
	global_load_dword v9, v[48:49], off
	global_load_dword v16, v[46:47], off offset:2048
	global_load_dword v17, v[48:49], off offset:2048
	v_lshl_add_u64 v[46:47], s[4:5], 0, v[4:5]
	global_load_dword v48, v[46:47], off
	s_waitcnt vmcnt(0)
	ds_write_b128 v92, v[24:27] offset:4096
	ds_write_b128 v93, v[28:31]
	ds_write_b128 v94, v[32:35] offset:4096
	ds_write_b128 v95, v[36:39]
	ds_write_b128 v96, v[50:53] offset:4096
	ds_write_b128 v97, v[54:57]
	ds_write_b128 v98, v[58:61] offset:4096
	ds_write_b128 v99, v[62:65]
	ds_write_b128 v100, v[196:199] offset:4096
	ds_write_b128 v101, v[200:203]
	ds_write_b128 v102, v[204:207] offset:4096
	ds_write_b128 v103, v[208:211]
	ds_write_b128 v104, v[212:215] offset:4096
	ds_write_b128 v105, v[216:219]
	ds_write_b128 v106, v[220:223] offset:4096
	ds_write_b128 v107, v[228:231]
	s_waitcnt lgkmcnt(0)
	s_barrier
	ds_read_b128 v[24:27], v69
	ds_read_b128 v[28:31], v69 offset:16
	ds_read_b128 v[32:35], v69 offset:32
	ds_read_b128 v[36:39], v69 offset:48
	s_waitcnt lgkmcnt(0)
	v_pk_mul_f32 v[26:27], v[14:15], v[26:27]
	v_pk_mul_f32 v[34:35], v[18:19], v[34:35]
	v_pk_fma_f32 v[24:25], v[10:11], v[24:25], v[26:27]
	v_pk_fma_f32 v[26:27], v[12:13], v[32:33], v[34:35]
	v_pk_fma_f32 v[24:25], v[22:23], v[28:29], v[24:25]
	v_pk_fma_f32 v[26:27], v[8:9], v[36:37], v[26:27]
	v_pk_fma_f32 v[24:25], v[20:21], v[30:31], v[24:25]
	v_pk_fma_f32 v[26:27], v[16:17], v[38:39], v[26:27]
	s_nop 0
	s_lshl_b32 s2, s18, 3
	s_or_b32 s4, s2, s17
	s_ashr_i32 s5, s4, 31
	s_mul_i32 s2, s4, 36
	s_mul_hi_i32 s3, s4, 36
	s_add_u32 s2, s2, s16
	s_addc_u32 s3, s3, 0
	s_lshl_b64 s[16:17], s[2:3], 11
	s_lshl_b64 s[2:3], s[2:3], 16
	v_readlane_b32 s37, v246, 4
	v_readlane_b32 s38, v246, 5
	v_readlane_b32 s39, v246, 6
	v_readlane_b32 s40, v246, 7
	v_readlane_b32 s41, v246, 8
	v_readlane_b32 s50, v246, 17
	v_readlane_b32 s51, v246, 18
	v_pk_add_f32 v[24:25], v[24:25], v[26:27]
	s_nop 0
	v_add_f32_e32 v24, v24, v25
	v_add_f32_e32 v24, v48, v24
	v_mul_f32_e64 v25, |v24|, s34
	v_exp_f32_e32 v25, v25
	v_min_f32_e32 v32, 0, v24
	v_add_f32_e32 v25, 1.0, v25
	v_log_f32_e32 v33, v25
	ds_read_b128 v[24:27], v69 offset:64
	ds_read_b128 v[28:31], v69 offset:80
	v_pk_mul_f32 v[46:47], v[32:33], s[14:15]
	ds_read_b128 v[32:35], v69 offset:96
	ds_read_b128 v[36:39], v69 offset:112
	s_waitcnt lgkmcnt(0)
	v_pk_mul_f32 v[26:27], v[14:15], v[26:27]
	v_pk_mul_f32 v[34:35], v[18:19], v[34:35]
	v_pk_fma_f32 v[24:25], v[10:11], v[24:25], v[26:27]
	v_pk_fma_f32 v[26:27], v[12:13], v[32:33], v[34:35]
	v_pk_fma_f32 v[24:25], v[22:23], v[28:29], v[24:25]
	v_pk_fma_f32 v[26:27], v[8:9], v[36:37], v[26:27]
	v_pk_fma_f32 v[24:25], v[20:21], v[30:31], v[24:25]
	v_pk_fma_f32 v[26:27], v[16:17], v[38:39], v[26:27]
	s_nop 0
	v_pk_add_f32 v[24:25], v[24:25], v[26:27]
	v_sub_f32_e32 v26, v46, v47
	v_add_f32_e32 v24, v24, v25
	v_add_f32_e32 v24, v48, v24
	v_mul_f32_e64 v25, |v24|, s34
	v_exp_f32_e32 v25, v25
	v_add_f32_e32 v46, 0, v26
	v_min_f32_e32 v50, 0, v24
	v_add_f32_e32 v32, 1.0, v25
	ds_read_b128 v[24:27], v69 offset:128
	ds_read_b128 v[28:31], v69 offset:144
	v_log_f32_e32 v51, v32
	ds_read_b128 v[32:35], v69 offset:160
	ds_read_b128 v[36:39], v69 offset:176
	s_waitcnt lgkmcnt(0)
; #define LAS __attribute__((address_space(3)))
; __device__ __forceinline__ void prep_item(const Args& a, LAS unsigned char* lds, int tid, int dir, int b, int ch) {
;     ...
;     for (int i = 0; i < 64; ++i) { float zp[4];
; #pragma unroll
;         for (int r4 = 0; r4 < 4; ++r4) { const f32x4 x = *(const LAS f32x4*)(alr + i * 16 + 4 * r4); zp[r4] = x[0] * w[4 * r4] + x[1] * w[4 * r4 + 1] + x[2] * w[4 * r4 + 2] + x[3] * w[4 * r4 + 3]; }
;         const float z = bia + ((zp[0] + zp[1]) + (zp[2] + zp[3]));
;         Gc += fminf(z, 0.f) * (L2E / 16.f) - __builtin_amdgcn_logf(1.f + __builtin_amdgcn_exp2f(-fabsf(z) * L2E)) * (1.f / 16.f); Gv[i] = Gc; }
	v_pk_mul_f32 v[26:27], v[14:15], v[26:27]
	v_pk_mul_f32 v[34:35], v[18:19], v[34:35]
	v_pk_fma_f32 v[24:25], v[10:11], v[24:25], v[26:27]
	v_pk_fma_f32 v[26:27], v[12:13], v[32:33], v[34:35]
	v_pk_fma_f32 v[24:25], v[22:23], v[28:29], v[24:25]
	v_pk_fma_f32 v[26:27], v[8:9], v[36:37], v[26:27]
	v_pk_fma_f32 v[24:25], v[20:21], v[30:31], v[24:25]
	v_pk_fma_f32 v[26:27], v[16:17], v[38:39], v[26:27]
	s_nop 0
	v_pk_add_f32 v[24:25], v[24:25], v[26:27]
	s_nop 0
	v_add_f32_e32 v24, v24, v25
	v_add_f32_e32 v26, v48, v24
	v_mul_f32_e64 v24, |v26|, s34
	v_exp_f32_e32 v27, v24
	v_pk_mul_f32 v[24:25], v[50:51], s[14:15]
	v_min_f32_e32 v32, 0, v26
	v_sub_f32_e32 v24, v24, v25
	v_add_f32_e32 v49, v46, v24
	v_add_f32_e32 v24, 1.0, v27
	v_log_f32_e32 v33, v24
	ds_read_b128 v[24:27], v69 offset:192
	ds_read_b128 v[28:31], v69 offset:208
	v_pk_mul_f32 v[50:51], v[32:33], s[14:15]
	ds_read_b128 v[32:35], v69 offset:224
	ds_read_b128 v[36:39], v69 offset:240
	s_waitcnt lgkmcnt(0)
	v_pk_mul_f32 v[26:27], v[14:15], v[26:27]
	v_pk_mul_f32 v[34:35], v[18:19], v[34:35]
	v_pk_fma_f32 v[24:25], v[10:11], v[24:25], v[26:27]
	v_pk_fma_f32 v[26:27], v[12:13], v[32:33], v[34:35]
	v_pk_fma_f32 v[24:25], v[22:23], v[28:29], v[24:25]
	v_pk_fma_f32 v[26:27], v[8:9], v[36:37], v[26:27]
	v_pk_fma_f32 v[24:25], v[20:21], v[30:31], v[24:25]
	v_pk_fma_f32 v[26:27], v[16:17], v[38:39], v[26:27]
	s_nop 0
	v_pk_add_f32 v[24:25], v[24:25], v[26:27]
	v_sub_f32_e32 v26, v50, v51
	v_add_f32_e32 v24, v24, v25
	v_add_f32_e32 v24, v48, v24
	v_mul_f32_e64 v25, |v24|, s34
	v_exp_f32_e32 v25, v25
	v_add_f32_e32 v51, v49, v26
	v_min_f32_e32 v52, 0, v24
	v_add_f32_e32 v32, 1.0, v25
	ds_read_b128 v[24:27], v69 offset:256
	ds_read_b128 v[28:31], v69 offset:272
	v_log_f32_e32 v53, v32
	ds_read_b128 v[32:35], v69 offset:288
	ds_read_b128 v[36:39], v69 offset:304
	s_waitcnt lgkmcnt(0)
	v_pk_mul_f32 v[26:27], v[14:15], v[26:27]
	v_pk_mul_f32 v[34:35], v[18:19], v[34:35]
	v_pk_fma_f32 v[24:25], v[10:11], v[24:25], v[26:27]
	v_pk_fma_f32 v[26:27], v[12:13], v[32:33], v[34:35]
	v_pk_fma_f32 v[24:25], v[22:23], v[28:29], v[24:25]
	v_pk_fma_f32 v[26:27], v[8:9], v[36:37], v[26:27]
	v_pk_fma_f32 v[24:25], v[20:21], v[30:31], v[24:25]
	v_pk_fma_f32 v[26:27], v[16:17], v[38:39], v[26:27]
	s_nop 0
	v_pk_add_f32 v[24:25], v[24:25], v[26:27]
	s_nop 0
	v_add_f32_e32 v24, v24, v25
	v_add_f32_e32 v26, v48, v24
	v_mul_f32_e64 v24, |v26|, s34
	v_exp_f32_e32 v27, v24
	v_pk_mul_f32 v[24:25], v[52:53], s[14:15]
	v_min_f32_e32 v32, 0, v26
	v_sub_f32_e32 v24, v24, v25
	v_add_f32_e32 v53, v51, v24
	v_add_f32_e32 v24, 1.0, v27
	v_log_f32_e32 v33, v24
	ds_read_b128 v[24:27], v69 offset:320
	ds_read_b128 v[28:31], v69 offset:336
	v_pk_mul_f32 v[54:55], v[32:33], s[14:15]
	ds_read_b128 v[32:35], v69 offset:352
	ds_read_b128 v[36:39], v69 offset:368
	s_waitcnt lgkmcnt(0)
	v_pk_mul_f32 v[26:27], v[14:15], v[26:27]
	v_pk_mul_f32 v[34:35], v[18:19], v[34:35]
	v_pk_fma_f32 v[24:25], v[10:11], v[24:25], v[26:27]
	v_pk_fma_f32 v[26:27], v[12:13], v[32:33], v[34:35]
	v_pk_fma_f32 v[24:25], v[22:23], v[28:29], v[24:25]
	v_pk_fma_f32 v[26:27], v[8:9], v[36:37], v[26:27]
	v_pk_fma_f32 v[24:25], v[20:21], v[30:31], v[24:25]
	v_pk_fma_f32 v[26:27], v[16:17], v[38:39], v[26:27]
	s_nop 0
	v_pk_add_f32 v[24:25], v[24:25], v[26:27]
	v_sub_f32_e32 v26, v54, v55
	v_add_f32_e32 v24, v24, v25
	v_add_f32_e32 v24, v48, v24
	v_mul_f32_e64 v25, |v24|, s34
	v_exp_f32_e32 v25, v25
	v_add_f32_e32 v55, v53, v26
	v_min_f32_e32 v56, 0, v24
	v_add_f32_e32 v32, 1.0, v25
	ds_read_b128 v[24:27], v69 offset:384
	ds_read_b128 v[28:31], v69 offset:400
	v_log_f32_e32 v57, v32
	ds_read_b128 v[32:35], v69 offset:416
	ds_read_b128 v[36:39], v69 offset:432
	s_waitcnt lgkmcnt(0)
	v_pk_mul_f32 v[26:27], v[14:15], v[26:27]
	v_pk_mul_f32 v[34:35], v[18:19], v[34:35]
	v_pk_fma_f32 v[24:25], v[10:11], v[24:25], v[26:27]
	v_pk_fma_f32 v[26:27], v[12:13], v[32:33], v[34:35]
	v_pk_fma_f32 v[24:25], v[22:23], v[28:29], v[24:25]
	v_pk_fma_f32 v[26:27], v[8:9], v[36:37], v[26:27]
	v_pk_fma_f32 v[24:25], v[20:21], v[30:31], v[24:25]
	v_pk_fma_f32 v[26:27], v[16:17], v[38:39], v[26:27]
	s_nop 0
	v_pk_add_f32 v[24:25], v[24:25], v[26:27]
	s_nop 0
	v_add_f32_e32 v24, v24, v25
	v_add_f32_e32 v26, v48, v24
	v_mul_f32_e64 v24, |v26|, s34
	v_exp_f32_e32 v27, v24
	v_pk_mul_f32 v[24:25], v[56:57], s[14:15]
	v_min_f32_e32 v32, 0, v26
	v_sub_f32_e32 v24, v24, v25
	v_add_f32_e32 v58, v55, v24
	v_add_f32_e32 v24, 1.0, v27
	v_log_f32_e32 v33, v24
	ds_read_b128 v[24:27], v69 offset:448
	ds_read_b128 v[28:31], v69 offset:464
	v_pk_mul_f32 v[56:57], v[32:33], s[14:15]
	ds_read_b128 v[32:35], v69 offset:480
	ds_read_b128 v[36:39], v69 offset:496
	s_waitcnt lgkmcnt(0)
	v_pk_mul_f32 v[26:27], v[14:15], v[26:27]
	v_pk_mul_f32 v[34:35], v[18:19], v[34:35]
	v_pk_fma_f32 v[24:25], v[10:11], v[24:25], v[26:27]
	v_pk_fma_f32 v[26:27], v[12:13], v[32:33], v[34:35]
	v_pk_fma_f32 v[24:25], v[22:23], v[28:29], v[24:25]
	v_pk_fma_f32 v[26:27], v[8:9], v[36:37], v[26:27]
	v_pk_fma_f32 v[24:25], v[20:21], v[30:31], v[24:25]
	v_pk_fma_f32 v[26:27], v[16:17], v[38:39], v[26:27]
	s_nop 0
	v_pk_add_f32 v[24:25], v[24:25], v[26:27]
	v_sub_f32_e32 v26, v56, v57
	v_add_f32_e32 v24, v24, v25
	v_add_f32_e32 v24, v48, v24
	v_mul_f32_e64 v25, |v24|, s34
	v_exp_f32_e32 v25, v25
	v_add_f32_e32 v61, v58, v26
	v_min_f32_e32 v56, 0, v24
	v_add_f32_e32 v32, 1.0, v25
	ds_read_b128 v[24:27], v69 offset:512
	ds_read_b128 v[28:31], v69 offset:528
	v_log_f32_e32 v57, v32
	ds_read_b128 v[32:35], v69 offset:544
	ds_read_b128 v[36:39], v69 offset:560
	s_waitcnt lgkmcnt(0)
; #define LAS __attribute__((address_space(3)))
; __device__ __forceinline__ void prep_item(const Args& a, LAS unsigned char* lds, int tid, int dir, int b, int ch) {
;     ...
;     for (int i = 0; i < 64; ++i) { float zp[4];
; #pragma unroll
;         for (int r4 = 0; r4 < 4; ++r4) { const f32x4 x = *(const LAS f32x4*)(alr + i * 16 + 4 * r4); zp[r4] = x[0] * w[4 * r4] + x[1] * w[4 * r4 + 1] + x[2] * w[4 * r4 + 2] + x[3] * w[4 * r4 + 3]; }
;         const float z = bia + ((zp[0] + zp[1]) + (zp[2] + zp[3]));
;         Gc += fminf(z, 0.f) * (L2E / 16.f) - __builtin_amdgcn_logf(1.f + __builtin_amdgcn_exp2f(-fabsf(z) * L2E)) * (1.f / 16.f); Gv[i] = Gc; }
	v_pk_mul_f32 v[26:27], v[14:15], v[26:27]
	v_pk_mul_f32 v[34:35], v[18:19], v[34:35]
	v_pk_fma_f32 v[24:25], v[10:11], v[24:25], v[26:27]
	v_pk_fma_f32 v[26:27], v[12:13], v[32:33], v[34:35]
	v_pk_fma_f32 v[24:25], v[22:23], v[28:29], v[24:25]
	v_pk_fma_f32 v[26:27], v[8:9], v[36:37], v[26:27]
	v_pk_fma_f32 v[24:25], v[20:21], v[30:31], v[24:25]
	v_pk_fma_f32 v[26:27], v[16:17], v[38:39], v[26:27]
	s_nop 0
	v_pk_add_f32 v[24:25], v[24:25], v[26:27]
	s_nop 0
	v_add_f32_e32 v24, v24, v25
	v_add_f32_e32 v26, v48, v24
	v_mul_f32_e64 v24, |v26|, s34
	v_exp_f32_e32 v27, v24
	v_pk_mul_f32 v[24:25], v[56:57], s[14:15]
	v_min_f32_e32 v32, 0, v26
	v_sub_f32_e32 v24, v24, v25
	v_add_f32_e32 v64, v61, v24
	v_add_f32_e32 v24, 1.0, v27
	v_log_f32_e32 v33, v24
	ds_read_b128 v[24:27], v69 offset:576
	ds_read_b128 v[28:31], v69 offset:592
	v_pk_mul_f32 v[56:57], v[32:33], s[14:15]
	ds_read_b128 v[32:35], v69 offset:608
	ds_read_b128 v[36:39], v69 offset:624
	s_waitcnt lgkmcnt(0)
	v_pk_mul_f32 v[26:27], v[14:15], v[26:27]
	v_pk_mul_f32 v[34:35], v[18:19], v[34:35]
	v_pk_fma_f32 v[24:25], v[10:11], v[24:25], v[26:27]
	v_pk_fma_f32 v[26:27], v[12:13], v[32:33], v[34:35]
	v_pk_fma_f32 v[24:25], v[22:23], v[28:29], v[24:25]
	v_pk_fma_f32 v[26:27], v[8:9], v[36:37], v[26:27]
	v_pk_fma_f32 v[24:25], v[20:21], v[30:31], v[24:25]
	v_pk_fma_f32 v[26:27], v[16:17], v[38:39], v[26:27]
	s_nop 0
	v_pk_add_f32 v[24:25], v[24:25], v[26:27]
	v_sub_f32_e32 v26, v56, v57
	v_add_f32_e32 v24, v24, v25
	v_add_f32_e32 v24, v48, v24
	v_mul_f32_e64 v25, |v24|, s34
	v_exp_f32_e32 v25, v25
	v_add_f32_e32 v57, v64, v26
	v_min_f32_e32 v62, 0, v24
	v_add_f32_e32 v32, 1.0, v25
	ds_read_b128 v[24:27], v69 offset:640
	ds_read_b128 v[28:31], v69 offset:656
	v_log_f32_e32 v63, v32
	ds_read_b128 v[32:35], v69 offset:672
	ds_read_b128 v[36:39], v69 offset:688
	s_waitcnt lgkmcnt(0)
	v_pk_mul_f32 v[26:27], v[14:15], v[26:27]
	v_pk_mul_f32 v[34:35], v[18:19], v[34:35]
	v_pk_fma_f32 v[24:25], v[10:11], v[24:25], v[26:27]
	v_pk_fma_f32 v[26:27], v[12:13], v[32:33], v[34:35]
	v_pk_fma_f32 v[24:25], v[22:23], v[28:29], v[24:25]
	v_pk_fma_f32 v[26:27], v[8:9], v[36:37], v[26:27]
	v_pk_fma_f32 v[24:25], v[20:21], v[30:31], v[24:25]
	v_pk_fma_f32 v[26:27], v[16:17], v[38:39], v[26:27]
	s_nop 0
	v_pk_add_f32 v[24:25], v[24:25], v[26:27]
	s_nop 0
	v_add_f32_e32 v24, v24, v25
	v_add_f32_e32 v26, v48, v24
	v_mul_f32_e64 v24, |v26|, s34
	v_exp_f32_e32 v27, v24
	v_pk_mul_f32 v[24:25], v[62:63], s[14:15]
	v_min_f32_e32 v32, 0, v26
	v_sub_f32_e32 v24, v24, v25
	v_add_f32_e32 v60, v57, v24
	v_add_f32_e32 v24, 1.0, v27
	v_log_f32_e32 v33, v24
	ds_read_b128 v[24:27], v69 offset:704
	ds_read_b128 v[28:31], v69 offset:720
	v_pk_mul_f32 v[62:63], v[32:33], s[14:15]
	ds_read_b128 v[32:35], v69 offset:736
	ds_read_b128 v[36:39], v69 offset:752
	s_waitcnt lgkmcnt(0)
	v_pk_mul_f32 v[26:27], v[14:15], v[26:27]
	v_pk_mul_f32 v[34:35], v[18:19], v[34:35]
	v_pk_fma_f32 v[24:25], v[10:11], v[24:25], v[26:27]
	v_pk_fma_f32 v[26:27], v[12:13], v[32:33], v[34:35]
	v_pk_fma_f32 v[24:25], v[22:23], v[28:29], v[24:25]
	v_pk_fma_f32 v[26:27], v[8:9], v[36:37], v[26:27]
	v_pk_fma_f32 v[24:25], v[20:21], v[30:31], v[24:25]
	v_pk_fma_f32 v[26:27], v[16:17], v[38:39], v[26:27]
	s_nop 0
	v_pk_add_f32 v[24:25], v[24:25], v[26:27]
	v_sub_f32_e32 v26, v62, v63
	v_add_f32_e32 v24, v24, v25
	v_add_f32_e32 v24, v48, v24
	v_mul_f32_e64 v25, |v24|, s34
	v_exp_f32_e32 v25, v25
	v_add_f32_e32 v63, v60, v26
	v_min_f32_e32 v78, 0, v24
	v_add_f32_e32 v32, 1.0, v25
	ds_read_b128 v[24:27], v69 offset:768
	ds_read_b128 v[28:31], v69 offset:784
	v_log_f32_e32 v79, v32
	ds_read_b128 v[32:35], v69 offset:800
	ds_read_b128 v[36:39], v69 offset:816
	s_waitcnt lgkmcnt(0)
	v_pk_mul_f32 v[26:27], v[14:15], v[26:27]
	v_pk_mul_f32 v[34:35], v[18:19], v[34:35]
	v_pk_fma_f32 v[24:25], v[10:11], v[24:25], v[26:27]
	v_pk_fma_f32 v[26:27], v[12:13], v[32:33], v[34:35]
	v_pk_fma_f32 v[24:25], v[22:23], v[28:29], v[24:25]
	v_pk_fma_f32 v[26:27], v[8:9], v[36:37], v[26:27]
	v_pk_fma_f32 v[24:25], v[20:21], v[30:31], v[24:25]
	v_pk_fma_f32 v[26:27], v[16:17], v[38:39], v[26:27]
	s_nop 0
	v_pk_add_f32 v[24:25], v[24:25], v[26:27]
	s_nop 0
	v_add_f32_e32 v24, v24, v25
	v_add_f32_e32 v26, v48, v24
	v_mul_f32_e64 v24, |v26|, s34
	v_exp_f32_e32 v27, v24
	v_pk_mul_f32 v[24:25], v[78:79], s[14:15]
	v_min_f32_e32 v32, 0, v26
	v_sub_f32_e32 v24, v24, v25
	v_add_f32_e32 v78, v63, v24
	v_add_f32_e32 v24, 1.0, v27
	v_log_f32_e32 v33, v24
	ds_read_b128 v[24:27], v69 offset:832
	ds_read_b128 v[28:31], v69 offset:848
	v_pk_mul_f32 v[196:197], v[32:33], s[14:15]
	ds_read_b128 v[32:35], v69 offset:864
	ds_read_b128 v[36:39], v69 offset:880
	s_waitcnt lgkmcnt(0)
	v_pk_mul_f32 v[26:27], v[14:15], v[26:27]
	v_pk_mul_f32 v[34:35], v[18:19], v[34:35]
	v_pk_fma_f32 v[24:25], v[10:11], v[24:25], v[26:27]
	v_pk_fma_f32 v[26:27], v[12:13], v[32:33], v[34:35]
	v_pk_fma_f32 v[24:25], v[22:23], v[28:29], v[24:25]
	v_pk_fma_f32 v[26:27], v[8:9], v[36:37], v[26:27]
	v_pk_fma_f32 v[24:25], v[20:21], v[30:31], v[24:25]
	v_pk_fma_f32 v[26:27], v[16:17], v[38:39], v[26:27]
	s_nop 0
	v_pk_add_f32 v[24:25], v[24:25], v[26:27]
	v_sub_f32_e32 v26, v196, v197
	v_add_f32_e32 v24, v24, v25
	v_add_f32_e32 v24, v48, v24
	v_mul_f32_e64 v25, |v24|, s34
	v_exp_f32_e32 v25, v25
	v_add_f32_e32 v79, v78, v26
	v_min_f32_e32 v196, 0, v24
	v_add_f32_e32 v32, 1.0, v25
	ds_read_b128 v[24:27], v69 offset:896
	ds_read_b128 v[28:31], v69 offset:912
	v_log_f32_e32 v197, v32
	ds_read_b128 v[32:35], v69 offset:928
	ds_read_b128 v[36:39], v69 offset:944
	s_waitcnt lgkmcnt(0)
; #define LAS __attribute__((address_space(3)))
; __device__ __forceinline__ void prep_item(const Args& a, LAS unsigned char* lds, int tid, int dir, int b, int ch) {
;     ...
;     for (int i = 0; i < 64; ++i) { float zp[4];
; #pragma unroll
;         for (int r4 = 0; r4 < 4; ++r4) { const f32x4 x = *(const LAS f32x4*)(alr + i * 16 + 4 * r4); zp[r4] = x[0] * w[4 * r4] + x[1] * w[4 * r4 + 1] + x[2] * w[4 * r4 + 2] + x[3] * w[4 * r4 + 3]; }
;         const float z = bia + ((zp[0] + zp[1]) + (zp[2] + zp[3]));
;         Gc += fminf(z, 0.f) * (L2E / 16.f) - __builtin_amdgcn_logf(1.f + __builtin_amdgcn_exp2f(-fabsf(z) * L2E)) * (1.f / 16.f); Gv[i] = Gc; }
	v_pk_mul_f32 v[26:27], v[14:15], v[26:27]
	v_pk_mul_f32 v[34:35], v[18:19], v[34:35]
	v_pk_fma_f32 v[24:25], v[10:11], v[24:25], v[26:27]
	v_pk_fma_f32 v[26:27], v[12:13], v[32:33], v[34:35]
	v_pk_fma_f32 v[24:25], v[22:23], v[28:29], v[24:25]
	v_pk_fma_f32 v[26:27], v[8:9], v[36:37], v[26:27]
	v_pk_fma_f32 v[24:25], v[20:21], v[30:31], v[24:25]
	v_pk_fma_f32 v[26:27], v[16:17], v[38:39], v[26:27]
	s_nop 0
	v_pk_add_f32 v[24:25], v[24:25], v[26:27]
	s_nop 0
	v_add_f32_e32 v24, v24, v25
	v_add_f32_e32 v26, v48, v24
	v_mul_f32_e64 v24, |v26|, s34
	v_exp_f32_e32 v27, v24
	v_pk_mul_f32 v[24:25], v[196:197], s[14:15]
	v_min_f32_e32 v32, 0, v26
	v_sub_f32_e32 v24, v24, v25
	v_add_f32_e32 v197, v79, v24
	v_add_f32_e32 v24, 1.0, v27
	v_log_f32_e32 v33, v24
	ds_read_b128 v[24:27], v69 offset:960
	ds_read_b128 v[28:31], v69 offset:976
	v_pk_mul_f32 v[198:199], v[32:33], s[14:15]
	ds_read_b128 v[32:35], v69 offset:992
	ds_read_b128 v[36:39], v69 offset:1008
	s_waitcnt lgkmcnt(0)
	v_pk_mul_f32 v[26:27], v[14:15], v[26:27]
	v_pk_mul_f32 v[34:35], v[18:19], v[34:35]
	v_pk_fma_f32 v[24:25], v[10:11], v[24:25], v[26:27]
	v_pk_fma_f32 v[26:27], v[12:13], v[32:33], v[34:35]
	v_pk_fma_f32 v[24:25], v[22:23], v[28:29], v[24:25]
	v_pk_fma_f32 v[26:27], v[8:9], v[36:37], v[26:27]
	v_pk_fma_f32 v[24:25], v[20:21], v[30:31], v[24:25]
	v_pk_fma_f32 v[26:27], v[16:17], v[38:39], v[26:27]
	s_nop 0
	v_pk_add_f32 v[24:25], v[24:25], v[26:27]
	v_sub_f32_e32 v26, v198, v199
	v_add_f32_e32 v24, v24, v25
	v_add_f32_e32 v24, v48, v24
	v_mul_f32_e64 v25, |v24|, s34
	v_exp_f32_e32 v25, v25
	v_add_f32_e32 v200, v197, v26
	v_min_f32_e32 v198, 0, v24
	v_add_f32_e32 v32, 1.0, v25
	ds_read_b128 v[24:27], v69 offset:1024
	ds_read_b128 v[28:31], v69 offset:1040
	v_log_f32_e32 v199, v32
	ds_read_b128 v[32:35], v69 offset:1056
	ds_read_b128 v[36:39], v69 offset:1072
	s_waitcnt lgkmcnt(0)
	v_pk_mul_f32 v[26:27], v[14:15], v[26:27]
	v_pk_mul_f32 v[34:35], v[18:19], v[34:35]
	v_pk_fma_f32 v[24:25], v[10:11], v[24:25], v[26:27]
	v_pk_fma_f32 v[26:27], v[12:13], v[32:33], v[34:35]
	v_pk_fma_f32 v[24:25], v[22:23], v[28:29], v[24:25]
	v_pk_fma_f32 v[26:27], v[8:9], v[36:37], v[26:27]
	v_pk_fma_f32 v[24:25], v[20:21], v[30:31], v[24:25]
	v_pk_fma_f32 v[26:27], v[16:17], v[38:39], v[26:27]
	s_nop 0
	v_pk_add_f32 v[24:25], v[24:25], v[26:27]
	s_nop 0
	v_add_f32_e32 v24, v24, v25
	v_add_f32_e32 v26, v48, v24
	v_mul_f32_e64 v24, |v26|, s34
	v_exp_f32_e32 v27, v24
	v_pk_mul_f32 v[24:25], v[198:199], s[14:15]
	v_min_f32_e32 v32, 0, v26
	v_sub_f32_e32 v24, v24, v25
	v_add_f32_e32 v203, v200, v24
	v_add_f32_e32 v24, 1.0, v27
	v_log_f32_e32 v33, v24
	ds_read_b128 v[24:27], v69 offset:1088
	ds_read_b128 v[28:31], v69 offset:1104
	v_pk_mul_f32 v[198:199], v[32:33], s[14:15]
	ds_read_b128 v[32:35], v69 offset:1120
	ds_read_b128 v[36:39], v69 offset:1136
	s_waitcnt lgkmcnt(0)
	v_pk_mul_f32 v[26:27], v[14:15], v[26:27]
	v_pk_mul_f32 v[34:35], v[18:19], v[34:35]
	v_pk_fma_f32 v[24:25], v[10:11], v[24:25], v[26:27]
	v_pk_fma_f32 v[26:27], v[12:13], v[32:33], v[34:35]
	v_pk_fma_f32 v[24:25], v[22:23], v[28:29], v[24:25]
	v_pk_fma_f32 v[26:27], v[8:9], v[36:37], v[26:27]
	v_pk_fma_f32 v[24:25], v[20:21], v[30:31], v[24:25]
	v_pk_fma_f32 v[26:27], v[16:17], v[38:39], v[26:27]
	s_nop 0
	v_pk_add_f32 v[24:25], v[24:25], v[26:27]
	v_sub_f32_e32 v26, v198, v199
	v_add_f32_e32 v24, v24, v25
	v_add_f32_e32 v24, v48, v24
	v_mul_f32_e64 v25, |v24|, s34
	v_exp_f32_e32 v25, v25
	v_add_f32_e32 v196, v203, v26
	v_min_f32_e32 v198, 0, v24
	v_add_f32_e32 v32, 1.0, v25
	ds_read_b128 v[24:27], v69 offset:1152
	ds_read_b128 v[28:31], v69 offset:1168
	v_log_f32_e32 v199, v32
	ds_read_b128 v[32:35], v69 offset:1184
	ds_read_b128 v[36:39], v69 offset:1200
	s_waitcnt lgkmcnt(0)
	v_pk_mul_f32 v[26:27], v[14:15], v[26:27]
	v_pk_mul_f32 v[34:35], v[18:19], v[34:35]
	v_pk_fma_f32 v[24:25], v[10:11], v[24:25], v[26:27]
	v_pk_fma_f32 v[26:27], v[12:13], v[32:33], v[34:35]
	v_pk_fma_f32 v[24:25], v[22:23], v[28:29], v[24:25]
	v_pk_fma_f32 v[26:27], v[8:9], v[36:37], v[26:27]
	v_pk_fma_f32 v[24:25], v[20:21], v[30:31], v[24:25]
	v_pk_fma_f32 v[26:27], v[16:17], v[38:39], v[26:27]
	s_nop 0
	v_pk_add_f32 v[24:25], v[24:25], v[26:27]
	s_nop 0
	v_add_f32_e32 v24, v24, v25
	v_add_f32_e32 v26, v48, v24
	v_mul_f32_e64 v24, |v26|, s34
	v_exp_f32_e32 v27, v24
	v_pk_mul_f32 v[24:25], v[198:199], s[14:15]
	v_min_f32_e32 v32, 0, v26
	v_sub_f32_e32 v24, v24, v25
	v_add_f32_e32 v199, v196, v24
	v_add_f32_e32 v24, 1.0, v27
	v_log_f32_e32 v33, v24
	ds_read_b128 v[24:27], v69 offset:1216
	ds_read_b128 v[28:31], v69 offset:1232
	v_pk_mul_f32 v[204:205], v[32:33], s[14:15]
	ds_read_b128 v[32:35], v69 offset:1248
	ds_read_b128 v[36:39], v69 offset:1264
	s_waitcnt lgkmcnt(0)
	v_pk_mul_f32 v[26:27], v[14:15], v[26:27]
	v_pk_mul_f32 v[34:35], v[18:19], v[34:35]
	v_pk_fma_f32 v[24:25], v[10:11], v[24:25], v[26:27]
	v_pk_fma_f32 v[26:27], v[12:13], v[32:33], v[34:35]
	v_pk_fma_f32 v[24:25], v[22:23], v[28:29], v[24:25]
	v_pk_fma_f32 v[26:27], v[8:9], v[36:37], v[26:27]
	v_pk_fma_f32 v[24:25], v[20:21], v[30:31], v[24:25]
	v_pk_fma_f32 v[26:27], v[16:17], v[38:39], v[26:27]
	s_nop 0
	v_pk_add_f32 v[24:25], v[24:25], v[26:27]
	v_sub_f32_e32 v26, v204, v205
	v_add_f32_e32 v24, v24, v25
	v_add_f32_e32 v24, v48, v24
	v_mul_f32_e64 v25, |v24|, s34
	v_exp_f32_e32 v25, v25
	v_add_f32_e32 v202, v199, v26
	v_min_f32_e32 v204, 0, v24
	v_add_f32_e32 v32, 1.0, v25
	ds_read_b128 v[24:27], v69 offset:1280
	ds_read_b128 v[28:31], v69 offset:1296
	v_log_f32_e32 v205, v32
	ds_read_b128 v[32:35], v69 offset:1312
	ds_read_b128 v[36:39], v69 offset:1328
	s_waitcnt lgkmcnt(0)
; #define LAS __attribute__((address_space(3)))
; __device__ __forceinline__ void prep_item(const Args& a, LAS unsigned char* lds, int tid, int dir, int b, int ch) {
;     ...
;     for (int i = 0; i < 64; ++i) { float zp[4];
; #pragma unroll
;         for (int r4 = 0; r4 < 4; ++r4) { const f32x4 x = *(const LAS f32x4*)(alr + i * 16 + 4 * r4); zp[r4] = x[0] * w[4 * r4] + x[1] * w[4 * r4 + 1] + x[2] * w[4 * r4 + 2] + x[3] * w[4 * r4 + 3]; }
;         const float z = bia + ((zp[0] + zp[1]) + (zp[2] + zp[3]));
;         Gc += fminf(z, 0.f) * (L2E / 16.f) - __builtin_amdgcn_logf(1.f + __builtin_amdgcn_exp2f(-fabsf(z) * L2E)) * (1.f / 16.f); Gv[i] = Gc; }
	v_pk_mul_f32 v[26:27], v[14:15], v[26:27]
	v_pk_mul_f32 v[34:35], v[18:19], v[34:35]
	v_pk_fma_f32 v[24:25], v[10:11], v[24:25], v[26:27]
	v_pk_fma_f32 v[26:27], v[12:13], v[32:33], v[34:35]
	v_pk_fma_f32 v[24:25], v[22:23], v[28:29], v[24:25]
	v_pk_fma_f32 v[26:27], v[8:9], v[36:37], v[26:27]
	v_pk_fma_f32 v[24:25], v[20:21], v[30:31], v[24:25]
	v_pk_fma_f32 v[26:27], v[16:17], v[38:39], v[26:27]
	s_nop 0
	v_pk_add_f32 v[24:25], v[24:25], v[26:27]
	s_nop 0
	v_add_f32_e32 v24, v24, v25
	v_add_f32_e32 v26, v48, v24
	v_mul_f32_e64 v24, |v26|, s34
	v_exp_f32_e32 v27, v24
	v_pk_mul_f32 v[24:25], v[204:205], s[14:15]
	v_min_f32_e32 v32, 0, v26
	v_sub_f32_e32 v24, v24, v25
	v_add_f32_e32 v205, v202, v24
	v_add_f32_e32 v24, 1.0, v27
	v_log_f32_e32 v33, v24
	ds_read_b128 v[24:27], v69 offset:1344
	ds_read_b128 v[28:31], v69 offset:1360
	v_pk_mul_f32 v[206:207], v[32:33], s[14:15]
	ds_read_b128 v[32:35], v69 offset:1376
	ds_read_b128 v[36:39], v69 offset:1392
	s_waitcnt lgkmcnt(0)
	v_pk_mul_f32 v[26:27], v[14:15], v[26:27]
	v_pk_mul_f32 v[34:35], v[18:19], v[34:35]
	v_pk_fma_f32 v[24:25], v[10:11], v[24:25], v[26:27]
	v_pk_fma_f32 v[26:27], v[12:13], v[32:33], v[34:35]
	v_pk_fma_f32 v[24:25], v[22:23], v[28:29], v[24:25]
	v_pk_fma_f32 v[26:27], v[8:9], v[36:37], v[26:27]
	v_pk_fma_f32 v[24:25], v[20:21], v[30:31], v[24:25]
	v_pk_fma_f32 v[26:27], v[16:17], v[38:39], v[26:27]
	s_nop 0
	v_pk_add_f32 v[24:25], v[24:25], v[26:27]
	v_sub_f32_e32 v26, v206, v207
	v_add_f32_e32 v24, v24, v25
	v_add_f32_e32 v24, v48, v24
	v_mul_f32_e64 v25, |v24|, s34
	v_exp_f32_e32 v25, v25
	v_add_f32_e32 v207, v205, v26
	v_min_f32_e32 v208, 0, v24
	v_add_f32_e32 v32, 1.0, v25
	ds_read_b128 v[24:27], v69 offset:1408
	ds_read_b128 v[28:31], v69 offset:1424
	v_log_f32_e32 v209, v32
	ds_read_b128 v[32:35], v69 offset:1440
	ds_read_b128 v[36:39], v69 offset:1456
	s_waitcnt lgkmcnt(0)
	v_pk_mul_f32 v[26:27], v[14:15], v[26:27]
	v_pk_mul_f32 v[34:35], v[18:19], v[34:35]
	v_pk_fma_f32 v[24:25], v[10:11], v[24:25], v[26:27]
	v_pk_fma_f32 v[26:27], v[12:13], v[32:33], v[34:35]
	v_pk_fma_f32 v[24:25], v[22:23], v[28:29], v[24:25]
	v_pk_fma_f32 v[26:27], v[8:9], v[36:37], v[26:27]
	v_pk_fma_f32 v[24:25], v[20:21], v[30:31], v[24:25]
	v_pk_fma_f32 v[26:27], v[16:17], v[38:39], v[26:27]
	s_nop 0
	v_pk_add_f32 v[24:25], v[24:25], v[26:27]
	s_nop 0
	v_add_f32_e32 v24, v24, v25
	v_add_f32_e32 v26, v48, v24
	v_mul_f32_e64 v24, |v26|, s34
	v_exp_f32_e32 v27, v24
	v_pk_mul_f32 v[24:25], v[208:209], s[14:15]
	v_min_f32_e32 v32, 0, v26
	v_sub_f32_e32 v24, v24, v25
	v_add_f32_e32 v209, v207, v24
	v_add_f32_e32 v24, 1.0, v27
	v_log_f32_e32 v33, v24
	ds_read_b128 v[24:27], v69 offset:1472
	ds_read_b128 v[28:31], v69 offset:1488
	v_pk_mul_f32 v[210:211], v[32:33], s[14:15]
	ds_read_b128 v[32:35], v69 offset:1504
	ds_read_b128 v[36:39], v69 offset:1520
	s_waitcnt lgkmcnt(0)
	v_pk_mul_f32 v[26:27], v[14:15], v[26:27]
	v_pk_mul_f32 v[34:35], v[18:19], v[34:35]
	v_pk_fma_f32 v[24:25], v[10:11], v[24:25], v[26:27]
	v_pk_fma_f32 v[26:27], v[12:13], v[32:33], v[34:35]
	v_pk_fma_f32 v[24:25], v[22:23], v[28:29], v[24:25]
	v_pk_fma_f32 v[26:27], v[8:9], v[36:37], v[26:27]
	v_pk_fma_f32 v[24:25], v[20:21], v[30:31], v[24:25]
	v_pk_fma_f32 v[26:27], v[16:17], v[38:39], v[26:27]
	s_nop 0
	v_pk_add_f32 v[24:25], v[24:25], v[26:27]
	v_sub_f32_e32 v26, v210, v211
	v_add_f32_e32 v24, v24, v25
	v_add_f32_e32 v24, v48, v24
	v_mul_f32_e64 v25, |v24|, s34
	v_exp_f32_e32 v25, v25
	v_add_f32_e32 v211, v209, v26
	v_min_f32_e32 v212, 0, v24
	v_add_f32_e32 v32, 1.0, v25
	ds_read_b128 v[24:27], v69 offset:1536
	ds_read_b128 v[28:31], v69 offset:1552
	v_log_f32_e32 v213, v32
	ds_read_b128 v[32:35], v69 offset:1568
	ds_read_b128 v[36:39], v69 offset:1584
	s_waitcnt lgkmcnt(0)
	v_pk_mul_f32 v[26:27], v[14:15], v[26:27]
	v_pk_mul_f32 v[34:35], v[18:19], v[34:35]
	v_pk_fma_f32 v[24:25], v[10:11], v[24:25], v[26:27]
	v_pk_fma_f32 v[26:27], v[12:13], v[32:33], v[34:35]
	v_pk_fma_f32 v[24:25], v[22:23], v[28:29], v[24:25]
	v_pk_fma_f32 v[26:27], v[8:9], v[36:37], v[26:27]
	v_pk_fma_f32 v[24:25], v[20:21], v[30:31], v[24:25]
	v_pk_fma_f32 v[26:27], v[16:17], v[38:39], v[26:27]
	s_nop 0
	v_pk_add_f32 v[24:25], v[24:25], v[26:27]
	s_nop 0
	v_add_f32_e32 v24, v24, v25
	v_add_f32_e32 v26, v48, v24
	v_mul_f32_e64 v24, |v26|, s34
	v_exp_f32_e32 v27, v24
	v_pk_mul_f32 v[24:25], v[212:213], s[14:15]
	v_min_f32_e32 v32, 0, v26
	v_sub_f32_e32 v24, v24, v25
	v_add_f32_e32 v213, v211, v24
	v_add_f32_e32 v24, 1.0, v27
	v_log_f32_e32 v33, v24
	ds_read_b128 v[24:27], v69 offset:1600
	ds_read_b128 v[28:31], v69 offset:1616
	v_pk_mul_f32 v[214:215], v[32:33], s[14:15]
	ds_read_b128 v[32:35], v69 offset:1632
	ds_read_b128 v[36:39], v69 offset:1648
	s_waitcnt lgkmcnt(0)
	v_pk_mul_f32 v[26:27], v[14:15], v[26:27]
	v_pk_mul_f32 v[34:35], v[18:19], v[34:35]
	v_pk_fma_f32 v[24:25], v[10:11], v[24:25], v[26:27]
	v_pk_fma_f32 v[26:27], v[12:13], v[32:33], v[34:35]
	v_pk_fma_f32 v[24:25], v[22:23], v[28:29], v[24:25]
	v_pk_fma_f32 v[26:27], v[8:9], v[36:37], v[26:27]
	v_pk_fma_f32 v[24:25], v[20:21], v[30:31], v[24:25]
	v_pk_fma_f32 v[26:27], v[16:17], v[38:39], v[26:27]
	s_nop 0
	v_pk_add_f32 v[24:25], v[24:25], v[26:27]
	v_sub_f32_e32 v26, v214, v215
	v_add_f32_e32 v24, v24, v25
	v_add_f32_e32 v24, v48, v24
	v_mul_f32_e64 v25, |v24|, s34
	v_exp_f32_e32 v25, v25
	v_add_f32_e32 v47, v213, v26
	v_min_f32_e32 v214, 0, v24
	v_add_f32_e32 v32, 1.0, v25
	ds_read_b128 v[24:27], v69 offset:1664
	ds_read_b128 v[28:31], v69 offset:1680
	v_log_f32_e32 v215, v32
	ds_read_b128 v[32:35], v69 offset:1696
	ds_read_b128 v[36:39], v69 offset:1712
	s_waitcnt lgkmcnt(0)
; #define LAS __attribute__((address_space(3)))
; __device__ __forceinline__ void prep_item(const Args& a, LAS unsigned char* lds, int tid, int dir, int b, int ch) {
;     ...
;     for (int i = 0; i < 64; ++i) { float zp[4];
; #pragma unroll
;         for (int r4 = 0; r4 < 4; ++r4) { const f32x4 x = *(const LAS f32x4*)(alr + i * 16 + 4 * r4); zp[r4] = x[0] * w[4 * r4] + x[1] * w[4 * r4 + 1] + x[2] * w[4 * r4 + 2] + x[3] * w[4 * r4 + 3]; }
;         const float z = bia + ((zp[0] + zp[1]) + (zp[2] + zp[3]));
;         Gc += fminf(z, 0.f) * (L2E / 16.f) - __builtin_amdgcn_logf(1.f + __builtin_amdgcn_exp2f(-fabsf(z) * L2E)) * (1.f / 16.f); Gv[i] = Gc; }
	v_pk_mul_f32 v[26:27], v[14:15], v[26:27]
	v_pk_mul_f32 v[34:35], v[18:19], v[34:35]
	v_pk_fma_f32 v[24:25], v[10:11], v[24:25], v[26:27]
	v_pk_fma_f32 v[26:27], v[12:13], v[32:33], v[34:35]
	v_pk_fma_f32 v[24:25], v[22:23], v[28:29], v[24:25]
	v_pk_fma_f32 v[26:27], v[8:9], v[36:37], v[26:27]
	v_pk_fma_f32 v[24:25], v[20:21], v[30:31], v[24:25]
	v_pk_fma_f32 v[26:27], v[16:17], v[38:39], v[26:27]
	s_nop 0
	v_pk_add_f32 v[24:25], v[24:25], v[26:27]
	s_nop 0
	v_add_f32_e32 v24, v24, v25
	v_add_f32_e32 v26, v48, v24
	v_mul_f32_e64 v24, |v26|, s34
	v_exp_f32_e32 v27, v24
	v_pk_mul_f32 v[24:25], v[214:215], s[14:15]
	v_min_f32_e32 v32, 0, v26
	v_sub_f32_e32 v24, v24, v25
	v_add_f32_e32 v50, v47, v24
	v_add_f32_e32 v24, 1.0, v27
	v_log_f32_e32 v33, v24
	ds_read_b128 v[24:27], v69 offset:1728
	ds_read_b128 v[28:31], v69 offset:1744
	v_pk_mul_f32 v[214:215], v[32:33], s[14:15]
	ds_read_b128 v[32:35], v69 offset:1760
	ds_read_b128 v[36:39], v69 offset:1776
	s_waitcnt lgkmcnt(0)
	v_pk_mul_f32 v[26:27], v[14:15], v[26:27]
	v_pk_mul_f32 v[34:35], v[18:19], v[34:35]
	v_pk_fma_f32 v[24:25], v[10:11], v[24:25], v[26:27]
	v_pk_fma_f32 v[26:27], v[12:13], v[32:33], v[34:35]
	v_pk_fma_f32 v[24:25], v[22:23], v[28:29], v[24:25]
	v_pk_fma_f32 v[26:27], v[8:9], v[36:37], v[26:27]
	v_pk_fma_f32 v[24:25], v[20:21], v[30:31], v[24:25]
	v_pk_fma_f32 v[26:27], v[16:17], v[38:39], v[26:27]
	s_nop 0
	v_pk_add_f32 v[24:25], v[24:25], v[26:27]
	v_sub_f32_e32 v26, v214, v215
	v_add_f32_e32 v24, v24, v25
	v_add_f32_e32 v24, v48, v24
	v_mul_f32_e64 v25, |v24|, s34
	v_exp_f32_e32 v25, v25
	v_add_f32_e32 v52, v50, v26
	v_min_f32_e32 v214, 0, v24
	v_add_f32_e32 v32, 1.0, v25
	ds_read_b128 v[24:27], v69 offset:1792
	ds_read_b128 v[28:31], v69 offset:1808
	v_log_f32_e32 v215, v32
	ds_read_b128 v[32:35], v69 offset:1824
	ds_read_b128 v[36:39], v69 offset:1840
	s_waitcnt lgkmcnt(0)
	v_pk_mul_f32 v[26:27], v[14:15], v[26:27]
	v_pk_mul_f32 v[34:35], v[18:19], v[34:35]
	v_pk_fma_f32 v[24:25], v[10:11], v[24:25], v[26:27]
	v_pk_fma_f32 v[26:27], v[12:13], v[32:33], v[34:35]
	v_pk_fma_f32 v[24:25], v[22:23], v[28:29], v[24:25]
	v_pk_fma_f32 v[26:27], v[8:9], v[36:37], v[26:27]
	v_pk_fma_f32 v[24:25], v[20:21], v[30:31], v[24:25]
	v_pk_fma_f32 v[26:27], v[16:17], v[38:39], v[26:27]
	s_nop 0
	v_pk_add_f32 v[24:25], v[24:25], v[26:27]
	s_nop 0
	v_add_f32_e32 v24, v24, v25
	v_add_f32_e32 v26, v48, v24
	v_mul_f32_e64 v24, |v26|, s34
	v_exp_f32_e32 v27, v24
	v_pk_mul_f32 v[24:25], v[214:215], s[14:15]
	v_min_f32_e32 v32, 0, v26
	v_sub_f32_e32 v24, v24, v25
	v_add_f32_e32 v54, v52, v24
	v_add_f32_e32 v24, 1.0, v27
	v_log_f32_e32 v33, v24
	ds_read_b128 v[24:27], v69 offset:1856
	ds_read_b128 v[28:31], v69 offset:1872
	v_pk_mul_f32 v[214:215], v[32:33], s[14:15]
	ds_read_b128 v[32:35], v69 offset:1888
	ds_read_b128 v[36:39], v69 offset:1904
	s_waitcnt lgkmcnt(0)
	v_pk_mul_f32 v[26:27], v[14:15], v[26:27]
	v_pk_mul_f32 v[34:35], v[18:19], v[34:35]
	v_pk_fma_f32 v[24:25], v[10:11], v[24:25], v[26:27]
	v_pk_fma_f32 v[26:27], v[12:13], v[32:33], v[34:35]
	v_pk_fma_f32 v[24:25], v[22:23], v[28:29], v[24:25]
	v_pk_fma_f32 v[26:27], v[8:9], v[36:37], v[26:27]
	v_pk_fma_f32 v[24:25], v[20:21], v[30:31], v[24:25]
	v_pk_fma_f32 v[26:27], v[16:17], v[38:39], v[26:27]
	s_nop 0
	v_pk_add_f32 v[24:25], v[24:25], v[26:27]
	v_sub_f32_e32 v26, v214, v215
	v_add_f32_e32 v24, v24, v25
	v_add_f32_e32 v24, v48, v24
	v_mul_f32_e64 v25, |v24|, s34
	v_exp_f32_e32 v25, v25
	v_add_f32_e32 v56, v54, v26
	v_min_f32_e32 v214, 0, v24
	v_add_f32_e32 v32, 1.0, v25
	ds_read_b128 v[24:27], v69 offset:1920
	ds_read_b128 v[28:31], v69 offset:1936
	v_log_f32_e32 v215, v32
	ds_read_b128 v[32:35], v69 offset:1952
	ds_read_b128 v[36:39], v69 offset:1968
	s_waitcnt lgkmcnt(0)
	v_pk_mul_f32 v[26:27], v[14:15], v[26:27]
	v_pk_mul_f32 v[34:35], v[18:19], v[34:35]
	v_pk_fma_f32 v[24:25], v[10:11], v[24:25], v[26:27]
	v_pk_fma_f32 v[26:27], v[12:13], v[32:33], v[34:35]
	v_pk_fma_f32 v[24:25], v[22:23], v[28:29], v[24:25]
	v_pk_fma_f32 v[26:27], v[8:9], v[36:37], v[26:27]
	v_pk_fma_f32 v[24:25], v[20:21], v[30:31], v[24:25]
	v_pk_fma_f32 v[26:27], v[16:17], v[38:39], v[26:27]
	s_nop 0
	v_pk_add_f32 v[24:25], v[24:25], v[26:27]
	s_nop 0
	v_add_f32_e32 v24, v24, v25
	v_add_f32_e32 v26, v48, v24
	v_mul_f32_e64 v24, |v26|, s34
	v_exp_f32_e32 v27, v24
	v_pk_mul_f32 v[24:25], v[214:215], s[14:15]
	v_min_f32_e32 v32, 0, v26
	v_sub_f32_e32 v24, v24, v25
	v_add_f32_e32 v59, v56, v24
	v_add_f32_e32 v24, 1.0, v27
	v_log_f32_e32 v33, v24
	ds_read_b128 v[24:27], v69 offset:1984
	ds_read_b128 v[28:31], v69 offset:2000
	v_pk_mul_f32 v[214:215], v[32:33], s[14:15]
	ds_read_b128 v[32:35], v69 offset:2016
	ds_read_b128 v[36:39], v69 offset:2032
	s_waitcnt lgkmcnt(0)
	v_pk_mul_f32 v[26:27], v[14:15], v[26:27]
	v_pk_mul_f32 v[34:35], v[18:19], v[34:35]
	v_pk_fma_f32 v[24:25], v[10:11], v[24:25], v[26:27]
	v_pk_fma_f32 v[26:27], v[12:13], v[32:33], v[34:35]
	v_pk_fma_f32 v[24:25], v[22:23], v[28:29], v[24:25]
	v_pk_fma_f32 v[26:27], v[8:9], v[36:37], v[26:27]
	v_pk_fma_f32 v[24:25], v[20:21], v[30:31], v[24:25]
	v_pk_fma_f32 v[26:27], v[16:17], v[38:39], v[26:27]
	s_nop 0
	v_pk_add_f32 v[24:25], v[24:25], v[26:27]
	v_sub_f32_e32 v26, v214, v215
	v_add_f32_e32 v24, v24, v25
	v_add_f32_e32 v24, v48, v24
	v_mul_f32_e64 v25, |v24|, s34
	v_exp_f32_e32 v25, v25
	v_add_f32_e32 v62, v59, v26
	v_min_f32_e32 v214, 0, v24
	v_add_f32_e32 v32, 1.0, v25
	ds_read_b128 v[24:27], v69 offset:2048
	ds_read_b128 v[28:31], v69 offset:2064
	v_log_f32_e32 v215, v32
	ds_read_b128 v[32:35], v69 offset:2080
	ds_read_b128 v[36:39], v69 offset:2096
	s_waitcnt lgkmcnt(0)
; #define LAS __attribute__((address_space(3)))
; __device__ __forceinline__ void prep_item(const Args& a, LAS unsigned char* lds, int tid, int dir, int b, int ch) {
;     ...
;     for (int i = 0; i < 64; ++i) { float zp[4];
; #pragma unroll
;         for (int r4 = 0; r4 < 4; ++r4) { const f32x4 x = *(const LAS f32x4*)(alr + i * 16 + 4 * r4); zp[r4] = x[0] * w[4 * r4] + x[1] * w[4 * r4 + 1] + x[2] * w[4 * r4 + 2] + x[3] * w[4 * r4 + 3]; }
;         const float z = bia + ((zp[0] + zp[1]) + (zp[2] + zp[3]));
;         Gc += fminf(z, 0.f) * (L2E / 16.f) - __builtin_amdgcn_logf(1.f + __builtin_amdgcn_exp2f(-fabsf(z) * L2E)) * (1.f / 16.f); Gv[i] = Gc; }
	v_pk_mul_f32 v[26:27], v[14:15], v[26:27]
	v_pk_mul_f32 v[34:35], v[18:19], v[34:35]
	v_pk_fma_f32 v[24:25], v[10:11], v[24:25], v[26:27]
	v_pk_fma_f32 v[26:27], v[12:13], v[32:33], v[34:35]
	v_pk_fma_f32 v[24:25], v[22:23], v[28:29], v[24:25]
	v_pk_fma_f32 v[26:27], v[8:9], v[36:37], v[26:27]
	v_pk_fma_f32 v[24:25], v[20:21], v[30:31], v[24:25]
	v_pk_fma_f32 v[26:27], v[16:17], v[38:39], v[26:27]
	s_nop 0
	v_pk_add_f32 v[24:25], v[24:25], v[26:27]
	s_nop 0
	v_add_f32_e32 v24, v24, v25
	v_add_f32_e32 v26, v48, v24
	v_mul_f32_e64 v24, |v26|, s34
	v_exp_f32_e32 v27, v24
	v_pk_mul_f32 v[24:25], v[214:215], s[14:15]
	v_min_f32_e32 v32, 0, v26
	v_sub_f32_e32 v24, v24, v25
	v_add_f32_e32 v65, v62, v24
	v_add_f32_e32 v24, 1.0, v27
	v_log_f32_e32 v33, v24
	ds_read_b128 v[24:27], v69 offset:2112
	ds_read_b128 v[28:31], v69 offset:2128
	v_pk_mul_f32 v[214:215], v[32:33], s[14:15]
	ds_read_b128 v[32:35], v69 offset:2144
	ds_read_b128 v[36:39], v69 offset:2160
	s_waitcnt lgkmcnt(0)
	v_pk_mul_f32 v[26:27], v[14:15], v[26:27]
	v_pk_mul_f32 v[34:35], v[18:19], v[34:35]
	v_pk_fma_f32 v[24:25], v[10:11], v[24:25], v[26:27]
	v_pk_fma_f32 v[26:27], v[12:13], v[32:33], v[34:35]
	v_pk_fma_f32 v[24:25], v[22:23], v[28:29], v[24:25]
	v_pk_fma_f32 v[26:27], v[8:9], v[36:37], v[26:27]
	v_pk_fma_f32 v[24:25], v[20:21], v[30:31], v[24:25]
	v_pk_fma_f32 v[26:27], v[16:17], v[38:39], v[26:27]
	s_nop 0
	v_pk_add_f32 v[24:25], v[24:25], v[26:27]
	v_sub_f32_e32 v26, v214, v215
	v_add_f32_e32 v24, v24, v25
	v_add_f32_e32 v24, v48, v24
	v_mul_f32_e64 v25, |v24|, s34
	v_exp_f32_e32 v25, v25
	v_add_f32_e32 v45, v65, v26
	v_min_f32_e32 v214, 0, v24
	v_add_f32_e32 v32, 1.0, v25
	ds_read_b128 v[24:27], v69 offset:2176
	ds_read_b128 v[28:31], v69 offset:2192
	v_log_f32_e32 v215, v32
	ds_read_b128 v[32:35], v69 offset:2208
	ds_read_b128 v[36:39], v69 offset:2224
	s_waitcnt lgkmcnt(0)
	v_pk_mul_f32 v[26:27], v[14:15], v[26:27]
	v_pk_mul_f32 v[34:35], v[18:19], v[34:35]
	v_pk_fma_f32 v[24:25], v[10:11], v[24:25], v[26:27]
	v_pk_fma_f32 v[26:27], v[12:13], v[32:33], v[34:35]
	v_pk_fma_f32 v[24:25], v[22:23], v[28:29], v[24:25]
	v_pk_fma_f32 v[26:27], v[8:9], v[36:37], v[26:27]
	v_pk_fma_f32 v[24:25], v[20:21], v[30:31], v[24:25]
	v_pk_fma_f32 v[26:27], v[16:17], v[38:39], v[26:27]
	s_nop 0
	v_pk_add_f32 v[24:25], v[24:25], v[26:27]
	s_nop 0
	v_add_f32_e32 v24, v24, v25
	v_add_f32_e32 v26, v48, v24
	v_mul_f32_e64 v24, |v26|, s34
	v_exp_f32_e32 v27, v24
	v_pk_mul_f32 v[24:25], v[214:215], s[14:15]
	v_min_f32_e32 v32, 0, v26
	v_sub_f32_e32 v24, v24, v25
	v_add_f32_e32 v195, v45, v24
	v_add_f32_e32 v24, 1.0, v27
	v_log_f32_e32 v33, v24
	ds_read_b128 v[24:27], v69 offset:2240
	ds_read_b128 v[28:31], v69 offset:2256
	v_pk_mul_f32 v[214:215], v[32:33], s[14:15]
	ds_read_b128 v[32:35], v69 offset:2272
	ds_read_b128 v[36:39], v69 offset:2288
	s_waitcnt lgkmcnt(0)
	v_pk_mul_f32 v[26:27], v[14:15], v[26:27]
	v_pk_mul_f32 v[34:35], v[18:19], v[34:35]
	v_pk_fma_f32 v[24:25], v[10:11], v[24:25], v[26:27]
	v_pk_fma_f32 v[26:27], v[12:13], v[32:33], v[34:35]
	v_pk_fma_f32 v[24:25], v[22:23], v[28:29], v[24:25]
	v_pk_fma_f32 v[26:27], v[8:9], v[36:37], v[26:27]
	v_pk_fma_f32 v[24:25], v[20:21], v[30:31], v[24:25]
	v_pk_fma_f32 v[26:27], v[16:17], v[38:39], v[26:27]
	s_nop 0
	v_pk_add_f32 v[24:25], v[24:25], v[26:27]
	v_sub_f32_e32 v26, v214, v215
	v_add_f32_e32 v24, v24, v25
	v_add_f32_e32 v24, v48, v24
	v_mul_f32_e64 v25, |v24|, s34
	v_exp_f32_e32 v25, v25
	v_add_f32_e32 v198, v195, v26
	v_min_f32_e32 v214, 0, v24
	v_add_f32_e32 v32, 1.0, v25
	ds_read_b128 v[24:27], v69 offset:2304
	ds_read_b128 v[28:31], v69 offset:2320
	v_log_f32_e32 v215, v32
	ds_read_b128 v[32:35], v69 offset:2336
	ds_read_b128 v[36:39], v69 offset:2352
	s_waitcnt lgkmcnt(0)
	v_pk_mul_f32 v[26:27], v[14:15], v[26:27]
	v_pk_mul_f32 v[34:35], v[18:19], v[34:35]
	v_pk_fma_f32 v[24:25], v[10:11], v[24:25], v[26:27]
	v_pk_fma_f32 v[26:27], v[12:13], v[32:33], v[34:35]
	v_pk_fma_f32 v[24:25], v[22:23], v[28:29], v[24:25]
	v_pk_fma_f32 v[26:27], v[8:9], v[36:37], v[26:27]
	v_pk_fma_f32 v[24:25], v[20:21], v[30:31], v[24:25]
	v_pk_fma_f32 v[26:27], v[16:17], v[38:39], v[26:27]
	s_nop 0
	v_pk_add_f32 v[24:25], v[24:25], v[26:27]
	s_nop 0
	v_add_f32_e32 v24, v24, v25
	v_add_f32_e32 v26, v48, v24
	v_mul_f32_e64 v24, |v26|, s34
	v_exp_f32_e32 v27, v24
	v_pk_mul_f32 v[24:25], v[214:215], s[14:15]
	v_min_f32_e32 v32, 0, v26
	v_sub_f32_e32 v24, v24, v25
	v_add_f32_e32 v201, v198, v24
	v_add_f32_e32 v24, 1.0, v27
	v_log_f32_e32 v33, v24
	ds_read_b128 v[24:27], v69 offset:2368
	ds_read_b128 v[28:31], v69 offset:2384
	v_pk_mul_f32 v[214:215], v[32:33], s[14:15]
	ds_read_b128 v[32:35], v69 offset:2400
	ds_read_b128 v[36:39], v69 offset:2416
	s_waitcnt lgkmcnt(0)
	v_pk_mul_f32 v[26:27], v[14:15], v[26:27]
	v_pk_mul_f32 v[34:35], v[18:19], v[34:35]
	v_pk_fma_f32 v[24:25], v[10:11], v[24:25], v[26:27]
	v_pk_fma_f32 v[26:27], v[12:13], v[32:33], v[34:35]
	v_pk_fma_f32 v[24:25], v[22:23], v[28:29], v[24:25]
	v_pk_fma_f32 v[26:27], v[8:9], v[36:37], v[26:27]
	v_pk_fma_f32 v[24:25], v[20:21], v[30:31], v[24:25]
	v_pk_fma_f32 v[26:27], v[16:17], v[38:39], v[26:27]
	s_nop 0
	v_pk_add_f32 v[24:25], v[24:25], v[26:27]
	v_sub_f32_e32 v26, v214, v215
	v_add_f32_e32 v24, v24, v25
	v_add_f32_e32 v24, v48, v24
	v_mul_f32_e64 v25, |v24|, s34
	v_exp_f32_e32 v25, v25
	v_add_f32_e32 v204, v201, v26
	v_min_f32_e32 v214, 0, v24
	v_add_f32_e32 v32, 1.0, v25
	ds_read_b128 v[24:27], v69 offset:2432
	ds_read_b128 v[28:31], v69 offset:2448
	v_log_f32_e32 v215, v32
	ds_read_b128 v[32:35], v69 offset:2464
	ds_read_b128 v[36:39], v69 offset:2480
	s_waitcnt lgkmcnt(0)
; #define LAS __attribute__((address_space(3)))
; __device__ __forceinline__ void prep_item(const Args& a, LAS unsigned char* lds, int tid, int dir, int b, int ch) {
;     ...
;     for (int i = 0; i < 64; ++i) { float zp[4];
; #pragma unroll
;         for (int r4 = 0; r4 < 4; ++r4) { const f32x4 x = *(const LAS f32x4*)(alr + i * 16 + 4 * r4); zp[r4] = x[0] * w[4 * r4] + x[1] * w[4 * r4 + 1] + x[2] * w[4 * r4 + 2] + x[3] * w[4 * r4 + 3]; }
;         const float z = bia + ((zp[0] + zp[1]) + (zp[2] + zp[3]));
;         Gc += fminf(z, 0.f) * (L2E / 16.f) - __builtin_amdgcn_logf(1.f + __builtin_amdgcn_exp2f(-fabsf(z) * L2E)) * (1.f / 16.f); Gv[i] = Gc; }
	v_pk_mul_f32 v[26:27], v[14:15], v[26:27]
	v_pk_mul_f32 v[34:35], v[18:19], v[34:35]
	v_pk_fma_f32 v[24:25], v[10:11], v[24:25], v[26:27]
	v_pk_fma_f32 v[26:27], v[12:13], v[32:33], v[34:35]
	v_pk_fma_f32 v[24:25], v[22:23], v[28:29], v[24:25]
	v_pk_fma_f32 v[26:27], v[8:9], v[36:37], v[26:27]
	v_pk_fma_f32 v[24:25], v[20:21], v[30:31], v[24:25]
	v_pk_fma_f32 v[26:27], v[16:17], v[38:39], v[26:27]
	s_nop 0
	v_pk_add_f32 v[24:25], v[24:25], v[26:27]
	s_nop 0
	v_add_f32_e32 v24, v24, v25
	v_add_f32_e32 v26, v48, v24
	v_mul_f32_e64 v24, |v26|, s34
	v_exp_f32_e32 v27, v24
	v_pk_mul_f32 v[24:25], v[214:215], s[14:15]
	v_min_f32_e32 v32, 0, v26
	v_sub_f32_e32 v24, v24, v25
	v_add_f32_e32 v206, v204, v24
	v_add_f32_e32 v24, 1.0, v27
	v_log_f32_e32 v33, v24
	ds_read_b128 v[24:27], v69 offset:2496
	ds_read_b128 v[28:31], v69 offset:2512
	v_pk_mul_f32 v[214:215], v[32:33], s[14:15]
	ds_read_b128 v[32:35], v69 offset:2528
	ds_read_b128 v[36:39], v69 offset:2544
	s_waitcnt lgkmcnt(0)
	v_pk_mul_f32 v[26:27], v[14:15], v[26:27]
	v_pk_mul_f32 v[34:35], v[18:19], v[34:35]
	v_pk_fma_f32 v[24:25], v[10:11], v[24:25], v[26:27]
	v_pk_fma_f32 v[26:27], v[12:13], v[32:33], v[34:35]
	v_pk_fma_f32 v[24:25], v[22:23], v[28:29], v[24:25]
	v_pk_fma_f32 v[26:27], v[8:9], v[36:37], v[26:27]
	v_pk_fma_f32 v[24:25], v[20:21], v[30:31], v[24:25]
	v_pk_fma_f32 v[26:27], v[16:17], v[38:39], v[26:27]
	s_nop 0
	v_pk_add_f32 v[24:25], v[24:25], v[26:27]
	v_sub_f32_e32 v26, v214, v215
	v_add_f32_e32 v24, v24, v25
	v_add_f32_e32 v24, v48, v24
	v_mul_f32_e64 v25, |v24|, s34
	v_exp_f32_e32 v25, v25
	v_add_f32_e32 v208, v206, v26
	v_min_f32_e32 v214, 0, v24
	v_add_f32_e32 v32, 1.0, v25
	ds_read_b128 v[24:27], v69 offset:2560
	ds_read_b128 v[28:31], v69 offset:2576
	v_log_f32_e32 v215, v32
	ds_read_b128 v[32:35], v69 offset:2592
	ds_read_b128 v[36:39], v69 offset:2608
	s_waitcnt lgkmcnt(0)
	v_pk_mul_f32 v[26:27], v[14:15], v[26:27]
	v_pk_mul_f32 v[34:35], v[18:19], v[34:35]
	v_pk_fma_f32 v[24:25], v[10:11], v[24:25], v[26:27]
	v_pk_fma_f32 v[26:27], v[12:13], v[32:33], v[34:35]
	v_pk_fma_f32 v[24:25], v[22:23], v[28:29], v[24:25]
	v_pk_fma_f32 v[26:27], v[8:9], v[36:37], v[26:27]
	v_pk_fma_f32 v[24:25], v[20:21], v[30:31], v[24:25]
	v_pk_fma_f32 v[26:27], v[16:17], v[38:39], v[26:27]
	s_nop 0
	v_pk_add_f32 v[24:25], v[24:25], v[26:27]
	s_nop 0
	v_add_f32_e32 v24, v24, v25
	v_add_f32_e32 v26, v48, v24
	v_mul_f32_e64 v24, |v26|, s34
	v_exp_f32_e32 v27, v24
	v_pk_mul_f32 v[24:25], v[214:215], s[14:15]
	v_min_f32_e32 v32, 0, v26
	v_sub_f32_e32 v24, v24, v25
	v_add_f32_e32 v210, v208, v24
	v_add_f32_e32 v24, 1.0, v27
	v_log_f32_e32 v33, v24
	ds_read_b128 v[24:27], v69 offset:2624
	ds_read_b128 v[28:31], v69 offset:2640
	v_pk_mul_f32 v[214:215], v[32:33], s[14:15]
	ds_read_b128 v[32:35], v69 offset:2656
	ds_read_b128 v[36:39], v69 offset:2672
	s_waitcnt lgkmcnt(0)
	v_pk_mul_f32 v[26:27], v[14:15], v[26:27]
	v_pk_mul_f32 v[34:35], v[18:19], v[34:35]
	v_pk_fma_f32 v[24:25], v[10:11], v[24:25], v[26:27]
	v_pk_fma_f32 v[26:27], v[12:13], v[32:33], v[34:35]
	v_pk_fma_f32 v[24:25], v[22:23], v[28:29], v[24:25]
	v_pk_fma_f32 v[26:27], v[8:9], v[36:37], v[26:27]
	v_pk_fma_f32 v[24:25], v[20:21], v[30:31], v[24:25]
	v_pk_fma_f32 v[26:27], v[16:17], v[38:39], v[26:27]
	s_nop 0
	v_pk_add_f32 v[24:25], v[24:25], v[26:27]
	v_sub_f32_e32 v26, v214, v215
	v_add_f32_e32 v24, v24, v25
	v_add_f32_e32 v24, v48, v24
	v_mul_f32_e64 v25, |v24|, s34
	v_exp_f32_e32 v25, v25
	v_add_f32_e32 v212, v210, v26
	v_min_f32_e32 v214, 0, v24
	v_add_f32_e32 v32, 1.0, v25
	ds_read_b128 v[24:27], v69 offset:2688
	ds_read_b128 v[28:31], v69 offset:2704
	v_log_f32_e32 v215, v32
	ds_read_b128 v[32:35], v69 offset:2720
	ds_read_b128 v[36:39], v69 offset:2736
	s_waitcnt lgkmcnt(0)
	v_pk_mul_f32 v[26:27], v[14:15], v[26:27]
	v_pk_mul_f32 v[34:35], v[18:19], v[34:35]
	v_pk_fma_f32 v[24:25], v[10:11], v[24:25], v[26:27]
	v_pk_fma_f32 v[26:27], v[12:13], v[32:33], v[34:35]
	v_pk_fma_f32 v[24:25], v[22:23], v[28:29], v[24:25]
	v_pk_fma_f32 v[26:27], v[8:9], v[36:37], v[26:27]
	v_pk_fma_f32 v[24:25], v[20:21], v[30:31], v[24:25]
	v_pk_fma_f32 v[26:27], v[16:17], v[38:39], v[26:27]
	s_nop 0
	v_pk_add_f32 v[24:25], v[24:25], v[26:27]
	s_nop 0
	v_add_f32_e32 v24, v24, v25
	v_add_f32_e32 v26, v48, v24
	v_mul_f32_e64 v24, |v26|, s34
	v_exp_f32_e32 v27, v24
	v_pk_mul_f32 v[24:25], v[214:215], s[14:15]
	v_min_f32_e32 v32, 0, v26
	v_sub_f32_e32 v24, v24, v25
	v_add_f32_e32 v214, v212, v24
	v_add_f32_e32 v24, 1.0, v27
	v_log_f32_e32 v33, v24
	ds_read_b128 v[24:27], v69 offset:2752
	ds_read_b128 v[28:31], v69 offset:2768
	v_pk_mul_f32 v[216:217], v[32:33], s[14:15]
	ds_read_b128 v[32:35], v69 offset:2784
	ds_read_b128 v[36:39], v69 offset:2800
	s_waitcnt lgkmcnt(0)
	v_pk_mul_f32 v[26:27], v[14:15], v[26:27]
	v_pk_mul_f32 v[34:35], v[18:19], v[34:35]
	v_pk_fma_f32 v[24:25], v[10:11], v[24:25], v[26:27]
	v_pk_fma_f32 v[26:27], v[12:13], v[32:33], v[34:35]
	v_pk_fma_f32 v[24:25], v[22:23], v[28:29], v[24:25]
	v_pk_fma_f32 v[26:27], v[8:9], v[36:37], v[26:27]
	v_pk_fma_f32 v[24:25], v[20:21], v[30:31], v[24:25]
	v_pk_fma_f32 v[26:27], v[16:17], v[38:39], v[26:27]
	s_nop 0
	v_pk_add_f32 v[24:25], v[24:25], v[26:27]
	v_sub_f32_e32 v26, v216, v217
	v_add_f32_e32 v24, v24, v25
	v_add_f32_e32 v24, v48, v24
	v_mul_f32_e64 v25, |v24|, s34
	v_exp_f32_e32 v25, v25
	v_add_f32_e32 v215, v214, v26
	v_min_f32_e32 v216, 0, v24
	v_add_f32_e32 v32, 1.0, v25
	ds_read_b128 v[24:27], v69 offset:2816
	ds_read_b128 v[28:31], v69 offset:2832
	v_log_f32_e32 v217, v32
	ds_read_b128 v[32:35], v69 offset:2848
	ds_read_b128 v[36:39], v69 offset:2864
	s_waitcnt lgkmcnt(0)
; #define LAS __attribute__((address_space(3)))
; __device__ __forceinline__ void prep_item(const Args& a, LAS unsigned char* lds, int tid, int dir, int b, int ch) {
;     ...
;     for (int i = 0; i < 64; ++i) { float zp[4];
; #pragma unroll
;         for (int r4 = 0; r4 < 4; ++r4) { const f32x4 x = *(const LAS f32x4*)(alr + i * 16 + 4 * r4); zp[r4] = x[0] * w[4 * r4] + x[1] * w[4 * r4 + 1] + x[2] * w[4 * r4 + 2] + x[3] * w[4 * r4 + 3]; }
;         const float z = bia + ((zp[0] + zp[1]) + (zp[2] + zp[3]));
;         Gc += fminf(z, 0.f) * (L2E / 16.f) - __builtin_amdgcn_logf(1.f + __builtin_amdgcn_exp2f(-fabsf(z) * L2E)) * (1.f / 16.f); Gv[i] = Gc; }
	v_pk_mul_f32 v[26:27], v[14:15], v[26:27]
	v_pk_mul_f32 v[34:35], v[18:19], v[34:35]
	v_pk_fma_f32 v[24:25], v[10:11], v[24:25], v[26:27]
	v_pk_fma_f32 v[26:27], v[12:13], v[32:33], v[34:35]
	v_pk_fma_f32 v[24:25], v[22:23], v[28:29], v[24:25]
	v_pk_fma_f32 v[26:27], v[8:9], v[36:37], v[26:27]
	v_pk_fma_f32 v[24:25], v[20:21], v[30:31], v[24:25]
	v_pk_fma_f32 v[26:27], v[16:17], v[38:39], v[26:27]
	s_nop 0
	v_pk_add_f32 v[24:25], v[24:25], v[26:27]
	s_nop 0
	v_add_f32_e32 v24, v24, v25
	v_add_f32_e32 v26, v48, v24
	v_mul_f32_e64 v24, |v26|, s34
	v_exp_f32_e32 v27, v24
	v_pk_mul_f32 v[24:25], v[216:217], s[14:15]
	v_min_f32_e32 v32, 0, v26
	v_sub_f32_e32 v24, v24, v25
	v_add_f32_e32 v216, v215, v24
	v_add_f32_e32 v24, 1.0, v27
	v_log_f32_e32 v33, v24
	ds_read_b128 v[24:27], v69 offset:2880
	ds_read_b128 v[28:31], v69 offset:2896
	v_pk_mul_f32 v[218:219], v[32:33], s[14:15]
	ds_read_b128 v[32:35], v69 offset:2912
	ds_read_b128 v[36:39], v69 offset:2928
	s_waitcnt lgkmcnt(0)
	v_pk_mul_f32 v[26:27], v[14:15], v[26:27]
	v_pk_mul_f32 v[34:35], v[18:19], v[34:35]
	v_pk_fma_f32 v[24:25], v[10:11], v[24:25], v[26:27]
	v_pk_fma_f32 v[26:27], v[12:13], v[32:33], v[34:35]
	v_pk_fma_f32 v[24:25], v[22:23], v[28:29], v[24:25]
	v_pk_fma_f32 v[26:27], v[8:9], v[36:37], v[26:27]
	v_pk_fma_f32 v[24:25], v[20:21], v[30:31], v[24:25]
	v_pk_fma_f32 v[26:27], v[16:17], v[38:39], v[26:27]
	s_nop 0
	v_pk_add_f32 v[24:25], v[24:25], v[26:27]
	v_sub_f32_e32 v26, v218, v219
	v_add_f32_e32 v24, v24, v25
	v_add_f32_e32 v24, v48, v24
	v_mul_f32_e64 v25, |v24|, s34
	v_exp_f32_e32 v25, v25
	v_add_f32_e32 v217, v216, v26
	v_min_f32_e32 v218, 0, v24
	v_add_f32_e32 v32, 1.0, v25
	ds_read_b128 v[24:27], v69 offset:2944
	ds_read_b128 v[28:31], v69 offset:2960
	v_log_f32_e32 v219, v32
	ds_read_b128 v[32:35], v69 offset:2976
	ds_read_b128 v[36:39], v69 offset:2992
	s_waitcnt lgkmcnt(0)
	v_pk_mul_f32 v[26:27], v[14:15], v[26:27]
	v_pk_mul_f32 v[34:35], v[18:19], v[34:35]
	v_pk_fma_f32 v[24:25], v[10:11], v[24:25], v[26:27]
	v_pk_fma_f32 v[26:27], v[12:13], v[32:33], v[34:35]
	v_pk_fma_f32 v[24:25], v[22:23], v[28:29], v[24:25]
	v_pk_fma_f32 v[26:27], v[8:9], v[36:37], v[26:27]
	v_pk_fma_f32 v[24:25], v[20:21], v[30:31], v[24:25]
	v_pk_fma_f32 v[26:27], v[16:17], v[38:39], v[26:27]
	s_nop 0
	v_pk_add_f32 v[24:25], v[24:25], v[26:27]
	s_nop 0
	v_add_f32_e32 v24, v24, v25
	v_add_f32_e32 v220, v48, v24
	v_mul_f32_e64 v24, |v220|, s34
	v_exp_f32_e32 v26, v24
	v_pk_mul_f32 v[24:25], v[218:219], s[14:15]
	v_min_f32_e32 v220, 0, v220
	v_sub_f32_e32 v24, v24, v25
	v_add_f32_e32 v218, v217, v24
	v_add_f32_e32 v32, 1.0, v26
	ds_read_b128 v[24:27], v69 offset:3008
	ds_read_b128 v[28:31], v69 offset:3024
	v_log_f32_e32 v221, v32
	ds_read_b128 v[32:35], v69 offset:3040
	ds_read_b128 v[36:39], v69 offset:3056
	s_waitcnt lgkmcnt(0)
	v_pk_mul_f32 v[26:27], v[14:15], v[26:27]
	v_pk_mul_f32 v[34:35], v[18:19], v[34:35]
	v_pk_fma_f32 v[24:25], v[10:11], v[24:25], v[26:27]
	v_pk_fma_f32 v[26:27], v[12:13], v[32:33], v[34:35]
	v_pk_fma_f32 v[24:25], v[22:23], v[28:29], v[24:25]
	v_pk_fma_f32 v[26:27], v[8:9], v[36:37], v[26:27]
	v_pk_fma_f32 v[24:25], v[20:21], v[30:31], v[24:25]
	v_pk_fma_f32 v[26:27], v[16:17], v[38:39], v[26:27]
	s_nop 0
	ds_read_b128 v[32:35], v69 offset:3088
	v_pk_add_f32 v[24:25], v[24:25], v[26:27]
	ds_read_b128 v[36:39], v69 offset:3104
	v_add_f32_e32 v24, v24, v25
	v_add_f32_e32 v26, v48, v24
	v_mul_f32_e64 v24, |v26|, s34
	v_exp_f32_e32 v27, v24
	v_pk_mul_f32 v[24:25], v[220:221], s[14:15]
	v_mov_b32_e32 v30, v22
	v_sub_f32_e32 v24, v24, v25
	v_add_f32_e32 v25, 1.0, v27
	v_log_f32_e32 v25, v25
	v_add_f32_e32 v219, v218, v24
	v_min_f32_e32 v24, 0, v26
	ds_read_b128 v[26:29], v69 offset:3072
	v_pk_mul_f32 v[224:225], v[24:25], s[14:15]
	v_mov_b32_e32 v24, v10
	v_mov_b32_e32 v25, v14
	v_mov_b32_e32 v31, v20
	ds_read_b128 v[220:223], v69 offset:3120
	s_waitcnt lgkmcnt(1)
	v_pk_mul_f32 v[228:229], v[24:25], v[26:27]
	v_pk_mul_f32 v[230:231], v[30:31], v[28:29]
	v_mov_b32_e32 v26, v12
	v_mov_b32_e32 v27, v18
	v_mov_b32_e32 v28, v8
	v_mov_b32_e32 v29, v16
	v_pk_mul_f32 v[232:233], v[26:27], v[32:33]
	v_pk_mul_f32 v[234:235], v[28:29], v[34:35]
	v_mov_b32_e32 v32, v11
	v_mov_b32_e32 v33, v15
	v_mov_b32_e32 v34, v23
	v_mov_b32_e32 v35, v21
	v_pk_mul_f32 v[236:237], v[32:33], v[36:37]
	v_pk_mul_f32 v[238:239], v[34:35], v[38:39]
	v_mov_b32_e32 v38, v13
	v_mov_b32_e32 v39, v19
	v_mov_b32_e32 v36, v9
	v_mov_b32_e32 v37, v17
	v_mov_b32_e32 v240, v231
	v_mov_b32_e32 v241, v239
	v_mov_b32_e32 v231, v238
	v_mov_b32_e32 v238, v228
	v_mov_b32_e32 v239, v236
	v_mov_b32_e32 v236, v229
	s_waitcnt lgkmcnt(0)
	v_pk_mul_f32 v[220:221], v[38:39], v[220:221]
	v_pk_mul_f32 v[222:223], v[36:37], v[222:223]
	v_pk_add_f32 v[228:229], v[238:239], v[236:237]
	s_nop 0
	v_pk_add_f32 v[228:229], v[230:231], v[228:229]
	v_mov_b32_e32 v230, v235
	v_mov_b32_e32 v231, v223
	v_mov_b32_e32 v235, v222
	v_mov_b32_e32 v222, v232
	v_mov_b32_e32 v223, v220
	v_mov_b32_e32 v220, v233
	v_pk_add_f32 v[220:221], v[222:223], v[220:221]
	v_pk_add_f32 v[228:229], v[240:241], v[228:229]
	v_pk_add_f32 v[220:221], v[234:235], v[220:221]
	ds_read_b128 v[232:235], v69 offset:3168
	v_pk_add_f32 v[220:221], v[230:231], v[220:221]
	s_nop 0
	v_pk_add_f32 v[220:221], v[228:229], v[220:221]
	s_nop 0
	v_add_f32_e32 v220, v220, v221
	v_add_f32_e32 v221, v48, v220
	v_mul_f32_e64 v220, |v221|, s34
	v_exp_f32_e32 v228, v220
	v_sub_f32_e32 v220, v224, v225
	ds_read_b128 v[222:225], v69 offset:3136
	v_min_f32_e32 v236, 0, v221
	v_add_f32_e32 v228, 1.0, v228
	v_log_f32_e32 v237, v228
	ds_read_b128 v[228:231], v69 offset:3152
	s_waitcnt lgkmcnt(1)
; #define LAS __attribute__((address_space(3)))
; __device__ __forceinline__ void prep_item(const Args& a, LAS unsigned char* lds, int tid, int dir, int b, int ch) {
;     ...
;     for (int i = 0; i < 64; ++i) { float zp[4];
; #pragma unroll
;         for (int r4 = 0; r4 < 4; ++r4) { const f32x4 x = *(const LAS f32x4*)(alr + i * 16 + 4 * r4); zp[r4] = x[0] * w[4 * r4] + x[1] * w[4 * r4 + 1] + x[2] * w[4 * r4 + 2] + x[3] * w[4 * r4 + 3]; }
;         const float z = bia + ((zp[0] + zp[1]) + (zp[2] + zp[3]));
;         Gc += fminf(z, 0.f) * (L2E / 16.f) - __builtin_amdgcn_logf(1.f + __builtin_amdgcn_exp2f(-fabsf(z) * L2E)) * (1.f / 16.f); Gv[i] = Gc; }
	v_pk_mul_f32 v[238:239], v[24:25], v[222:223]
	v_pk_mul_f32 v[240:241], v[30:31], v[224:225]
	ds_read_b128 v[222:225], v69 offset:3184
	v_pk_mul_f32 v[232:233], v[32:33], v[232:233]
	v_pk_mul_f32 v[234:235], v[34:35], v[234:235]
	s_waitcnt lgkmcnt(1)
	v_pk_mul_f32 v[228:229], v[26:27], v[228:229]
	v_pk_mul_f32 v[230:231], v[28:29], v[230:231]
	s_waitcnt lgkmcnt(0)
	v_pk_mul_f32 v[222:223], v[38:39], v[222:223]
	v_pk_mul_f32 v[224:225], v[36:37], v[224:225]
	v_mov_b32_e32 v242, v241
	v_mov_b32_e32 v243, v235
	v_mov_b32_e32 v241, v234
	v_mov_b32_e32 v234, v238
	v_mov_b32_e32 v235, v232
	v_mov_b32_e32 v232, v239
	v_pk_add_f32 v[232:233], v[234:235], v[232:233]
	v_mov_b32_e32 v234, v231
	v_mov_b32_e32 v235, v225
	v_mov_b32_e32 v231, v224
	v_mov_b32_e32 v224, v228
	v_mov_b32_e32 v225, v222
	v_mov_b32_e32 v222, v229
	v_pk_add_f32 v[222:223], v[224:225], v[222:223]
	v_pk_add_f32 v[232:233], v[240:241], v[232:233]
	v_pk_add_f32 v[222:223], v[230:231], v[222:223]
	v_pk_add_f32 v[232:233], v[242:243], v[232:233]
	v_pk_add_f32 v[222:223], v[234:235], v[222:223]
	v_add_f32_e32 v220, v219, v220
	v_pk_add_f32 v[222:223], v[232:233], v[222:223]
	ds_read_b128 v[232:235], v69 offset:3232
	v_add_f32_e32 v222, v222, v223
	v_add_f32_e32 v228, v48, v222
	v_mul_f32_e64 v222, |v228|, s34
	v_exp_f32_e32 v224, v222
	v_pk_mul_f32 v[222:223], v[236:237], s[14:15]
	v_min_f32_e32 v228, 0, v228
	v_sub_f32_e32 v221, v222, v223
	v_add_f32_e32 v222, 1.0, v224
	v_log_f32_e32 v229, v222
	ds_read_b128 v[222:225], v69 offset:3200
	v_add_f32_e32 v221, v220, v221
	v_pk_mul_f32 v[236:237], v[228:229], s[14:15]
	ds_read_b128 v[228:231], v69 offset:3216
	s_waitcnt lgkmcnt(1)
	v_pk_mul_f32 v[238:239], v[24:25], v[222:223]
	v_pk_mul_f32 v[240:241], v[30:31], v[224:225]
	ds_read_b128 v[222:225], v69 offset:3248
	v_pk_mul_f32 v[232:233], v[32:33], v[232:233]
	v_pk_mul_f32 v[234:235], v[34:35], v[234:235]
	s_waitcnt lgkmcnt(1)
	v_pk_mul_f32 v[228:229], v[26:27], v[228:229]
	v_pk_mul_f32 v[230:231], v[28:29], v[230:231]
	s_waitcnt lgkmcnt(0)
	v_pk_mul_f32 v[222:223], v[38:39], v[222:223]
	v_pk_mul_f32 v[224:225], v[36:37], v[224:225]
	v_mov_b32_e32 v242, v241
	v_mov_b32_e32 v243, v235
	v_mov_b32_e32 v241, v234
	v_mov_b32_e32 v234, v238
	v_mov_b32_e32 v235, v232
	v_mov_b32_e32 v232, v239
	v_pk_add_f32 v[232:233], v[234:235], v[232:233]
	v_mov_b32_e32 v234, v231
	v_mov_b32_e32 v235, v225
	v_mov_b32_e32 v231, v224
	v_mov_b32_e32 v224, v228
	v_mov_b32_e32 v225, v222
	v_mov_b32_e32 v222, v229
	v_pk_add_f32 v[222:223], v[224:225], v[222:223]
	v_pk_add_f32 v[232:233], v[240:241], v[232:233]
	v_pk_add_f32 v[222:223], v[230:231], v[222:223]
	v_pk_add_f32 v[232:233], v[242:243], v[232:233]
	v_pk_add_f32 v[222:223], v[234:235], v[222:223]
	ds_read_b128 v[228:231], v69 offset:3264
	v_pk_add_f32 v[222:223], v[232:233], v[222:223]
	ds_read_b128 v[232:235], v69 offset:3280
	v_add_f32_e32 v222, v222, v223
	v_add_f32_e32 v223, v48, v222
	v_mul_f32_e64 v222, |v223|, s34
	v_exp_f32_e32 v224, v222
	v_sub_f32_e32 v222, v236, v237
	ds_read_b128 v[236:239], v69 offset:3296
	s_waitcnt lgkmcnt(2)
	v_pk_mul_f32 v[240:241], v[24:25], v[228:229]
	v_pk_mul_f32 v[242:243], v[30:31], v[230:231]
	ds_read_b128 v[228:231], v69 offset:3312
	s_waitcnt lgkmcnt(2)
	v_pk_mul_f32 v[232:233], v[26:27], v[232:233]
	s_waitcnt lgkmcnt(1)
	v_pk_mul_f32 v[236:237], v[32:33], v[236:237]
	v_pk_mul_f32 v[238:239], v[34:35], v[238:239]
	v_pk_mul_f32 v[234:235], v[28:29], v[234:235]
	s_waitcnt lgkmcnt(0)
	v_pk_mul_f32 v[228:229], v[38:39], v[228:229]
	v_pk_mul_f32 v[230:231], v[36:37], v[230:231]
	v_mov_b32_e32 v244, v243
	v_mov_b32_e32 v245, v239
	v_mov_b32_e32 v243, v238
	v_mov_b32_e32 v238, v240
	v_mov_b32_e32 v239, v236
	v_mov_b32_e32 v236, v241
	v_pk_add_f32 v[236:237], v[238:239], v[236:237]
	v_mov_b32_e32 v238, v235
	v_mov_b32_e32 v239, v231
	v_mov_b32_e32 v235, v230
	v_mov_b32_e32 v230, v232
	v_mov_b32_e32 v231, v228
	v_mov_b32_e32 v228, v233
	v_pk_add_f32 v[228:229], v[230:231], v[228:229]
	v_pk_add_f32 v[236:237], v[242:243], v[236:237]
	v_pk_add_f32 v[228:229], v[234:235], v[228:229]
	v_pk_add_f32 v[236:237], v[244:245], v[236:237]
	v_pk_add_f32 v[228:229], v[238:239], v[228:229]
	v_add_f32_e32 v224, 1.0, v224
	v_pk_add_f32 v[228:229], v[236:237], v[228:229]
	v_log_f32_e32 v225, v224
	v_add_f32_e32 v224, v228, v229
	v_add_f32_e32 v232, v48, v224
	v_mul_f32_e64 v224, |v232|, s34
	v_exp_f32_e32 v228, v224
	v_min_f32_e32 v224, 0, v223
	v_pk_mul_f32 v[224:225], v[224:225], s[14:15]
	ds_read_b128 v[236:239], v69 offset:3360
	v_sub_f32_e32 v223, v224, v225
	v_add_f32_e32 v224, 1.0, v228
	v_log_f32_e32 v225, v224
	ds_read_b128 v[228:231], v69 offset:3328
	v_min_f32_e32 v224, 0, v232
	ds_read_b128 v[232:235], v69 offset:3344
	v_pk_mul_f32 v[224:225], v[224:225], s[14:15]
	v_add_f32_e32 v222, v221, v222
	v_sub_f32_e32 v244, v224, v225
	s_waitcnt lgkmcnt(1)
	v_pk_mul_f32 v[224:225], v[24:25], v[228:229]
	v_pk_mul_f32 v[240:241], v[30:31], v[230:231]
	ds_read_b128 v[228:231], v69 offset:3376
	v_pk_mul_f32 v[236:237], v[32:33], v[236:237]
	v_pk_mul_f32 v[238:239], v[34:35], v[238:239]
	s_waitcnt lgkmcnt(1)
	v_pk_mul_f32 v[232:233], v[26:27], v[232:233]
	v_pk_mul_f32 v[234:235], v[28:29], v[234:235]
	s_waitcnt lgkmcnt(0)
; #define LAS __attribute__((address_space(3)))
; __device__ __forceinline__ void prep_item(const Args& a, LAS unsigned char* lds, int tid, int dir, int b, int ch) {
;     ...
;     float Gv[64]; float Gc = 0.f;
; #pragma unroll
;     for (int i = 0; i < 64; ++i) { float zp[4];
; #pragma unroll
;         for (int r4 = 0; r4 < 4; ++r4) { const f32x4 x = *(const LAS f32x4*)(alr + i * 16 + 4 * r4); zp[r4] = x[0] * w[4 * r4] + x[1] * w[4 * r4 + 1] + x[2] * w[4 * r4 + 2] + x[3] * w[4 * r4 + 3]; }
;         const float z = bia + ((zp[0] + zp[1]) + (zp[2] + zp[3]));
;         Gc += fminf(z, 0.f) * (L2E / 16.f) - __builtin_amdgcn_logf(1.f + __builtin_amdgcn_exp2f(-fabsf(z) * L2E)) * (1.f / 16.f); Gv[i] = Gc; }
	v_pk_mul_f32 v[228:229], v[38:39], v[228:229]
	v_pk_mul_f32 v[230:231], v[36:37], v[230:231]
	v_mov_b32_e32 v242, v241
	v_mov_b32_e32 v243, v239
	v_mov_b32_e32 v241, v238
	v_mov_b32_e32 v238, v224
	v_mov_b32_e32 v239, v236
	v_mov_b32_e32 v236, v225
	v_pk_add_f32 v[224:225], v[238:239], v[236:237]
	v_mov_b32_e32 v236, v235
	v_mov_b32_e32 v237, v231
	v_mov_b32_e32 v235, v230
	v_mov_b32_e32 v230, v232
	v_mov_b32_e32 v231, v228
	v_mov_b32_e32 v228, v233
	v_pk_add_f32 v[228:229], v[230:231], v[228:229]
	v_pk_add_f32 v[224:225], v[240:241], v[224:225]
	v_pk_add_f32 v[228:229], v[234:235], v[228:229]
	v_pk_add_f32 v[224:225], v[242:243], v[224:225]
	v_pk_add_f32 v[228:229], v[236:237], v[228:229]
	ds_read_b128 v[236:239], v69 offset:3424
	v_pk_add_f32 v[224:225], v[224:225], v[228:229]
	ds_read_b128 v[228:231], v69 offset:3392
	v_add_f32_e32 v224, v224, v225
	v_add_f32_e32 v225, v48, v224
	v_mul_f32_e64 v224, |v225|, s34
	v_exp_f32_e32 v232, v224
	v_min_f32_e32 v240, 0, v225
	v_add_f32_e32 v223, v222, v223
	v_add_f32_e32 v224, v223, v244
	v_add_f32_e32 v225, 1.0, v232
	ds_read_b128 v[232:235], v69 offset:3408
	s_waitcnt lgkmcnt(1)
	v_pk_mul_f32 v[24:25], v[24:25], v[228:229]
	v_pk_mul_f32 v[30:31], v[30:31], v[230:231]
	ds_read_b128 v[228:231], v69 offset:3440
	v_pk_mul_f32 v[32:33], v[32:33], v[236:237]
	v_pk_mul_f32 v[34:35], v[34:35], v[238:239]
	s_waitcnt lgkmcnt(1)
	v_pk_mul_f32 v[26:27], v[26:27], v[232:233]
	v_pk_mul_f32 v[28:29], v[28:29], v[234:235]
	s_waitcnt lgkmcnt(0)
	v_pk_mul_f32 v[38:39], v[38:39], v[228:229]
	v_mov_b32_e32 v228, v31
	v_mov_b32_e32 v229, v35
	v_mov_b32_e32 v31, v34
	v_mov_b32_e32 v34, v24
	v_mov_b32_e32 v35, v32
	v_mov_b32_e32 v32, v25
	v_pk_mul_f32 v[36:37], v[36:37], v[230:231]
	v_pk_add_f32 v[24:25], v[34:35], v[32:33]
	v_mov_b32_e32 v32, v26
	v_mov_b32_e32 v33, v38
	v_mov_b32_e32 v38, v27
	v_pk_add_f32 v[24:25], v[30:31], v[24:25]
	v_mov_b32_e32 v30, v29
	v_mov_b32_e32 v29, v36
	v_pk_add_f32 v[26:27], v[32:33], v[38:39]
	v_mov_b32_e32 v31, v37
	v_pk_add_f32 v[26:27], v[28:29], v[26:27]
	v_pk_add_f32 v[24:25], v[228:229], v[24:25]
	v_pk_add_f32 v[26:27], v[30:31], v[26:27]
	v_log_f32_e32 v241, v225
	v_pk_add_f32 v[24:25], v[24:25], v[26:27]
	s_nop 0
	v_add_f32_e32 v24, v24, v25
	v_add_f32_e32 v26, v48, v24
	v_mul_f32_e64 v24, |v26|, s34
	v_exp_f32_e32 v27, v24
	v_pk_mul_f32 v[24:25], v[240:241], s[14:15]
	v_min_f32_e32 v34, 0, v26
	v_sub_f32_e32 v24, v24, v25
	v_add_f32_e32 v25, 1.0, v27
	v_log_f32_e32 v35, v25
	ds_read_b128 v[26:29], v69 offset:3456
	ds_read_b128 v[30:33], v69 offset:3488
	v_add_f32_e32 v24, v224, v24
	v_pk_mul_f32 v[38:39], v[34:35], s[14:15]
	ds_read_b128 v[34:37], v69 offset:3472
	ds_read_b128 v[228:231], v69 offset:3504
	s_waitcnt lgkmcnt(2)
	v_mov_b32_e32 v233, v30
	v_mov_b32_e32 v30, v27
	v_mov_b32_e32 v232, v26
	v_pk_mul_f32 v[26:27], v[14:15], v[30:31]
	v_mov_b32_e32 v30, v28
	v_pk_fma_f32 v[26:27], v[10:11], v[232:233], v[26:27]
	v_mov_b32_e32 v31, v32
	v_mov_b32_e32 v32, v29
	s_waitcnt lgkmcnt(0)
	v_mov_b32_e32 v29, v228
	v_mov_b32_e32 v228, v35
	v_pk_fma_f32 v[26:27], v[22:23], v[30:31], v[26:27]
	v_mov_b32_e32 v28, v34
	v_pk_mul_f32 v[30:31], v[18:19], v[228:229]
	v_pk_fma_f32 v[26:27], v[20:21], v[32:33], v[26:27]
	v_pk_fma_f32 v[28:29], v[12:13], v[28:29], v[30:31]
	v_mov_b32_e32 v30, v36
	v_mov_b32_e32 v31, v230
	v_pk_fma_f32 v[28:29], v[8:9], v[30:31], v[28:29]
	v_mov_b32_e32 v230, v37
	v_pk_fma_f32 v[28:29], v[16:17], v[230:231], v[28:29]
	s_nop 0
	v_pk_add_f32 v[26:27], v[26:27], v[28:29]
	s_nop 0
	v_add_f32_e32 v25, v26, v27
	v_add_f32_e32 v26, v48, v25
	v_mul_f32_e64 v25, |v26|, s34
	v_exp_f32_e32 v27, v25
	v_sub_f32_e32 v25, v38, v39
	v_min_f32_e32 v38, 0, v26
	v_add_f32_e32 v25, v24, v25
	v_add_f32_e32 v34, 1.0, v27
	ds_read_b128 v[26:29], v69 offset:3520
	ds_read_b128 v[30:33], v69 offset:3552
	v_log_f32_e32 v39, v34
	ds_read_b128 v[34:37], v69 offset:3536
	ds_read_b128 v[228:231], v69 offset:3568
	s_waitcnt lgkmcnt(3)
	v_mov_b32_e32 v232, v26
	s_waitcnt lgkmcnt(2)
	v_mov_b32_e32 v233, v30
	v_mov_b32_e32 v30, v27
	v_pk_mul_f32 v[26:27], v[14:15], v[30:31]
	v_mov_b32_e32 v30, v28
	v_pk_fma_f32 v[26:27], v[10:11], v[232:233], v[26:27]
	v_mov_b32_e32 v31, v32
	v_mov_b32_e32 v32, v29
	s_waitcnt lgkmcnt(0)
	v_mov_b32_e32 v29, v228
	v_mov_b32_e32 v228, v35
	v_pk_fma_f32 v[26:27], v[22:23], v[30:31], v[26:27]
	v_mov_b32_e32 v28, v34
	v_pk_mul_f32 v[30:31], v[18:19], v[228:229]
	v_pk_fma_f32 v[26:27], v[20:21], v[32:33], v[26:27]
	v_pk_fma_f32 v[28:29], v[12:13], v[28:29], v[30:31]
	v_mov_b32_e32 v30, v36
	v_mov_b32_e32 v31, v230
	v_pk_fma_f32 v[28:29], v[8:9], v[30:31], v[28:29]
	v_mov_b32_e32 v230, v37
	v_pk_fma_f32 v[28:29], v[16:17], v[230:231], v[28:29]
	s_nop 0
	v_pk_add_f32 v[26:27], v[26:27], v[28:29]
	s_nop 0
	v_add_f32_e32 v26, v26, v27
	v_add_f32_e32 v28, v48, v26
	v_mul_f32_e64 v26, |v28|, s34
	v_exp_f32_e32 v29, v26
	v_pk_mul_f32 v[26:27], v[38:39], s[14:15]
	v_min_f32_e32 v36, 0, v28
	v_sub_f32_e32 v26, v26, v27
	v_add_f32_e32 v27, 1.0, v29
	v_log_f32_e32 v37, v27
	ds_read_b128 v[28:31], v69 offset:3584
	ds_read_b128 v[32:35], v69 offset:3616
	v_add_f32_e32 v26, v25, v26
	v_pk_mul_f32 v[232:233], v[36:37], s[14:15]
	ds_read_b128 v[36:39], v69 offset:3600
	ds_read_b128 v[228:231], v69 offset:3632
	s_waitcnt lgkmcnt(2)
	v_mov_b32_e32 v235, v32
	v_mov_b32_e32 v32, v29
	v_mov_b32_e32 v234, v28
	v_pk_mul_f32 v[28:29], v[14:15], v[32:33]
	v_mov_b32_e32 v32, v30
	v_pk_fma_f32 v[28:29], v[10:11], v[234:235], v[28:29]
	v_mov_b32_e32 v33, v34
	v_mov_b32_e32 v34, v31
	s_waitcnt lgkmcnt(0)
; #define LAS __attribute__((address_space(3)))
; __device__ __forceinline__ void prep_item(const Args& a, LAS unsigned char* lds, int tid, int dir, int b, int ch) {
;     ...
;     float Gv[64]; float Gc = 0.f;
; #pragma unroll
;     for (int i = 0; i < 64; ++i) { float zp[4];
; #pragma unroll
;         for (int r4 = 0; r4 < 4; ++r4) { const f32x4 x = *(const LAS f32x4*)(alr + i * 16 + 4 * r4); zp[r4] = x[0] * w[4 * r4] + x[1] * w[4 * r4 + 1] + x[2] * w[4 * r4 + 2] + x[3] * w[4 * r4 + 3]; }
;         const float z = bia + ((zp[0] + zp[1]) + (zp[2] + zp[3]));
;         Gc += fminf(z, 0.f) * (L2E / 16.f) - __builtin_amdgcn_logf(1.f + __builtin_amdgcn_exp2f(-fabsf(z) * L2E)) * (1.f / 16.f); Gv[i] = Gc; }
	v_mov_b32_e32 v31, v228
	v_mov_b32_e32 v228, v37
	v_pk_fma_f32 v[28:29], v[22:23], v[32:33], v[28:29]
	v_mov_b32_e32 v30, v36
	v_pk_mul_f32 v[32:33], v[18:19], v[228:229]
	v_pk_fma_f32 v[28:29], v[20:21], v[34:35], v[28:29]
	v_pk_fma_f32 v[30:31], v[12:13], v[30:31], v[32:33]
	v_mov_b32_e32 v32, v38
	v_mov_b32_e32 v33, v230
	v_pk_fma_f32 v[30:31], v[8:9], v[32:33], v[30:31]
	v_mov_b32_e32 v230, v39
	v_pk_fma_f32 v[30:31], v[16:17], v[230:231], v[30:31]
	s_nop 0
	v_pk_add_f32 v[28:29], v[28:29], v[30:31]
	s_nop 0
	v_add_f32_e32 v27, v28, v29
	v_add_f32_e32 v28, v48, v27
	v_mul_f32_e64 v27, |v28|, s34
	v_exp_f32_e32 v29, v27
	v_sub_f32_e32 v27, v232, v233
	v_min_f32_e32 v232, 0, v28
	v_add_f32_e32 v27, v26, v27
	v_add_f32_e32 v36, 1.0, v29
	ds_read_b128 v[28:31], v69 offset:3648
	ds_read_b128 v[32:35], v69 offset:3680
	v_log_f32_e32 v233, v36
	ds_read_b128 v[36:39], v69 offset:3664
	ds_read_b128 v[228:231], v69 offset:3696
	s_waitcnt lgkmcnt(3)
	v_mov_b32_e32 v234, v28
	s_waitcnt lgkmcnt(2)
	v_mov_b32_e32 v235, v32
	v_mov_b32_e32 v32, v29
	v_pk_mul_f32 v[28:29], v[14:15], v[32:33]
	v_mov_b32_e32 v32, v30
	v_pk_fma_f32 v[28:29], v[10:11], v[234:235], v[28:29]
	v_mov_b32_e32 v33, v34
	v_mov_b32_e32 v34, v31
	s_waitcnt lgkmcnt(0)
	v_mov_b32_e32 v31, v228
	v_mov_b32_e32 v228, v37
	v_pk_fma_f32 v[28:29], v[22:23], v[32:33], v[28:29]
	v_mov_b32_e32 v30, v36
	v_pk_mul_f32 v[32:33], v[18:19], v[228:229]
	v_pk_fma_f32 v[28:29], v[20:21], v[34:35], v[28:29]
	v_pk_fma_f32 v[30:31], v[12:13], v[30:31], v[32:33]
	v_mov_b32_e32 v32, v38
	v_mov_b32_e32 v33, v230
	v_pk_fma_f32 v[30:31], v[8:9], v[32:33], v[30:31]
	v_mov_b32_e32 v230, v39
	v_pk_fma_f32 v[30:31], v[16:17], v[230:231], v[30:31]
	s_nop 0
	v_pk_add_f32 v[28:29], v[28:29], v[30:31]
	s_nop 0
	v_add_f32_e32 v28, v28, v29
	v_add_f32_e32 v30, v48, v28
	v_mul_f32_e64 v28, |v30|, s34
	v_exp_f32_e32 v31, v28
	v_pk_mul_f32 v[28:29], v[232:233], s[14:15]
	v_min_f32_e32 v38, 0, v30
	v_sub_f32_e32 v28, v28, v29
	v_add_f32_e32 v29, 1.0, v31
	ds_read_b128 v[30:33], v69 offset:3712
	ds_read_b128 v[34:37], v69 offset:3744
	ds_read_b128 v[228:231], v69 offset:3728
	ds_read_b128 v[232:235], v69 offset:3760
	v_log_f32_e32 v39, v29
	v_add_f32_e32 v28, v27, v28
	s_waitcnt lgkmcnt(3)
	v_mov_b32_e32 v236, v30
	s_waitcnt lgkmcnt(2)
	v_mov_b32_e32 v237, v34
	v_mov_b32_e32 v34, v31
	v_pk_mul_f32 v[30:31], v[14:15], v[34:35]
	v_mov_b32_e32 v34, v32
	v_pk_fma_f32 v[30:31], v[10:11], v[236:237], v[30:31]
	v_mov_b32_e32 v35, v36
	v_mov_b32_e32 v36, v33
	s_waitcnt lgkmcnt(0)
	v_mov_b32_e32 v33, v232
	v_mov_b32_e32 v232, v229
	v_pk_fma_f32 v[30:31], v[22:23], v[34:35], v[30:31]
	v_mov_b32_e32 v32, v228
	v_pk_mul_f32 v[34:35], v[18:19], v[232:233]
	v_pk_fma_f32 v[30:31], v[20:21], v[36:37], v[30:31]
	v_pk_fma_f32 v[32:33], v[12:13], v[32:33], v[34:35]
	v_mov_b32_e32 v34, v230
	v_mov_b32_e32 v35, v234
	v_pk_fma_f32 v[32:33], v[8:9], v[34:35], v[32:33]
	v_mov_b32_e32 v234, v231
	v_pk_fma_f32 v[32:33], v[16:17], v[234:235], v[32:33]
	v_pk_mul_f32 v[38:39], v[38:39], s[14:15]
	v_pk_add_f32 v[30:31], v[30:31], v[32:33]
	s_nop 0
	v_add_f32_e32 v29, v30, v31
	v_add_f32_e32 v30, v48, v29
	v_mul_f32_e64 v29, |v30|, s34
	v_exp_f32_e32 v31, v29
	v_sub_f32_e32 v29, v38, v39
	v_min_f32_e32 v38, 0, v30
	v_add_f32_e32 v29, v28, v29
	v_add_f32_e32 v39, 1.0, v31
	ds_read_b128 v[30:33], v69 offset:3776
	ds_read_b128 v[34:37], v69 offset:3808
	ds_read_b128 v[228:231], v69 offset:3792
	ds_read_b128 v[232:235], v69 offset:3824
	v_log_f32_e32 v39, v39
	s_waitcnt lgkmcnt(3)
	v_mov_b32_e32 v236, v30
	s_waitcnt lgkmcnt(2)
	v_mov_b32_e32 v237, v34
	v_mov_b32_e32 v34, v31
	v_pk_mul_f32 v[30:31], v[14:15], v[34:35]
	v_mov_b32_e32 v34, v32
	v_pk_fma_f32 v[30:31], v[10:11], v[236:237], v[30:31]
	v_mov_b32_e32 v35, v36
	v_mov_b32_e32 v36, v33
	s_waitcnt lgkmcnt(0)
	v_mov_b32_e32 v33, v232
	v_mov_b32_e32 v232, v229
	v_pk_fma_f32 v[30:31], v[22:23], v[34:35], v[30:31]
	v_mov_b32_e32 v32, v228
	v_pk_mul_f32 v[34:35], v[18:19], v[232:233]
	v_pk_fma_f32 v[30:31], v[20:21], v[36:37], v[30:31]
	v_pk_fma_f32 v[32:33], v[12:13], v[32:33], v[34:35]
	v_mov_b32_e32 v34, v230
	v_mov_b32_e32 v35, v234
	v_pk_fma_f32 v[32:33], v[8:9], v[34:35], v[32:33]
	v_mov_b32_e32 v234, v231
	v_pk_fma_f32 v[32:33], v[16:17], v[234:235], v[32:33]
	s_nop 0
	v_pk_add_f32 v[30:31], v[30:31], v[32:33]
	s_nop 0
	v_add_f32_e32 v30, v30, v31
	v_add_f32_e32 v32, v48, v30
	v_mul_f32_e64 v30, |v32|, s34
	v_exp_f32_e32 v33, v30
	v_pk_mul_f32 v[30:31], v[38:39], s[14:15]
	v_min_f32_e32 v228, 0, v32
	v_sub_f32_e32 v30, v30, v31
	v_add_f32_e32 v31, 1.0, v33
	v_log_f32_e32 v229, v31
	ds_read_b128 v[32:35], v69 offset:3840
	ds_read_b128 v[36:39], v69 offset:3872
	v_add_f32_e32 v30, v29, v30
	v_pk_mul_f32 v[236:237], v[228:229], s[14:15]
	ds_read_b128 v[228:231], v69 offset:3856
	ds_read_b128 v[232:235], v69 offset:3888
	s_waitcnt lgkmcnt(2)
	v_mov_b32_e32 v239, v36
	v_mov_b32_e32 v36, v33
	v_mov_b32_e32 v238, v32
	v_pk_mul_f32 v[32:33], v[14:15], v[36:37]
	v_mov_b32_e32 v36, v34
	v_pk_fma_f32 v[32:33], v[10:11], v[238:239], v[32:33]
	v_mov_b32_e32 v37, v38
	v_mov_b32_e32 v38, v35
	s_waitcnt lgkmcnt(0)
	v_mov_b32_e32 v35, v232
	v_mov_b32_e32 v232, v229
	v_pk_fma_f32 v[32:33], v[22:23], v[36:37], v[32:33]
	v_mov_b32_e32 v34, v228
	v_pk_mul_f32 v[36:37], v[18:19], v[232:233]
	v_pk_fma_f32 v[32:33], v[20:21], v[38:39], v[32:33]
	v_pk_fma_f32 v[34:35], v[12:13], v[34:35], v[36:37]
	v_mov_b32_e32 v36, v230
	v_mov_b32_e32 v37, v234
	v_pk_fma_f32 v[34:35], v[8:9], v[36:37], v[34:35]
	v_mov_b32_e32 v234, v231
	v_pk_fma_f32 v[34:35], v[16:17], v[234:235], v[34:35]
	s_nop 0
	v_pk_add_f32 v[32:33], v[32:33], v[34:35]
	s_nop 0
	v_add_f32_e32 v31, v32, v33
	v_add_f32_e32 v32, v48, v31
	v_mul_f32_e64 v31, |v32|, s34
	v_exp_f32_e32 v33, v31
	v_sub_f32_e32 v31, v236, v237
	v_min_f32_e32 v236, 0, v32
	v_add_f32_e32 v31, v30, v31
	v_add_f32_e32 v225, 1.0, v33
	ds_read_b128 v[32:35], v69 offset:3904
	ds_read_b128 v[36:39], v69 offset:3936
	ds_read_b128 v[228:231], v69 offset:3920
	ds_read_b128 v[232:235], v69 offset:3952
	v_log_f32_e32 v237, v225
	s_waitcnt lgkmcnt(3)
; #define LAS __attribute__((address_space(3)))
; __device__ __forceinline__ unsigned cvtpk_bf16(float lo, float hi) { unsigned r; asm("v_cvt_pk_bf16_f32 %0, %1, %2" : "=v"(r) : "v"(lo), "v"(hi)); return r; }
; __device__ __forceinline__ void prep_item(const Args& a, LAS unsigned char* lds, int tid, int dir, int b, int ch) {
;     ...
;     for (int i = 0; i < 64; ++i) { float zp[4];
; #pragma unroll
;         for (int r4 = 0; r4 < 4; ++r4) { const f32x4 x = *(const LAS f32x4*)(alr + i * 16 + 4 * r4); zp[r4] = x[0] * w[4 * r4] + x[1] * w[4 * r4 + 1] + x[2] * w[4 * r4 + 2] + x[3] * w[4 * r4 + 3]; }
;         const float z = bia + ((zp[0] + zp[1]) + (zp[2] + zp[3]));
;         Gc += fminf(z, 0.f) * (L2E / 16.f) - __builtin_amdgcn_logf(1.f + __builtin_amdgcn_exp2f(-fabsf(z) * L2E)) * (1.f / 16.f); Gv[i] = Gc; }
;     const float Gmid = Gv[32], Gend = Gv[63];
;     DEC[((size_t)(dir * 8 + b) * 36 + ch) * 512 + col] = __builtin_amdgcn_exp2f(Gend);
;     const float eEM = __builtin_amdgcn_exp2f(Gend - Gmid);
;     bf16* kdrow = KD + ((((size_t)(dir * 8 + b) * 36 + ch) * 4 + h) * 128 + dk) * 64;
; #pragma unroll
;     for (int i0 = 0; i0 < 64; i0 += 8) { float kd[8];
; #pragma unroll
;         for (int ii = 0; ii < 8; ++ii) { const int i = i0 + ii; const float kv = bf1(Kt[i * TS + col]);
;             if (lat) { const float em = __builtin_amdgcn_exp2f(Gmid - Gv[i]); kd[ii] = kv * (em * eEM);
;                 const float qv = bf1(Qt[i * TS + col]) * 0.08838834764831845f;
;                 const unsigned qk = cvtpk_bf16(qv * __builtin_amdgcn_exp2f(Gv[i] - Gmid), kv * em);
;                 Qt[i * TS + col] = (bf16)(qk & 0xffffu); Kt[i * TS + col] = (bf16)(qk >> 16); }
;             else kd[ii] = kv * __builtin_amdgcn_exp2f(Gend - Gv[i]); }
	v_mov_b32_e32 v238, v32
	s_waitcnt lgkmcnt(2)
	v_mov_b32_e32 v239, v36
	v_mov_b32_e32 v36, v33
	v_pk_mul_f32 v[32:33], v[14:15], v[36:37]
	v_mov_b32_e32 v36, v34
	v_pk_fma_f32 v[32:33], v[10:11], v[238:239], v[32:33]
	v_mov_b32_e32 v37, v38
	v_mov_b32_e32 v38, v35
	s_waitcnt lgkmcnt(0)
	v_mov_b32_e32 v35, v232
	v_mov_b32_e32 v232, v229
	v_pk_fma_f32 v[32:33], v[22:23], v[36:37], v[32:33]
	v_mov_b32_e32 v34, v228
	v_pk_mul_f32 v[36:37], v[18:19], v[232:233]
	v_pk_fma_f32 v[32:33], v[20:21], v[38:39], v[32:33]
	v_pk_fma_f32 v[34:35], v[12:13], v[34:35], v[36:37]
	v_mov_b32_e32 v36, v230
	v_mov_b32_e32 v37, v234
	v_pk_fma_f32 v[34:35], v[8:9], v[36:37], v[34:35]
	v_mov_b32_e32 v234, v231
	v_pk_fma_f32 v[34:35], v[16:17], v[234:235], v[34:35]
	s_nop 0
	v_pk_add_f32 v[32:33], v[32:33], v[34:35]
	s_nop 0
	v_add_f32_e32 v32, v32, v33
	v_add_f32_e32 v38, v48, v32
	v_mul_f32_e64 v32, |v38|, s34
	v_exp_f32_e32 v34, v32
	v_pk_mul_f32 v[32:33], v[236:237], s[14:15]
	v_min_f32_e32 v38, 0, v38
	v_sub_f32_e32 v32, v32, v33
	v_add_f32_e32 v33, 1.0, v34
	ds_read_b128 v[34:37], v69 offset:3968
	ds_read_b128 v[228:231], v69 offset:4000
	ds_read_b128 v[232:235], v69 offset:3984
	ds_read_b128 v[236:239], v69 offset:4016
	v_log_f32_e32 v39, v33
	v_add_f32_e32 v32, v31, v32
	s_waitcnt lgkmcnt(3)
	v_mov_b32_e32 v240, v34
	s_waitcnt lgkmcnt(2)
	v_mov_b32_e32 v241, v228
	v_mov_b32_e32 v228, v35
	v_pk_mul_f32 v[34:35], v[14:15], v[228:229]
	v_mov_b32_e32 v228, v36
	v_pk_fma_f32 v[34:35], v[10:11], v[240:241], v[34:35]
	v_mov_b32_e32 v229, v230
	v_mov_b32_e32 v230, v37
	s_waitcnt lgkmcnt(0)
	v_mov_b32_e32 v37, v236
	v_mov_b32_e32 v236, v233
	v_pk_fma_f32 v[34:35], v[22:23], v[228:229], v[34:35]
	v_mov_b32_e32 v36, v232
	v_pk_mul_f32 v[228:229], v[18:19], v[236:237]
	v_pk_fma_f32 v[34:35], v[20:21], v[230:231], v[34:35]
	v_pk_fma_f32 v[36:37], v[12:13], v[36:37], v[228:229]
	v_mov_b32_e32 v228, v234
	v_mov_b32_e32 v229, v238
	v_pk_fma_f32 v[36:37], v[8:9], v[228:229], v[36:37]
	v_mov_b32_e32 v238, v235
	v_pk_fma_f32 v[36:37], v[16:17], v[238:239], v[36:37]
	s_nop 0
	v_pk_add_f32 v[34:35], v[34:35], v[36:37]
	s_nop 0
	v_add_f32_e32 v33, v34, v35
	v_add_f32_e32 v33, v48, v33
	v_mul_f32_e64 v34, |v33|, s34
	v_exp_f32_e32 v36, v34
	v_pk_mul_f32 v[34:35], v[38:39], s[14:15]
	v_add_f32_e32 v39, 1.0, v36
	v_sub_f32_e32 v38, v34, v35
	ds_read_b128 v[34:37], v69 offset:4032
	ds_read_b128 v[228:231], v69 offset:4064
	ds_read_b128 v[232:235], v69 offset:4048
	ds_read_b128 v[236:239], v69 offset:4080
	v_log_f32_e32 v39, v39
	s_waitcnt lgkmcnt(3)
	v_mov_b32_e32 v240, v34
	s_waitcnt lgkmcnt(2)
	v_mov_b32_e32 v241, v228
	v_mov_b32_e32 v228, v35
	v_pk_mul_f32 v[14:15], v[14:15], v[228:229]
	s_nop 0
	v_pk_fma_f32 v[10:11], v[10:11], v[240:241], v[14:15]
	v_mov_b32_e32 v14, v36
	v_mov_b32_e32 v15, v230
	v_pk_fma_f32 v[10:11], v[22:23], v[14:15], v[10:11]
	s_waitcnt lgkmcnt(0)
	v_mov_b32_e32 v15, v236
	v_mov_b32_e32 v236, v233
	v_mov_b32_e32 v14, v232
	v_pk_mul_f32 v[18:19], v[18:19], v[236:237]
	v_mov_b32_e32 v230, v37
	v_pk_fma_f32 v[12:13], v[12:13], v[14:15], v[18:19]
	v_mov_b32_e32 v14, v234
	v_mov_b32_e32 v15, v238
	v_pk_fma_f32 v[8:9], v[8:9], v[14:15], v[12:13]
	v_mov_b32_e32 v238, v235
	v_pk_fma_f32 v[10:11], v[20:21], v[230:231], v[10:11]
	v_pk_fma_f32 v[8:9], v[16:17], v[238:239], v[8:9]
	v_add_f32_e32 v13, v32, v38
	v_pk_add_f32 v[8:9], v[10:11], v[8:9]
	v_min_f32_e32 v38, 0, v33
	v_add_f32_e32 v8, v8, v9
	v_add_f32_e32 v10, v48, v8
	v_mul_f32_e64 v8, |v10|, s34
	v_exp_f32_e32 v11, v8
	v_pk_mul_f32 v[8:9], v[38:39], s[14:15]
	v_min_f32_e32 v14, 0, v10
	v_sub_f32_e32 v8, v8, v9
	v_add_f32_e32 v11, 1.0, v11
	v_log_f32_e32 v15, v11
	v_add_f32_e32 v11, v13, v8
	v_sub_f32_e32 v33, v46, v45
	v_exp_f32_e32 v33, v33
	v_pk_mul_f32 v[8:9], v[14:15], s[14:15]
	v_sub_f32_e32 v14, v45, v46
	v_sub_f32_e32 v8, v8, v9
	v_add_f32_e32 v10, v11, v8
	v_exp_f32_e32 v12, v10
	v_lshl_add_u64 v[8:9], v[74:75], 0, s[16:17]
	v_exp_f32_e32 v14, v14
	s_lshl_b64 s[16:17], s[4:5], 7
	global_store_dword v[8:9], v12, off
	v_sub_f32_e32 v8, v10, v45
	v_exp_f32_e32 v12, v8
	ds_read_u16 v15, v108 offset:4096
	ds_read_u16 v16, v108 offset:5136
	ds_read_u16 v17, v108 offset:6176
	ds_read_u16 v18, v108 offset:7216
	ds_read_u16 v19, v108 offset:8256
	ds_read_u16 v20, v108 offset:9296
	ds_read_u16 v21, v108 offset:10336
	ds_read_u16 v22, v108 offset:11376
	ds_read_u16 v34, v110
	ds_read_u16 v35, v111
	ds_read_u16 v36, v112
	ds_read_u16 v37, v113
	ds_read_u16 v38, v114
	ds_read_u16 v39, v115
	ds_read_u16 v46, v116
	ds_read_u16 v48, v117
	s_waitcnt lgkmcnt(14)
	v_lshlrev_b32_e32 v15, 16, v15
	v_mul_f32_e32 v23, v14, v12
	s_waitcnt lgkmcnt(7)
	v_lshlrev_b32_e32 v34, 16, v34
	v_mul_f32_e32 v23, v23, v15
	v_mul_f32_e32 v34, 0x3db504f3, v34
	v_mul_f32_e32 v14, v14, v15
	v_sub_f32_e32 v15, v45, v49
	v_mul_f32_e32 v33, v33, v34
	v_exp_f32_e32 v15, v15
	v_cvt_pk_bf16_f32 v14, v33, v14
	v_sub_f32_e32 v33, v49, v45
	v_exp_f32_e32 v33, v33
	ds_write_b16 v110, v14
	ds_write_b16_d16_hi v108, v14 offset:4096
	v_lshlrev_b32_e32 v14, 16, v16
	v_mul_f32_e32 v16, v15, v12
	s_waitcnt lgkmcnt(8)
	v_lshlrev_b32_e32 v34, 16, v35
	v_mul_f32_e32 v16, v16, v14
	v_mul_f32_e32 v34, 0x3db504f3, v34
	v_mul_f32_e32 v14, v15, v14
	v_sub_f32_e32 v15, v45, v51
	v_mul_f32_e32 v33, v33, v34
	v_exp_f32_e32 v15, v15
	v_cvt_pk_bf16_f32 v14, v33, v14
	v_sub_f32_e32 v33, v51, v45
	v_exp_f32_e32 v33, v33
	ds_write_b16 v111, v14
	ds_write_b16_d16_hi v108, v14 offset:5136
	v_lshlrev_b32_e32 v14, 16, v17
	v_mul_f32_e32 v17, v15, v12
	s_waitcnt lgkmcnt(9)
; __device__ __forceinline__ unsigned cvtpk_bf16(float lo, float hi) { unsigned r; asm("v_cvt_pk_bf16_f32 %0, %1, %2" : "=v"(r) : "v"(lo), "v"(hi)); return r; }
; __device__ __forceinline__ void prep_item(const Args& a, LAS unsigned char* lds, int tid, int dir, int b, int ch) {
;     ...
;     for (int i0 = 0; i0 < 64; i0 += 8) { float kd[8];
; #pragma unroll
;         for (int ii = 0; ii < 8; ++ii) { const int i = i0 + ii; const float kv = bf1(Kt[i * TS + col]);
;             if (lat) { const float em = __builtin_amdgcn_exp2f(Gmid - Gv[i]); kd[ii] = kv * (em * eEM);
;                 const float qv = bf1(Qt[i * TS + col]) * 0.08838834764831845f;
;                 const unsigned qk = cvtpk_bf16(qv * __builtin_amdgcn_exp2f(Gv[i] - Gmid), kv * em);
;                 Qt[i * TS + col] = (bf16)(qk & 0xffffu); Kt[i * TS + col] = (bf16)(qk >> 16); }
;             else kd[ii] = kv * __builtin_amdgcn_exp2f(Gend - Gv[i]); }
;         v4u o; o.x = cvtpk_bf16(kd[0], kd[1]); o.y = cvtpk_bf16(kd[2], kd[3]); o.z = cvtpk_bf16(kd[4], kd[5]); o.w = cvtpk_bf16(kd[6], kd[7]);
;         *(v4u*)(kdrow + i0) = o; }
	v_lshlrev_b32_e32 v34, 16, v36
	v_mul_f32_e32 v17, v17, v14
	v_mul_f32_e32 v34, 0x3db504f3, v34
	v_mul_f32_e32 v14, v15, v14
	v_sub_f32_e32 v15, v45, v53
	v_mul_f32_e32 v33, v33, v34
	v_exp_f32_e32 v15, v15
	v_cvt_pk_bf16_f32 v14, v33, v14
	v_sub_f32_e32 v33, v53, v45
	v_exp_f32_e32 v33, v33
	ds_write_b16 v112, v14
	ds_write_b16_d16_hi v108, v14 offset:6176
	v_lshlrev_b32_e32 v14, 16, v18
	v_mul_f32_e32 v18, v15, v12
	s_waitcnt lgkmcnt(10)
	v_lshlrev_b32_e32 v34, 16, v37
	v_mul_f32_e32 v18, v18, v14
	v_mul_f32_e32 v34, 0x3db504f3, v34
	v_mul_f32_e32 v14, v15, v14
	v_sub_f32_e32 v15, v45, v55
	v_mul_f32_e32 v33, v33, v34
	v_exp_f32_e32 v15, v15
	v_cvt_pk_bf16_f32 v14, v33, v14
	v_sub_f32_e32 v33, v55, v45
	v_exp_f32_e32 v33, v33
	ds_write_b16 v113, v14
	ds_write_b16_d16_hi v108, v14 offset:7216
	v_lshlrev_b32_e32 v14, 16, v19
	v_mul_f32_e32 v19, v15, v12
	s_waitcnt lgkmcnt(11)
	v_lshlrev_b32_e32 v34, 16, v38
	v_mul_f32_e32 v19, v19, v14
	v_mul_f32_e32 v34, 0x3db504f3, v34
	v_mul_f32_e32 v14, v15, v14
	v_sub_f32_e32 v15, v45, v58
	v_mul_f32_e32 v33, v33, v34
	v_exp_f32_e32 v15, v15
	v_cvt_pk_bf16_f32 v14, v33, v14
	v_sub_f32_e32 v33, v58, v45
	v_exp_f32_e32 v33, v33
	ds_write_b16 v114, v14
	ds_write_b16_d16_hi v108, v14 offset:8256
	v_lshlrev_b32_e32 v14, 16, v20
	v_mul_f32_e32 v20, v15, v12
	s_waitcnt lgkmcnt(12)
	v_lshlrev_b32_e32 v34, 16, v39
	v_mul_f32_e32 v20, v20, v14
	v_mul_f32_e32 v34, 0x3db504f3, v34
	v_mul_f32_e32 v14, v15, v14
	v_sub_f32_e32 v15, v45, v61
	v_mul_f32_e32 v33, v33, v34
	v_exp_f32_e32 v15, v15
	v_cvt_pk_bf16_f32 v14, v33, v14
	v_sub_f32_e32 v33, v61, v45
	v_exp_f32_e32 v33, v33
	ds_write_b16 v115, v14
	ds_write_b16_d16_hi v108, v14 offset:9296
	v_lshlrev_b32_e32 v14, 16, v21
	v_mul_f32_e32 v21, v15, v12
	s_waitcnt lgkmcnt(13)
	v_lshlrev_b32_e32 v34, 16, v46
	v_mul_f32_e32 v21, v21, v14
	v_mul_f32_e32 v34, 0x3db504f3, v34
	v_mul_f32_e32 v14, v15, v14
	v_sub_f32_e32 v15, v45, v64
	v_mul_f32_e32 v33, v33, v34
	v_exp_f32_e32 v15, v15
	v_cvt_pk_bf16_f32 v14, v33, v14
	v_sub_f32_e32 v33, v64, v45
	v_exp_f32_e32 v33, v33
	ds_write_b16 v116, v14
	ds_write_b16_d16_hi v108, v14 offset:10336
	v_lshlrev_b32_e32 v14, 16, v22
	v_mul_f32_e32 v22, v15, v12
	s_waitcnt lgkmcnt(14)
	v_lshlrev_b32_e32 v34, 16, v48
	v_mul_f32_e32 v22, v22, v14
	v_mul_f32_e32 v34, 0x3db504f3, v34
	v_mul_f32_e32 v14, v15, v14
	v_mul_f32_e32 v33, v33, v34
	v_cvt_pk_bf16_f32 v14, v33, v14
	v_lshl_add_u64 v[8:9], v[76:77], 0, s[2:3]
	ds_write_b16 v117, v14
	ds_write_b16_d16_hi v108, v14 offset:11376
	v_cvt_pk_bf16_f32 v14, v23, v16
	v_cvt_pk_bf16_f32 v15, v17, v18
	v_cvt_pk_bf16_f32 v16, v19, v20
	v_cvt_pk_bf16_f32 v17, v21, v22
	global_store_dwordx4 v[8:9], v[14:17], off
	v_sub_f32_e32 v33, v57, v45
	v_exp_f32_e32 v33, v33
	v_sub_f32_e32 v14, v45, v57
	v_exp_f32_e32 v14, v14
	ds_read_u16 v15, v108 offset:12416
	ds_read_u16 v16, v108 offset:13456
	ds_read_u16 v17, v108 offset:14496
	ds_read_u16 v18, v108 offset:15536
	ds_read_u16 v19, v108 offset:16576
	ds_read_u16 v20, v108 offset:17616
	ds_read_u16 v21, v108 offset:18656
	ds_read_u16 v22, v108 offset:19696
	ds_read_u16 v34, v118
	ds_read_u16 v35, v119
	ds_read_u16 v36, v120
	ds_read_u16 v37, v121
	ds_read_u16 v38, v122
	ds_read_u16 v39, v123
	ds_read_u16 v46, v124
	ds_read_u16 v48, v125
	s_waitcnt lgkmcnt(14)
	v_lshlrev_b32_e32 v15, 16, v15
	v_mul_f32_e32 v23, v14, v12
	s_waitcnt lgkmcnt(7)
	v_lshlrev_b32_e32 v34, 16, v34
	v_mul_f32_e32 v23, v23, v15
	v_mul_f32_e32 v34, 0x3db504f3, v34
	v_mul_f32_e32 v14, v14, v15
	v_sub_f32_e32 v15, v45, v60
	v_mul_f32_e32 v33, v33, v34
	v_exp_f32_e32 v15, v15
	v_cvt_pk_bf16_f32 v14, v33, v14
	v_sub_f32_e32 v33, v60, v45
	v_exp_f32_e32 v33, v33
	ds_write_b16 v118, v14
	ds_write_b16_d16_hi v108, v14 offset:12416
	v_lshlrev_b32_e32 v14, 16, v16
	v_mul_f32_e32 v16, v15, v12
	s_waitcnt lgkmcnt(8)
	v_lshlrev_b32_e32 v34, 16, v35
	v_mul_f32_e32 v16, v16, v14
	v_mul_f32_e32 v34, 0x3db504f3, v34
	v_mul_f32_e32 v14, v15, v14
	v_sub_f32_e32 v15, v45, v63
	v_mul_f32_e32 v33, v33, v34
	v_exp_f32_e32 v15, v15
	v_cvt_pk_bf16_f32 v14, v33, v14
	v_sub_f32_e32 v33, v63, v45
	v_exp_f32_e32 v33, v33
	ds_write_b16 v119, v14
	ds_write_b16_d16_hi v108, v14 offset:13456
	v_lshlrev_b32_e32 v14, 16, v17
	v_mul_f32_e32 v17, v15, v12
	s_waitcnt lgkmcnt(9)
	v_lshlrev_b32_e32 v34, 16, v36
	v_mul_f32_e32 v17, v17, v14
	v_mul_f32_e32 v34, 0x3db504f3, v34
	v_mul_f32_e32 v14, v15, v14
	v_sub_f32_e32 v15, v45, v78
	v_mul_f32_e32 v33, v33, v34
	v_exp_f32_e32 v15, v15
	v_cvt_pk_bf16_f32 v14, v33, v14
	v_sub_f32_e32 v33, v78, v45
	v_exp_f32_e32 v33, v33
	ds_write_b16 v120, v14
	ds_write_b16_d16_hi v108, v14 offset:14496
	v_lshlrev_b32_e32 v14, 16, v18
	v_mul_f32_e32 v18, v15, v12
	s_waitcnt lgkmcnt(10)
	v_lshlrev_b32_e32 v34, 16, v37
	v_mul_f32_e32 v18, v18, v14
	v_mul_f32_e32 v34, 0x3db504f3, v34
	v_mul_f32_e32 v14, v15, v14
	v_sub_f32_e32 v15, v45, v79
	v_mul_f32_e32 v33, v33, v34
	v_exp_f32_e32 v15, v15
	v_cvt_pk_bf16_f32 v14, v33, v14
	v_sub_f32_e32 v33, v79, v45
	v_exp_f32_e32 v33, v33
	ds_write_b16 v121, v14
	ds_write_b16_d16_hi v108, v14 offset:15536
	v_lshlrev_b32_e32 v14, 16, v19
	v_mul_f32_e32 v19, v15, v12
	s_waitcnt lgkmcnt(11)
	v_lshlrev_b32_e32 v34, 16, v38
	v_mul_f32_e32 v19, v19, v14
	v_mul_f32_e32 v34, 0x3db504f3, v34
	v_mul_f32_e32 v14, v15, v14
	v_sub_f32_e32 v15, v45, v197
	v_mul_f32_e32 v33, v33, v34
	v_exp_f32_e32 v15, v15
	v_cvt_pk_bf16_f32 v14, v33, v14
	v_sub_f32_e32 v33, v197, v45
	v_exp_f32_e32 v33, v33
	ds_write_b16 v122, v14
	ds_write_b16_d16_hi v108, v14 offset:16576
	v_lshlrev_b32_e32 v14, 16, v20
	v_mul_f32_e32 v20, v15, v12
	s_waitcnt lgkmcnt(12)
; __device__ __forceinline__ unsigned cvtpk_bf16(float lo, float hi) { unsigned r; asm("v_cvt_pk_bf16_f32 %0, %1, %2" : "=v"(r) : "v"(lo), "v"(hi)); return r; }
; __device__ __forceinline__ void prep_item(const Args& a, LAS unsigned char* lds, int tid, int dir, int b, int ch) {
;     ...
;     for (int i0 = 0; i0 < 64; i0 += 8) { float kd[8];
; #pragma unroll
;         for (int ii = 0; ii < 8; ++ii) { const int i = i0 + ii; const float kv = bf1(Kt[i * TS + col]);
;             if (lat) { const float em = __builtin_amdgcn_exp2f(Gmid - Gv[i]); kd[ii] = kv * (em * eEM);
;                 const float qv = bf1(Qt[i * TS + col]) * 0.08838834764831845f;
;                 const unsigned qk = cvtpk_bf16(qv * __builtin_amdgcn_exp2f(Gv[i] - Gmid), kv * em);
;                 Qt[i * TS + col] = (bf16)(qk & 0xffffu); Kt[i * TS + col] = (bf16)(qk >> 16); }
;             else kd[ii] = kv * __builtin_amdgcn_exp2f(Gend - Gv[i]); }
;         v4u o; o.x = cvtpk_bf16(kd[0], kd[1]); o.y = cvtpk_bf16(kd[2], kd[3]); o.z = cvtpk_bf16(kd[4], kd[5]); o.w = cvtpk_bf16(kd[6], kd[7]);
;         *(v4u*)(kdrow + i0) = o; }
	v_lshlrev_b32_e32 v34, 16, v39
	v_mul_f32_e32 v20, v20, v14
	v_mul_f32_e32 v34, 0x3db504f3, v34
	v_mul_f32_e32 v14, v15, v14
	v_sub_f32_e32 v15, v45, v200
	v_mul_f32_e32 v33, v33, v34
	v_exp_f32_e32 v15, v15
	v_cvt_pk_bf16_f32 v14, v33, v14
	v_sub_f32_e32 v33, v200, v45
	v_exp_f32_e32 v33, v33
	ds_write_b16 v123, v14
	ds_write_b16_d16_hi v108, v14 offset:17616
	v_lshlrev_b32_e32 v14, 16, v21
	v_mul_f32_e32 v21, v15, v12
	s_waitcnt lgkmcnt(13)
	v_lshlrev_b32_e32 v34, 16, v46
	v_mul_f32_e32 v21, v21, v14
	v_mul_f32_e32 v34, 0x3db504f3, v34
	v_mul_f32_e32 v14, v15, v14
	v_sub_f32_e32 v15, v45, v203
	v_mul_f32_e32 v33, v33, v34
	v_exp_f32_e32 v15, v15
	v_cvt_pk_bf16_f32 v14, v33, v14
	v_sub_f32_e32 v33, v203, v45
	v_exp_f32_e32 v33, v33
	ds_write_b16 v124, v14
	ds_write_b16_d16_hi v108, v14 offset:18656
	v_lshlrev_b32_e32 v14, 16, v22
	v_mul_f32_e32 v22, v15, v12
	s_waitcnt lgkmcnt(14)
	v_lshlrev_b32_e32 v34, 16, v48
	v_mul_f32_e32 v22, v22, v14
	v_mul_f32_e32 v34, 0x3db504f3, v34
	v_mul_f32_e32 v14, v15, v14
	v_mul_f32_e32 v33, v33, v34
	v_cvt_pk_bf16_f32 v14, v33, v14
	ds_write_b16 v125, v14
	ds_write_b16_d16_hi v108, v14 offset:19696
	v_cvt_pk_bf16_f32 v14, v23, v16
	v_cvt_pk_bf16_f32 v15, v17, v18
	v_cvt_pk_bf16_f32 v16, v19, v20
	v_cvt_pk_bf16_f32 v17, v21, v22
	global_store_dwordx4 v[8:9], v[14:17], off offset:16
	v_sub_f32_e32 v33, v196, v45
	v_exp_f32_e32 v33, v33
	v_sub_f32_e32 v14, v45, v196
	v_exp_f32_e32 v14, v14
	ds_read_u16 v15, v108 offset:20736
	ds_read_u16 v16, v108 offset:21776
	ds_read_u16 v17, v108 offset:22816
	ds_read_u16 v18, v108 offset:23856
	ds_read_u16 v19, v108 offset:24896
	ds_read_u16 v20, v108 offset:25936
	ds_read_u16 v21, v108 offset:26976
	ds_read_u16 v22, v108 offset:28016
	ds_read_u16 v34, v126
	ds_read_u16 v35, v127
	ds_read_u16 v36, v128
	ds_read_u16 v37, v129
	ds_read_u16 v38, v130
	ds_read_u16 v39, v131
	ds_read_u16 v46, v132
	ds_read_u16 v48, v133
	s_waitcnt lgkmcnt(14)
	v_lshlrev_b32_e32 v15, 16, v15
	v_mul_f32_e32 v23, v14, v12
	s_waitcnt lgkmcnt(7)
	v_lshlrev_b32_e32 v34, 16, v34
	v_mul_f32_e32 v23, v23, v15
	v_mul_f32_e32 v34, 0x3db504f3, v34
	v_mul_f32_e32 v14, v14, v15
	v_sub_f32_e32 v15, v45, v199
	v_mul_f32_e32 v33, v33, v34
	v_exp_f32_e32 v15, v15
	v_cvt_pk_bf16_f32 v14, v33, v14
	v_sub_f32_e32 v33, v199, v45
	v_exp_f32_e32 v33, v33
	ds_write_b16 v126, v14
	ds_write_b16_d16_hi v108, v14 offset:20736
	v_lshlrev_b32_e32 v14, 16, v16
	v_mul_f32_e32 v16, v15, v12
	s_waitcnt lgkmcnt(8)
	v_lshlrev_b32_e32 v34, 16, v35
	v_mul_f32_e32 v16, v16, v14
	v_mul_f32_e32 v34, 0x3db504f3, v34
	v_mul_f32_e32 v14, v15, v14
	v_sub_f32_e32 v15, v45, v202
	v_mul_f32_e32 v33, v33, v34
	v_exp_f32_e32 v15, v15
	v_cvt_pk_bf16_f32 v14, v33, v14
	v_sub_f32_e32 v33, v202, v45
	v_exp_f32_e32 v33, v33
	ds_write_b16 v127, v14
	ds_write_b16_d16_hi v108, v14 offset:21776
	v_lshlrev_b32_e32 v14, 16, v17
	v_mul_f32_e32 v17, v15, v12
	s_waitcnt lgkmcnt(9)
	v_lshlrev_b32_e32 v34, 16, v36
	v_mul_f32_e32 v17, v17, v14
	v_mul_f32_e32 v34, 0x3db504f3, v34
	v_mul_f32_e32 v14, v15, v14
	v_sub_f32_e32 v15, v45, v205
	v_mul_f32_e32 v33, v33, v34
	v_exp_f32_e32 v15, v15
	v_cvt_pk_bf16_f32 v14, v33, v14
	v_sub_f32_e32 v33, v205, v45
	v_exp_f32_e32 v33, v33
	ds_write_b16 v128, v14
	ds_write_b16_d16_hi v108, v14 offset:22816
	v_lshlrev_b32_e32 v14, 16, v18
	v_mul_f32_e32 v18, v15, v12
	s_waitcnt lgkmcnt(10)
	v_lshlrev_b32_e32 v34, 16, v37
	v_mul_f32_e32 v18, v18, v14
	v_mul_f32_e32 v34, 0x3db504f3, v34
	v_mul_f32_e32 v14, v15, v14
	v_sub_f32_e32 v15, v45, v207
	v_mul_f32_e32 v33, v33, v34
	v_exp_f32_e32 v15, v15
	v_cvt_pk_bf16_f32 v14, v33, v14
	v_sub_f32_e32 v33, v207, v45
	v_exp_f32_e32 v33, v33
	ds_write_b16 v129, v14
	ds_write_b16_d16_hi v108, v14 offset:23856
	v_lshlrev_b32_e32 v14, 16, v19
	v_mul_f32_e32 v19, v15, v12
	s_waitcnt lgkmcnt(11)
	v_lshlrev_b32_e32 v34, 16, v38
	v_mul_f32_e32 v19, v19, v14
	v_mul_f32_e32 v34, 0x3db504f3, v34
	v_mul_f32_e32 v14, v15, v14
	v_sub_f32_e32 v15, v45, v209
	v_mul_f32_e32 v33, v33, v34
	v_exp_f32_e32 v15, v15
	v_cvt_pk_bf16_f32 v14, v33, v14
	v_sub_f32_e32 v33, v209, v45
	v_exp_f32_e32 v33, v33
	ds_write_b16 v130, v14
	ds_write_b16_d16_hi v108, v14 offset:24896
	v_lshlrev_b32_e32 v14, 16, v20
	v_mul_f32_e32 v20, v15, v12
	s_waitcnt lgkmcnt(12)
	v_lshlrev_b32_e32 v34, 16, v39
	v_mul_f32_e32 v20, v20, v14
	v_mul_f32_e32 v34, 0x3db504f3, v34
	v_mul_f32_e32 v14, v15, v14
	v_sub_f32_e32 v15, v45, v211
	v_mul_f32_e32 v33, v33, v34
	v_exp_f32_e32 v15, v15
	v_cvt_pk_bf16_f32 v14, v33, v14
	v_sub_f32_e32 v33, v211, v45
	v_exp_f32_e32 v33, v33
	ds_write_b16 v131, v14
	ds_write_b16_d16_hi v108, v14 offset:25936
	v_lshlrev_b32_e32 v14, 16, v21
	v_mul_f32_e32 v21, v15, v12
	s_waitcnt lgkmcnt(13)
	v_lshlrev_b32_e32 v34, 16, v46
	v_mul_f32_e32 v21, v21, v14
	v_mul_f32_e32 v34, 0x3db504f3, v34
	v_mul_f32_e32 v14, v15, v14
	v_sub_f32_e32 v15, v45, v213
	v_mul_f32_e32 v33, v33, v34
	v_exp_f32_e32 v15, v15
	v_cvt_pk_bf16_f32 v14, v33, v14
	v_sub_f32_e32 v33, v213, v45
	v_exp_f32_e32 v33, v33
	ds_write_b16 v132, v14
	ds_write_b16_d16_hi v108, v14 offset:26976
	v_lshlrev_b32_e32 v14, 16, v22
	v_mul_f32_e32 v22, v15, v12
	s_waitcnt lgkmcnt(14)
; __device__ __forceinline__ unsigned cvtpk_bf16(float lo, float hi) { unsigned r; asm("v_cvt_pk_bf16_f32 %0, %1, %2" : "=v"(r) : "v"(lo), "v"(hi)); return r; }
; __device__ __forceinline__ void prep_item(const Args& a, LAS unsigned char* lds, int tid, int dir, int b, int ch) {
;     ...
;     for (int i0 = 0; i0 < 64; i0 += 8) { float kd[8];
; #pragma unroll
;         for (int ii = 0; ii < 8; ++ii) { const int i = i0 + ii; const float kv = bf1(Kt[i * TS + col]);
;             if (lat) { const float em = __builtin_amdgcn_exp2f(Gmid - Gv[i]); kd[ii] = kv * (em * eEM);
;                 const float qv = bf1(Qt[i * TS + col]) * 0.08838834764831845f;
;                 const unsigned qk = cvtpk_bf16(qv * __builtin_amdgcn_exp2f(Gv[i] - Gmid), kv * em);
;                 Qt[i * TS + col] = (bf16)(qk & 0xffffu); Kt[i * TS + col] = (bf16)(qk >> 16); }
;             else kd[ii] = kv * __builtin_amdgcn_exp2f(Gend - Gv[i]); }
;         v4u o; o.x = cvtpk_bf16(kd[0], kd[1]); o.y = cvtpk_bf16(kd[2], kd[3]); o.z = cvtpk_bf16(kd[4], kd[5]); o.w = cvtpk_bf16(kd[6], kd[7]);
;         *(v4u*)(kdrow + i0) = o; }
	v_lshlrev_b32_e32 v34, 16, v48
	v_mul_f32_e32 v22, v22, v14
	v_mul_f32_e32 v34, 0x3db504f3, v34
	v_mul_f32_e32 v14, v15, v14
	v_mul_f32_e32 v33, v33, v34
	v_cvt_pk_bf16_f32 v14, v33, v14
	ds_write_b16 v133, v14
	ds_write_b16_d16_hi v108, v14 offset:28016
	v_cvt_pk_bf16_f32 v14, v23, v16
	v_cvt_pk_bf16_f32 v15, v17, v18
	v_cvt_pk_bf16_f32 v16, v19, v20
	v_cvt_pk_bf16_f32 v17, v21, v22
	global_store_dwordx4 v[8:9], v[14:17], off offset:32
	v_sub_f32_e32 v33, v47, v45
	v_exp_f32_e32 v33, v33
	v_sub_f32_e32 v14, v45, v47
	v_exp_f32_e32 v14, v14
	ds_read_u16 v18, v108 offset:29056
	ds_read_u16 v15, v108 offset:30096
	ds_read_u16 v16, v108 offset:31136
	ds_read_u16 v17, v108 offset:32176
	ds_read_u16 v19, v109 offset:62400
	ds_read_u16 v20, v109 offset:63440
	ds_read_u16 v21, v109 offset:64480
	ds_read_u16 v22, v109 offset:65520
	ds_read_u16 v34, v134
	ds_read_u16 v35, v135
	ds_read_u16 v36, v136
	ds_read_u16 v37, v137
	ds_read_u16 v38, v138
	ds_read_u16 v39, v139
	ds_read_u16 v46, v140
	ds_read_u16 v47, v141
	s_waitcnt lgkmcnt(14)
	v_lshlrev_b32_e32 v18, 16, v18
	v_mul_f32_e32 v23, v14, v12
	s_waitcnt lgkmcnt(7)
	v_lshlrev_b32_e32 v34, 16, v34
	v_mul_f32_e32 v23, v23, v18
	v_mul_f32_e32 v34, 0x3db504f3, v34
	v_mul_f32_e32 v14, v14, v18
	v_sub_f32_e32 v18, v45, v50
	v_mul_f32_e32 v33, v33, v34
	v_exp_f32_e32 v18, v18
	v_cvt_pk_bf16_f32 v14, v33, v14
	v_sub_f32_e32 v33, v50, v45
	v_exp_f32_e32 v33, v33
	ds_write_b16 v134, v14
	ds_write_b16_d16_hi v108, v14 offset:29056
	v_lshlrev_b32_e32 v14, 16, v15
	v_mul_f32_e32 v15, v18, v12
	s_waitcnt lgkmcnt(8)
	v_lshlrev_b32_e32 v34, 16, v35
	v_mul_f32_e32 v15, v15, v14
	v_mul_f32_e32 v34, 0x3db504f3, v34
	v_mul_f32_e32 v14, v18, v14
	v_sub_f32_e32 v18, v45, v52
	v_mul_f32_e32 v33, v33, v34
	v_exp_f32_e32 v18, v18
	v_cvt_pk_bf16_f32 v14, v33, v14
	v_sub_f32_e32 v33, v52, v45
	v_exp_f32_e32 v33, v33
	ds_write_b16 v135, v14
	ds_write_b16_d16_hi v108, v14 offset:30096
	v_lshlrev_b32_e32 v14, 16, v16
	v_mul_f32_e32 v16, v18, v12
	s_waitcnt lgkmcnt(9)
	v_lshlrev_b32_e32 v34, 16, v36
	v_mul_f32_e32 v16, v16, v14
	v_mul_f32_e32 v34, 0x3db504f3, v34
	v_mul_f32_e32 v14, v18, v14
	v_sub_f32_e32 v18, v45, v54
	v_mul_f32_e32 v33, v33, v34
	v_exp_f32_e32 v18, v18
	v_cvt_pk_bf16_f32 v14, v33, v14
	v_sub_f32_e32 v33, v54, v45
	v_exp_f32_e32 v33, v33
	ds_write_b16 v136, v14
	ds_write_b16_d16_hi v108, v14 offset:31136
	v_lshlrev_b32_e32 v14, 16, v17
	v_mul_f32_e32 v17, v18, v12
	s_waitcnt lgkmcnt(10)
	v_lshlrev_b32_e32 v34, 16, v37
	v_mul_f32_e32 v17, v17, v14
	v_mul_f32_e32 v34, 0x3db504f3, v34
	v_mul_f32_e32 v14, v18, v14
	v_mul_f32_e32 v33, v33, v34
	v_cvt_pk_bf16_f32 v14, v33, v14
	ds_write_b16 v137, v14
	ds_write_b16_d16_hi v108, v14 offset:32176
	v_sub_f32_e32 v14, v45, v56
	v_exp_f32_e32 v14, v14
	v_sub_f32_e32 v51, v56, v45
	v_exp_f32_e32 v51, v51
	ds_read_u16 v18, v108 offset:33216
	ds_read_u16 v33, v108 offset:34256
	ds_read_u16 v34, v108 offset:35296
	ds_read_u16 v35, v108 offset:36336
	ds_read_u16 v36, v108 offset:37376
	ds_read_u16 v37, v108 offset:38416
	ds_read_u16 v48, v108 offset:39456
	ds_read_u16 v49, v108 offset:40496
	s_waitcnt lgkmcnt(7)
	v_lshlrev_b32_e32 v18, 16, v18
	v_mul_f32_e32 v50, v14, v12
	v_lshlrev_b32_e32 v38, 16, v38
	v_mul_f32_e32 v50, v50, v18
	v_mul_f32_e32 v38, 0x3db504f3, v38
	v_mul_f32_e32 v14, v14, v18
	v_sub_f32_e32 v18, v45, v59
	v_mul_f32_e32 v38, v51, v38
	v_exp_f32_e32 v18, v18
	v_cvt_pk_bf16_f32 v14, v38, v14
	v_sub_f32_e32 v38, v59, v45
	v_exp_f32_e32 v38, v38
	ds_write_b16 v138, v14
	ds_write_b16_d16_hi v108, v14 offset:33216
	s_waitcnt lgkmcnt(8)
	v_lshlrev_b32_e32 v14, 16, v33
	v_mul_f32_e32 v33, v18, v12
	v_lshlrev_b32_e32 v39, 16, v39
	v_mul_f32_e32 v33, v33, v14
	v_mul_f32_e32 v39, 0x3db504f3, v39
	v_mul_f32_e32 v14, v18, v14
	v_sub_f32_e32 v18, v45, v62
	v_mul_f32_e32 v38, v38, v39
	v_exp_f32_e32 v18, v18
	v_cvt_pk_bf16_f32 v14, v38, v14
	v_sub_f32_e32 v38, v62, v45
	v_exp_f32_e32 v38, v38
	ds_write_b16 v139, v14
	ds_write_b16_d16_hi v108, v14 offset:34256
	s_waitcnt lgkmcnt(9)
	v_lshlrev_b32_e32 v14, 16, v34
	v_mul_f32_e32 v34, v18, v12
	v_lshlrev_b32_e32 v39, 16, v46
	v_mul_f32_e32 v34, v34, v14
	v_mul_f32_e32 v39, 0x3db504f3, v39
	v_mul_f32_e32 v14, v18, v14
	v_sub_f32_e32 v18, v45, v65
	v_mul_f32_e32 v38, v38, v39
	v_exp_f32_e32 v18, v18
	v_cvt_pk_bf16_f32 v14, v38, v14
	v_sub_f32_e32 v38, v65, v45
	v_exp_f32_e32 v38, v38
	ds_write_b16 v140, v14
	ds_write_b16_d16_hi v108, v14 offset:35296
	s_waitcnt lgkmcnt(10)
	v_lshlrev_b32_e32 v14, 16, v35
	v_mul_f32_e32 v35, v18, v12
	v_lshlrev_b32_e32 v39, 16, v47
	v_mul_f32_e32 v35, v35, v14
	v_mul_f32_e32 v39, 0x3db504f3, v39
	v_mul_f32_e32 v14, v18, v14
	v_mul_f32_e32 v38, v38, v39
	v_cvt_pk_bf16_f32 v14, v38, v14
	ds_write_b16 v141, v14
	ds_write_b16_d16_hi v108, v14 offset:36336
	v_cvt_pk_bf16_f32 v14, v23, v15
	v_cvt_pk_bf16_f32 v15, v16, v17
	v_sub_f32_e32 v17, v45, v45
	v_exp_f32_e32 v18, v17
	v_cvt_pk_bf16_f32 v16, v50, v33
	v_cvt_pk_bf16_f32 v17, v34, v35
	global_store_dwordx4 v[8:9], v[14:17], off offset:48
	v_sub_f32_e32 v51, v204, v45
	v_exp_f32_e32 v51, v51
	s_waitcnt lgkmcnt(11)
	v_lshlrev_b32_e32 v14, 16, v36
	ds_read_u16 v16, v142
	ds_read_u16 v17, v143
	ds_read_u16 v23, v144
	ds_read_u16 v33, v145
	ds_read_u16 v34, v146
	ds_read_u16 v35, v147
	ds_read_u16 v36, v148
	ds_read_u16 v38, v149
	s_waitcnt lgkmcnt(7)
	v_lshlrev_b32_e32 v16, 16, v16
	v_mul_f32_e32 v15, v18, v12
	v_mul_f32_e32 v16, 0x3db504f3, v16
	v_mul_f32_e32 v15, v15, v14
	v_mul_f32_e32 v16, v18, v16
	v_mul_f32_e32 v14, v18, v14
	v_cvt_pk_bf16_f32 v14, v16, v14
	v_sub_f32_e32 v16, v45, v195
	v_exp_f32_e32 v16, v16
	ds_write_b16 v142, v14
	ds_write_b16_d16_hi v108, v14 offset:37376
	v_lshlrev_b32_e32 v14, 16, v37
	v_sub_f32_e32 v37, v195, v45
	v_mul_f32_e32 v18, v16, v12
	v_exp_f32_e32 v37, v37
	v_mul_f32_e32 v18, v18, v14
	v_mul_f32_e32 v14, v16, v14
	v_sub_f32_e32 v16, v45, v198
	s_waitcnt lgkmcnt(8)
; __device__ __forceinline__ unsigned cvtpk_bf16(float lo, float hi) { unsigned r; asm("v_cvt_pk_bf16_f32 %0, %1, %2" : "=v"(r) : "v"(lo), "v"(hi)); return r; }
; __device__ __forceinline__ void prep_item(const Args& a, LAS unsigned char* lds, int tid, int dir, int b, int ch) {
;     ...
;     for (int i0 = 0; i0 < 64; i0 += 8) { float kd[8];
; #pragma unroll
;         for (int ii = 0; ii < 8; ++ii) { const int i = i0 + ii; const float kv = bf1(Kt[i * TS + col]);
;             if (lat) { const float em = __builtin_amdgcn_exp2f(Gmid - Gv[i]); kd[ii] = kv * (em * eEM);
;                 const float qv = bf1(Qt[i * TS + col]) * 0.08838834764831845f;
;                 const unsigned qk = cvtpk_bf16(qv * __builtin_amdgcn_exp2f(Gv[i] - Gmid), kv * em);
;                 Qt[i * TS + col] = (bf16)(qk & 0xffffu); Kt[i * TS + col] = (bf16)(qk >> 16); }
;             else kd[ii] = kv * __builtin_amdgcn_exp2f(Gend - Gv[i]); }
;         v4u o; o.x = cvtpk_bf16(kd[0], kd[1]); o.y = cvtpk_bf16(kd[2], kd[3]); o.z = cvtpk_bf16(kd[4], kd[5]); o.w = cvtpk_bf16(kd[6], kd[7]);
;         *(v4u*)(kdrow + i0) = o; }
	v_lshlrev_b32_e32 v17, 16, v17
	v_exp_f32_e32 v16, v16
	v_mul_f32_e32 v17, 0x3db504f3, v17
	v_mul_f32_e32 v17, v37, v17
	v_sub_f32_e32 v37, v198, v45
	v_cvt_pk_bf16_f32 v14, v17, v14
	v_exp_f32_e32 v37, v37
	ds_write_b16 v143, v14
	ds_write_b16_d16_hi v108, v14 offset:38416
	v_lshlrev_b32_e32 v14, 16, v48
	v_mul_f32_e32 v17, v16, v12
	v_mul_f32_e32 v17, v17, v14
	s_waitcnt lgkmcnt(9)
	v_lshlrev_b32_e32 v23, 16, v23
	v_mul_f32_e32 v14, v16, v14
	v_sub_f32_e32 v16, v45, v201
	v_mul_f32_e32 v23, 0x3db504f3, v23
	v_exp_f32_e32 v16, v16
	v_mul_f32_e32 v23, v37, v23
	v_sub_f32_e32 v37, v201, v45
	v_exp_f32_e32 v37, v37
	v_cvt_pk_bf16_f32 v14, v23, v14
	ds_write_b16 v144, v14
	ds_write_b16_d16_hi v108, v14 offset:39456
	v_lshlrev_b32_e32 v14, 16, v49
	v_mul_f32_e32 v23, v16, v12
	s_waitcnt lgkmcnt(10)
	v_lshlrev_b32_e32 v33, 16, v33
	v_mul_f32_e32 v23, v23, v14
	v_mul_f32_e32 v33, 0x3db504f3, v33
	v_mul_f32_e32 v14, v16, v14
	v_mul_f32_e32 v33, v37, v33
	v_cvt_pk_bf16_f32 v14, v33, v14
	ds_write_b16 v145, v14
	ds_write_b16_d16_hi v108, v14 offset:40496
	v_sub_f32_e32 v14, v45, v204
	v_exp_f32_e32 v14, v14
	ds_read_u16 v16, v108 offset:41536
	ds_read_u16 v33, v108 offset:42576
	ds_read_u16 v37, v108 offset:43616
	ds_read_u16 v39, v108 offset:44656
	ds_read_u16 v46, v108 offset:45696
	ds_read_u16 v47, v108 offset:46736
	ds_read_u16 v48, v108 offset:47776
	ds_read_u16 v49, v108 offset:48816
	s_waitcnt lgkmcnt(7)
	v_lshlrev_b32_e32 v16, 16, v16
	v_lshlrev_b32_e32 v34, 16, v34
	v_mul_f32_e32 v50, v14, v12
	v_mul_f32_e32 v50, v50, v16
	v_mul_f32_e32 v14, v14, v16
	v_sub_f32_e32 v16, v45, v206
	v_exp_f32_e32 v16, v16
	v_mul_f32_e32 v34, 0x3db504f3, v34
	v_mul_f32_e32 v34, v51, v34
	v_cvt_pk_bf16_f32 v14, v34, v14
	v_sub_f32_e32 v34, v206, v45
	ds_write_b16 v146, v14
	ds_write_b16_d16_hi v108, v14 offset:41536
	s_waitcnt lgkmcnt(8)
	v_lshlrev_b32_e32 v14, 16, v33
	v_mul_f32_e32 v33, v16, v12
	v_exp_f32_e32 v34, v34
	v_mul_f32_e32 v33, v33, v14
	v_mul_f32_e32 v14, v16, v14
	v_sub_f32_e32 v16, v45, v208
	v_lshlrev_b32_e32 v35, 16, v35
	v_exp_f32_e32 v16, v16
	v_mul_f32_e32 v35, 0x3db504f3, v35
	v_mul_f32_e32 v34, v34, v35
	v_sub_f32_e32 v35, v208, v45
	v_cvt_pk_bf16_f32 v14, v34, v14
	v_exp_f32_e32 v35, v35
	ds_write_b16 v147, v14
	ds_write_b16_d16_hi v108, v14 offset:42576
	s_waitcnt lgkmcnt(9)
	v_lshlrev_b32_e32 v14, 16, v37
	v_mul_f32_e32 v34, v16, v12
	v_mul_f32_e32 v34, v34, v14
	v_lshlrev_b32_e32 v36, 16, v36
	v_mul_f32_e32 v14, v16, v14
	v_sub_f32_e32 v16, v45, v210
	v_mul_f32_e32 v36, 0x3db504f3, v36
	v_exp_f32_e32 v16, v16
	v_mul_f32_e32 v35, v35, v36
	v_sub_f32_e32 v36, v210, v45
	v_exp_f32_e32 v36, v36
	v_cvt_pk_bf16_f32 v14, v35, v14
	ds_write_b16 v148, v14
	ds_write_b16_d16_hi v108, v14 offset:43616
	s_waitcnt lgkmcnt(10)
	v_lshlrev_b32_e32 v14, 16, v39
	v_mul_f32_e32 v35, v16, v12
	v_lshlrev_b32_e32 v37, 16, v38
	v_mul_f32_e32 v35, v35, v14
	v_mul_f32_e32 v37, 0x3db504f3, v37
	v_mul_f32_e32 v14, v16, v14
	v_mul_f32_e32 v36, v36, v37
	v_cvt_pk_bf16_f32 v14, v36, v14
	ds_write_b16 v149, v14
	ds_write_b16_d16_hi v108, v14 offset:44656
	v_cvt_pk_bf16_f32 v14, v15, v18
	v_cvt_pk_bf16_f32 v15, v17, v23
	v_cvt_pk_bf16_f32 v16, v50, v33
	v_sub_f32_e32 v17, v45, v212
	v_exp_f32_e32 v18, v17
	v_cvt_pk_bf16_f32 v17, v34, v35
	global_store_dwordx4 v[8:9], v[14:17], off offset:64
	ds_read_u16 v17, v150
	ds_read_u16 v23, v151
	ds_read_u16 v33, v152
	ds_read_u16 v34, v153
	ds_read_u16 v35, v154
	ds_read_u16 v36, v155
	ds_read_u16 v37, v156
	ds_read_u16 v38, v157
	v_sub_f32_e32 v16, v212, v45
	v_exp_f32_e32 v16, v16
	s_waitcnt lgkmcnt(7)
	v_lshlrev_b32_e32 v17, 16, v17
	v_lshlrev_b32_e32 v14, 16, v46
	v_mul_f32_e32 v15, v18, v12
	v_mul_f32_e32 v17, 0x3db504f3, v17
	v_mul_f32_e32 v15, v15, v14
	v_mul_f32_e32 v16, v16, v17
	v_mul_f32_e32 v14, v18, v14
	v_cvt_pk_bf16_f32 v14, v16, v14
	v_sub_f32_e32 v16, v45, v214
	v_exp_f32_e32 v16, v16
	v_sub_f32_e32 v18, v214, v45
	ds_write_b16 v150, v14
	ds_write_b16_d16_hi v108, v14 offset:45696
	v_lshlrev_b32_e32 v14, 16, v47
	v_mul_f32_e32 v17, v16, v12
	v_exp_f32_e32 v18, v18
	v_mul_f32_e32 v17, v17, v14
	v_mul_f32_e32 v14, v16, v14
	v_sub_f32_e32 v16, v45, v215
	s_waitcnt lgkmcnt(8)
	v_lshlrev_b32_e32 v23, 16, v23
	v_exp_f32_e32 v16, v16
	v_mul_f32_e32 v23, 0x3db504f3, v23
	v_mul_f32_e32 v18, v18, v23
	v_sub_f32_e32 v23, v215, v45
	v_cvt_pk_bf16_f32 v14, v18, v14
	v_exp_f32_e32 v23, v23
	ds_write_b16 v151, v14
	ds_write_b16_d16_hi v108, v14 offset:46736
	v_lshlrev_b32_e32 v14, 16, v48
	v_mul_f32_e32 v18, v16, v12
	v_mul_f32_e32 v18, v18, v14
	s_waitcnt lgkmcnt(9)
	v_lshlrev_b32_e32 v33, 16, v33
	v_mul_f32_e32 v14, v16, v14
	v_sub_f32_e32 v16, v45, v216
	v_mul_f32_e32 v33, 0x3db504f3, v33
	v_exp_f32_e32 v16, v16
	v_mul_f32_e32 v23, v23, v33
	v_sub_f32_e32 v33, v216, v45
	v_exp_f32_e32 v33, v33
	v_cvt_pk_bf16_f32 v14, v23, v14
	ds_write_b16 v152, v14
	ds_write_b16_d16_hi v108, v14 offset:47776
	v_lshlrev_b32_e32 v14, 16, v49
	v_mul_f32_e32 v23, v16, v12
	s_waitcnt lgkmcnt(10)
	v_lshlrev_b32_e32 v34, 16, v34
	v_mul_f32_e32 v23, v23, v14
	v_mul_f32_e32 v34, 0x3db504f3, v34
	v_mul_f32_e32 v14, v16, v14
	v_mul_f32_e32 v33, v33, v34
	v_cvt_pk_bf16_f32 v14, v33, v14
	ds_write_b16 v153, v14
	ds_write_b16_d16_hi v108, v14 offset:48816
	v_sub_f32_e32 v14, v45, v217
	v_exp_f32_e32 v14, v14
	v_sub_f32_e32 v51, v217, v45
	ds_read_u16 v16, v108 offset:49856
	ds_read_u16 v33, v108 offset:50896
	ds_read_u16 v34, v108 offset:51936
	ds_read_u16 v39, v108 offset:52976
	ds_read_u16 v46, v108 offset:54016
	ds_read_u16 v47, v108 offset:55056
	ds_read_u16 v48, v108 offset:56096
	ds_read_u16 v49, v108 offset:57136
	v_exp_f32_e32 v51, v51
	s_waitcnt lgkmcnt(7)
; __device__ __forceinline__ unsigned cvtpk_bf16(float lo, float hi) { unsigned r; asm("v_cvt_pk_bf16_f32 %0, %1, %2" : "=v"(r) : "v"(lo), "v"(hi)); return r; }
; __device__ __forceinline__ void prep_item(const Args& a, LAS unsigned char* lds, int tid, int dir, int b, int ch) {
;     ...
;     for (int i0 = 0; i0 < 64; i0 += 8) { float kd[8];
; #pragma unroll
;         for (int ii = 0; ii < 8; ++ii) { const int i = i0 + ii; const float kv = bf1(Kt[i * TS + col]);
;             if (lat) { const float em = __builtin_amdgcn_exp2f(Gmid - Gv[i]); kd[ii] = kv * (em * eEM);
;                 const float qv = bf1(Qt[i * TS + col]) * 0.08838834764831845f;
;                 const unsigned qk = cvtpk_bf16(qv * __builtin_amdgcn_exp2f(Gv[i] - Gmid), kv * em);
;                 Qt[i * TS + col] = (bf16)(qk & 0xffffu); Kt[i * TS + col] = (bf16)(qk >> 16); }
;             else kd[ii] = kv * __builtin_amdgcn_exp2f(Gend - Gv[i]); }
;         v4u o; o.x = cvtpk_bf16(kd[0], kd[1]); o.y = cvtpk_bf16(kd[2], kd[3]); o.z = cvtpk_bf16(kd[4], kd[5]); o.w = cvtpk_bf16(kd[6], kd[7]);
;         *(v4u*)(kdrow + i0) = o; }
	v_lshlrev_b32_e32 v16, 16, v16
	v_mul_f32_e32 v50, v14, v12
	v_mul_f32_e32 v50, v50, v16
	v_lshlrev_b32_e32 v35, 16, v35
	v_mul_f32_e32 v14, v14, v16
	v_sub_f32_e32 v16, v45, v218
	v_mul_f32_e32 v35, 0x3db504f3, v35
	v_exp_f32_e32 v16, v16
	v_mul_f32_e32 v35, v51, v35
	v_cvt_pk_bf16_f32 v14, v35, v14
	v_sub_f32_e32 v35, v218, v45
	v_exp_f32_e32 v35, v35
	ds_write_b16 v154, v14
	ds_write_b16_d16_hi v108, v14 offset:49856
	s_waitcnt lgkmcnt(8)
	v_lshlrev_b32_e32 v14, 16, v33
	v_mul_f32_e32 v33, v16, v12
	v_mul_f32_e32 v33, v33, v14
	v_lshlrev_b32_e32 v36, 16, v36
	v_mul_f32_e32 v14, v16, v14
	v_sub_f32_e32 v16, v45, v219
	v_mul_f32_e32 v36, 0x3db504f3, v36
	v_exp_f32_e32 v16, v16
	v_mul_f32_e32 v35, v35, v36
	v_cvt_pk_bf16_f32 v14, v35, v14
	v_sub_f32_e32 v35, v219, v45
	v_exp_f32_e32 v35, v35
	ds_write_b16 v155, v14
	ds_write_b16_d16_hi v108, v14 offset:50896
	s_waitcnt lgkmcnt(9)
	v_lshlrev_b32_e32 v14, 16, v34
	v_mul_f32_e32 v34, v16, v12
	v_mul_f32_e32 v34, v34, v14
	v_lshlrev_b32_e32 v36, 16, v37
	v_mul_f32_e32 v14, v16, v14
	v_sub_f32_e32 v16, v45, v220
	v_mul_f32_e32 v36, 0x3db504f3, v36
	v_exp_f32_e32 v16, v16
	v_mul_f32_e32 v35, v35, v36
	v_sub_f32_e32 v36, v220, v45
	v_exp_f32_e32 v36, v36
	v_cvt_pk_bf16_f32 v14, v35, v14
	ds_write_b16 v156, v14
	ds_write_b16_d16_hi v108, v14 offset:51936
	s_waitcnt lgkmcnt(10)
	v_lshlrev_b32_e32 v14, 16, v39
	v_mul_f32_e32 v35, v16, v12
	v_lshlrev_b32_e32 v37, 16, v38
	v_mul_f32_e32 v35, v35, v14
	v_mul_f32_e32 v37, 0x3db504f3, v37
	v_mul_f32_e32 v14, v16, v14
	v_mul_f32_e32 v36, v36, v37
	v_cvt_pk_bf16_f32 v14, v36, v14
	ds_write_b16 v157, v14
	ds_write_b16_d16_hi v108, v14 offset:52976
	v_cvt_pk_bf16_f32 v14, v15, v17
	v_cvt_pk_bf16_f32 v16, v50, v33
	v_sub_f32_e32 v17, v45, v221
	v_cvt_pk_bf16_f32 v15, v18, v23
	v_exp_f32_e32 v18, v17
	v_cvt_pk_bf16_f32 v17, v34, v35
	global_store_dwordx4 v[8:9], v[14:17], off offset:80
	ds_read_u16 v17, v158
	ds_read_u16 v23, v159
	ds_read_u16 v33, v160
	ds_read_u16 v34, v161
	ds_read_u16 v35, v162
	ds_read_u16 v36, v163
	ds_read_u16 v37, v164
	ds_read_u16 v38, v165
	v_sub_f32_e32 v16, v221, v45
	v_exp_f32_e32 v16, v16
	s_waitcnt lgkmcnt(7)
	v_lshlrev_b32_e32 v17, 16, v17
	v_lshlrev_b32_e32 v14, 16, v46
	v_mul_f32_e32 v15, v18, v12
	v_mul_f32_e32 v17, 0x3db504f3, v17
	v_mul_f32_e32 v15, v15, v14
	v_mul_f32_e32 v16, v16, v17
	v_mul_f32_e32 v14, v18, v14
	v_cvt_pk_bf16_f32 v14, v16, v14
	v_sub_f32_e32 v16, v45, v222
	v_exp_f32_e32 v16, v16
	v_sub_f32_e32 v18, v222, v45
	ds_write_b16 v158, v14
	ds_write_b16_d16_hi v108, v14 offset:54016
	v_lshlrev_b32_e32 v14, 16, v47
	v_mul_f32_e32 v17, v16, v12
	v_exp_f32_e32 v18, v18
	v_mul_f32_e32 v17, v17, v14
	v_mul_f32_e32 v14, v16, v14
	v_sub_f32_e32 v16, v45, v223
	s_waitcnt lgkmcnt(8)
	v_lshlrev_b32_e32 v23, 16, v23
	v_exp_f32_e32 v16, v16
	v_mul_f32_e32 v23, 0x3db504f3, v23
	v_mul_f32_e32 v18, v18, v23
	v_sub_f32_e32 v23, v223, v45
	v_cvt_pk_bf16_f32 v14, v18, v14
	v_exp_f32_e32 v23, v23
	ds_write_b16 v159, v14
	ds_write_b16_d16_hi v108, v14 offset:55056
	v_lshlrev_b32_e32 v14, 16, v48
	v_mul_f32_e32 v18, v16, v12
	v_mul_f32_e32 v18, v18, v14
	s_waitcnt lgkmcnt(9)
	v_lshlrev_b32_e32 v33, 16, v33
	v_mul_f32_e32 v14, v16, v14
	v_sub_f32_e32 v16, v45, v224
	v_mul_f32_e32 v33, 0x3db504f3, v33
	v_exp_f32_e32 v16, v16
	v_mul_f32_e32 v23, v23, v33
	v_sub_f32_e32 v33, v224, v45
	v_exp_f32_e32 v33, v33
	v_cvt_pk_bf16_f32 v14, v23, v14
	ds_write_b16 v160, v14
	ds_write_b16_d16_hi v108, v14 offset:56096
	v_lshlrev_b32_e32 v14, 16, v49
	v_mul_f32_e32 v23, v16, v12
	s_waitcnt lgkmcnt(10)
	v_lshlrev_b32_e32 v34, 16, v34
	v_mul_f32_e32 v23, v23, v14
	v_mul_f32_e32 v34, 0x3db504f3, v34
	v_mul_f32_e32 v14, v16, v14
	v_mul_f32_e32 v33, v33, v34
	v_cvt_pk_bf16_f32 v14, v33, v14
	ds_write_b16 v161, v14
	ds_write_b16_d16_hi v108, v14 offset:57136
	v_sub_f32_e32 v14, v45, v24
	v_exp_f32_e32 v14, v14
	ds_read_u16 v16, v108 offset:58176
	ds_read_u16 v33, v108 offset:59216
	ds_read_u16 v34, v108 offset:60256
	ds_read_u16 v39, v108 offset:61296
	ds_read_u16 v46, v108 offset:62336
	ds_read_u16 v47, v108 offset:63376
	ds_read_u16 v48, v108 offset:64416
	ds_read_u16 v49, v108 offset:65456
	s_waitcnt lgkmcnt(7)
	v_lshlrev_b32_e32 v16, 16, v16
	v_sub_f32_e32 v24, v24, v45
	v_mul_f32_e32 v50, v14, v12
	v_exp_f32_e32 v24, v24
	v_mul_f32_e32 v50, v50, v16
	v_mul_f32_e32 v14, v14, v16
	v_sub_f32_e32 v16, v45, v25
	v_exp_f32_e32 v16, v16
	v_lshlrev_b32_e32 v35, 16, v35
	v_mul_f32_e32 v35, 0x3db504f3, v35
	v_mul_f32_e32 v24, v24, v35
	v_cvt_pk_bf16_f32 v14, v24, v14
	ds_write_b16 v162, v14
	ds_write_b16_d16_hi v108, v14 offset:58176
	s_waitcnt lgkmcnt(8)
	v_lshlrev_b32_e32 v14, 16, v33
	v_mul_f32_e32 v24, v16, v12
	v_sub_f32_e32 v25, v25, v45
	v_exp_f32_e32 v25, v25
	v_mul_f32_e32 v24, v24, v14
	v_mul_f32_e32 v14, v16, v14
	v_sub_f32_e32 v16, v45, v26
	v_exp_f32_e32 v16, v16
	v_lshlrev_b32_e32 v33, 16, v36
	v_mul_f32_e32 v33, 0x3db504f3, v33
	v_mul_f32_e32 v25, v25, v33
	v_cvt_pk_bf16_f32 v14, v25, v14
	ds_write_b16 v163, v14
	ds_write_b16_d16_hi v108, v14 offset:59216
	s_waitcnt lgkmcnt(9)
	v_lshlrev_b32_e32 v14, 16, v34
	v_mul_f32_e32 v25, v16, v12
	v_sub_f32_e32 v26, v26, v45
	v_exp_f32_e32 v26, v26
	v_mul_f32_e32 v25, v25, v14
	v_mul_f32_e32 v14, v16, v14
	v_sub_f32_e32 v16, v45, v27
	v_exp_f32_e32 v16, v16
	v_lshlrev_b32_e32 v33, 16, v37
	v_sub_f32_e32 v27, v27, v45
	v_mul_f32_e32 v33, 0x3db504f3, v33
	v_exp_f32_e32 v27, v27
	v_mul_f32_e32 v26, v26, v33
	v_cvt_pk_bf16_f32 v14, v26, v14
	ds_write_b16 v164, v14
	ds_write_b16_d16_hi v108, v14 offset:60256
	s_waitcnt lgkmcnt(10)
; #define LDS_BARRIER() do { asm volatile("s_waitcnt lgkmcnt(0)" ::: "memory"); __builtin_amdgcn_s_barrier(); asm volatile("" ::: "memory"); } while (0)
; __device__ __forceinline__ unsigned cvtpk_bf16(float lo, float hi) { unsigned r; asm("v_cvt_pk_bf16_f32 %0, %1, %2" : "=v"(r) : "v"(lo), "v"(hi)); return r; }
; __device__ __forceinline__ void prep_item(const Args& a, LAS unsigned char* lds, int tid, int dir, int b, int ch) {
;     ...
;     for (int i0 = 0; i0 < 64; i0 += 8) { float kd[8];
; #pragma unroll
;         for (int ii = 0; ii < 8; ++ii) { const int i = i0 + ii; const float kv = bf1(Kt[i * TS + col]);
;             if (lat) { const float em = __builtin_amdgcn_exp2f(Gmid - Gv[i]); kd[ii] = kv * (em * eEM);
;                 const float qv = bf1(Qt[i * TS + col]) * 0.08838834764831845f;
;                 const unsigned qk = cvtpk_bf16(qv * __builtin_amdgcn_exp2f(Gv[i] - Gmid), kv * em);
;                 Qt[i * TS + col] = (bf16)(qk & 0xffffu); Kt[i * TS + col] = (bf16)(qk >> 16); }
;             else kd[ii] = kv * __builtin_amdgcn_exp2f(Gend - Gv[i]); }
;         v4u o; o.x = cvtpk_bf16(kd[0], kd[1]); o.y = cvtpk_bf16(kd[2], kd[3]); o.z = cvtpk_bf16(kd[4], kd[5]); o.w = cvtpk_bf16(kd[6], kd[7]);
;         *(v4u*)(kdrow + i0) = o; }
;     if (lat) {
;         LDS_BARRIER();
	v_lshlrev_b32_e32 v14, 16, v39
	v_mul_f32_e32 v26, v16, v12
	v_lshlrev_b32_e32 v33, 16, v38
	v_mul_f32_e32 v26, v26, v14
	v_mul_f32_e32 v33, 0x3db504f3, v33
	v_mul_f32_e32 v14, v16, v14
	v_mul_f32_e32 v27, v27, v33
	v_cvt_pk_bf16_f32 v14, v27, v14
	ds_write_b16 v165, v14
	ds_write_b16_d16_hi v108, v14 offset:61296
	v_cvt_pk_bf16_f32 v14, v15, v17
	v_cvt_pk_bf16_f32 v16, v50, v24
	v_sub_f32_e32 v17, v45, v28
	v_cvt_pk_bf16_f32 v15, v18, v23
	v_exp_f32_e32 v18, v17
	v_cvt_pk_bf16_f32 v17, v25, v26
	global_store_dwordx4 v[8:9], v[14:17], off offset:96
	v_sub_f32_e32 v10, v45, v10
	s_ashr_i32 s2, s8, 7
	v_sub_f32_e32 v16, v28, v45
	v_exp_f32_e32 v16, v16
	ds_read_u16 v17, v166
	ds_read_u16 v23, v167
	ds_read_u16 v24, v168
	ds_read_u16 v25, v169
	ds_read_u16 v26, v170
	ds_read_u16 v27, v171
	ds_read_u16 v28, v172
	ds_read_u16 v33, v173
	s_waitcnt lgkmcnt(7)
	v_lshlrev_b32_e32 v17, 16, v17
	v_lshlrev_b32_e32 v14, 16, v46
	v_mul_f32_e32 v15, v18, v12
	v_mul_f32_e32 v17, 0x3db504f3, v17
	v_mul_f32_e32 v15, v15, v14
	v_mul_f32_e32 v16, v16, v17
	v_mul_f32_e32 v14, v18, v14
	v_cvt_pk_bf16_f32 v14, v16, v14
	v_sub_f32_e32 v16, v45, v29
	v_exp_f32_e32 v16, v16
	ds_write_b16 v166, v14
	ds_write_b16_d16_hi v108, v14 offset:62336
	v_lshlrev_b32_e32 v14, 16, v47
	v_sub_f32_e32 v18, v29, v45
	v_mul_f32_e32 v17, v16, v12
	v_exp_f32_e32 v18, v18
	v_mul_f32_e32 v17, v17, v14
	v_mul_f32_e32 v14, v16, v14
	v_sub_f32_e32 v16, v45, v30
	v_exp_f32_e32 v16, v16
	s_waitcnt lgkmcnt(8)
	v_lshlrev_b32_e32 v23, 16, v23
	v_mul_f32_e32 v23, 0x3db504f3, v23
	v_mul_f32_e32 v18, v18, v23
	v_cvt_pk_bf16_f32 v14, v18, v14
	ds_write_b16 v167, v14
	ds_write_b16_d16_hi v108, v14 offset:63376
	v_lshlrev_b32_e32 v14, 16, v48
	v_mul_f32_e32 v18, v16, v12
	v_sub_f32_e32 v23, v30, v45
	v_exp_f32_e32 v23, v23
	v_mul_f32_e32 v18, v18, v14
	v_mul_f32_e32 v14, v16, v14
	v_sub_f32_e32 v16, v45, v31
	v_exp_f32_e32 v16, v16
	s_waitcnt lgkmcnt(9)
	v_lshlrev_b32_e32 v24, 16, v24
	v_mul_f32_e32 v24, 0x3db504f3, v24
	v_mul_f32_e32 v23, v23, v24
	v_cvt_pk_bf16_f32 v14, v23, v14
	v_sub_f32_e32 v24, v31, v45
	ds_write_b16 v168, v14
	ds_write_b16_d16_hi v108, v14 offset:64416
	v_lshlrev_b32_e32 v14, 16, v49
	v_mul_f32_e32 v23, v16, v12
	v_exp_f32_e32 v24, v24
	v_mul_f32_e32 v23, v23, v14
	v_mul_f32_e32 v14, v16, v14
	v_sub_f32_e32 v16, v45, v32
	s_waitcnt lgkmcnt(10)
	v_lshlrev_b32_e32 v25, 16, v25
	v_exp_f32_e32 v16, v16
	v_mul_f32_e32 v25, 0x3db504f3, v25
	v_mul_f32_e32 v24, v24, v25
	v_cvt_pk_bf16_f32 v14, v24, v14
	v_sub_f32_e32 v24, v32, v45
	ds_write_b16 v169, v14
	ds_write_b16_d16_hi v108, v14 offset:65456
	v_lshlrev_b32_e32 v14, 16, v19
	v_mul_f32_e32 v19, v16, v12
	v_exp_f32_e32 v24, v24
	v_mul_f32_e32 v19, v19, v14
	v_mul_f32_e32 v14, v16, v14
	v_sub_f32_e32 v16, v45, v13
	s_waitcnt lgkmcnt(11)
	v_lshlrev_b32_e32 v25, 16, v26
	v_exp_f32_e32 v16, v16
	v_sub_f32_e32 v13, v13, v45
	v_mul_f32_e32 v25, 0x3db504f3, v25
	v_exp_f32_e32 v13, v13
	v_mul_f32_e32 v24, v24, v25
	v_cvt_pk_bf16_f32 v14, v24, v14
	s_waitcnt lgkmcnt(10)
	v_lshlrev_b32_e32 v24, 16, v27
	ds_write_b16 v170, v14
	ds_write_b16_d16_hi v109, v14 offset:62400
	v_lshlrev_b32_e32 v14, 16, v20
	v_mul_f32_e32 v20, v16, v12
	v_mul_f32_e32 v24, 0x3db504f3, v24
	v_mul_f32_e32 v20, v20, v14
	v_mul_f32_e32 v13, v13, v24
	v_mul_f32_e32 v14, v16, v14
	v_cvt_pk_bf16_f32 v13, v13, v14
	v_sub_f32_e32 v14, v45, v11
	v_sub_f32_e32 v11, v11, v45
	v_exp_f32_e32 v14, v14
	v_exp_f32_e32 v11, v11
	ds_write_b16 v171, v13
	ds_write_b16_d16_hi v109, v13 offset:63440
	v_lshlrev_b32_e32 v13, 16, v21
	s_waitcnt lgkmcnt(13)
	v_lshlrev_b32_e32 v21, 16, v28
	s_lshl_b32 s3, s9, 2
	v_mul_f32_e32 v21, 0x3db504f3, v21
	v_exp_f32_e32 v10, v10
	s_or_b32 s16, s16, s3
	s_ashr_i32 s3, s2, 31
	v_mul_f32_e32 v16, v14, v12
	v_mul_f32_e32 v11, v11, v21
	s_add_u32 s2, s16, s2
	v_mul_f32_e32 v16, v16, v13
	v_mul_f32_e32 v13, v14, v13
	v_cvt_pk_bf16_f32 v11, v11, v13
	s_addc_u32 s3, s17, s3
	ds_write_b16 v172, v11
	ds_write_b16_d16_hi v109, v11 offset:64480
	v_lshlrev_b32_e32 v11, 16, v22
	s_waitcnt lgkmcnt(14)
	v_lshlrev_b32_e32 v14, 16, v33
	s_lshl_b64 s[2:3], s[2:3], 13
	v_mul_f32_e32 v13, v12, v10
	v_mul_f32_e32 v14, 0x3db504f3, v14
	v_mul_f32_e32 v10, v10, v11
	s_add_u32 s18, s25, s2
	v_mul_f32_e32 v13, v13, v11
	v_mul_f32_e32 v12, v12, v14
	v_cvt_pk_bf16_f32 v10, v12, v10
	s_addc_u32 s19, s26, s3
	s_and_b32 s2, s8, 0x7fffff80
	ds_write_b16 v173, v10
	ds_write_b16_d16_hi v109, v10 offset:65520
	v_cvt_pk_bf16_f32 v10, v15, v17
	v_cvt_pk_bf16_f32 v11, v18, v23
	v_cvt_pk_bf16_f32 v12, v19, v20
	v_cvt_pk_bf16_f32 v13, v16, v13
	global_store_dwordx4 v[8:9], v[10:13], off offset:112
	v_or_b32_e32 v8, s2, v174
	v_lshlrev_b32_e32 v195, 1, v8
	s_waitcnt lgkmcnt(0)
	s_barrier
; #define LAS __attribute__((address_space(3)))
; __device__ __forceinline__ unsigned pk2(float lo, float hi) { return f2bf(lo) | (f2bf(hi) << 16); }
; __device__ __forceinline__ void prep_item(const Args& a, LAS unsigned char* lds, int tid, int dir, int b, int ch) {
;     ...
;         const int hh = wave >> 1; bf16* amt = AM + ((((size_t)(dir * 8 + b) * 32 + (ch - 4)) * 4 + hh) * 64) * 64;
; #pragma unroll
;         for (int t2 = 0; t2 < 2; ++t2) { const int ti = (wave & 1) * 2 + t2; f32x4 c[4];
; #pragma unroll
;             for (int tj = 0; tj < 4; ++tj) c[tj] = (f32x4){0.f, 0.f, 0.f, 0.f};
; #pragma unroll
;             for (int ks = 0; ks < 4; ++ks) { const int ko = hh * 128 + 32 * ks + 8 * l4;
;                 const bf16x8 bq = *(const LAS bf16x8*)(Qt + (16 * ti + l15) * TS + ko);
; #pragma unroll
;                 for (int tj = 0; tj < 4; ++tj) { const bf16x8 ak = *(const LAS bf16x8*)(Kt + (16 * tj + l15) * TS + ko);
;                     c[tj] = __builtin_amdgcn_mfma_f32_16x16x32_bf16(ak, bq, c[tj], 0, 0, 0); } }
;             const int i = 16 * ti + l15;
; #pragma unroll
;             for (int tj = 0; tj < 4; ++tj) { const int j0 = 16 * tj + 4 * l4;
;                 v2u p; p.x = pk2(j0 <= i ? c[tj][0] : 0.f, j0 + 1 <= i ? c[tj][1] : 0.f); p.y = pk2(j0 + 2 <= i ? c[tj][2] : 0.f, j0 + 3 <= i ? c[tj][3] : 0.f);
;                 *(v2u*)(amt + i * 64 + j0) = p; } }
	v_add_u32_e32 v216, v41, v195
	ds_read_b128 v[8:11], v216 offset:4096
	s_lshr_b32 s2, s8, 1
	v_and_or_b32 v217, s2, 32, v81
	v_mul_u32_u24_e32 v12, 0x410, v217
	v_add3_u32 v58, s24, v12, v195
	ds_read_b128 v[12:15], v58
	ds_read_b128 v[16:19], v58 offset:64
	ds_read_b128 v[20:23], v216 offset:4160
	ds_read_b128 v[28:31], v216 offset:20736
	ds_read_b128 v[32:35], v216 offset:20800
	ds_read_b128 v[46:49], v216 offset:37376
	ds_read_b128 v[50:53], v216 offset:37440
	ds_read_b128 v[54:57], v216 offset:4224
	s_waitcnt lgkmcnt(7)
	v_mfma_f32_16x16x32_bf16 v[24:27], v[8:11], v[12:15], 0
	v_cmp_gt_u32_e32 vcc, v175, v217
	v_cmp_lt_u32_e64 s[4:5], v175, v217
	v_cmp_le_u32_e64 s[8:9], v176, v217
	s_waitcnt lgkmcnt(4)
	v_mfma_f32_16x16x32_bf16 v[36:39], v[28:31], v[12:15], 0
	v_or_b32_e32 v218, 16, v217
	s_mov_b32 s2, 0
	s_waitcnt lgkmcnt(2)
	v_mfma_f32_16x16x32_bf16 v[12:15], v[46:49], v[12:15], 0
	v_mfma_f32_16x16x32_bf16 v[24:27], v[20:23], v[16:19], v[24:27]
	v_mfma_f32_16x16x32_bf16 v[36:39], v[32:35], v[16:19], v[36:39]
	s_waitcnt lgkmcnt(1)
	v_mfma_f32_16x16x32_bf16 v[12:15], v[50:53], v[16:19], v[12:15]
	ds_read_b128 v[16:19], v58 offset:128
	ds_read_b128 v[58:61], v58 offset:192
	ds_read_b128 v[62:65], v216 offset:4288
	ds_read_b128 v[196:199], v216 offset:20864
	ds_read_b128 v[200:203], v216 offset:20928
	ds_read_b128 v[204:207], v216 offset:37504
	ds_read_b128 v[208:211], v216 offset:37568
	s_waitcnt lgkmcnt(6)
	v_mfma_f32_16x16x32_bf16 v[24:27], v[54:57], v[16:19], v[24:27]
	s_waitcnt lgkmcnt(3)
	v_mfma_f32_16x16x32_bf16 v[36:39], v[196:199], v[16:19], v[36:39]
	s_waitcnt lgkmcnt(1)
	v_mfma_f32_16x16x32_bf16 v[12:15], v[204:207], v[16:19], v[12:15]
	v_mfma_f32_16x16x32_bf16 v[16:19], v[62:65], v[58:61], v[24:27]
	v_mfma_f32_16x16x32_bf16 v[24:27], v[200:203], v[58:61], v[36:39]
	s_waitcnt lgkmcnt(0)
	v_mfma_f32_16x16x32_bf16 v[12:15], v[208:211], v[58:61], v[12:15]
	s_nop 4
	v_cndmask_b32_e64 v16, v16, 0, vcc
	v_cndmask_b32_e64 v17, 0, v17, s[4:5]
	v_bfe_u32 v38, v16, 16, 1
	v_add3_u32 v16, v16, v38, s35
	v_bfe_u32 v38, v17, 16, 1
	v_lshrrev_b32_e32 v16, 16, v16
	v_add3_u32 v17, v17, v38, s35
	v_and_or_b32 v38, v17, s58, v16
	v_cndmask_b32_e64 v16, 0, v18, s[8:9]
	v_cmp_le_u32_e64 s[8:9], v177, v217
	v_bfe_u32 v18, v16, 16, 1
	v_add3_u32 v16, v16, v18, s35
	v_cndmask_b32_e64 v17, 0, v19, s[8:9]
	v_bfe_u32 v18, v17, 16, 1
	v_lshrrev_b32_e32 v16, 16, v16
	v_add3_u32 v17, v17, v18, s35
	v_and_or_b32 v39, v17, s58, v16
	v_mul_u32_u24_e32 v16, 0x410, v218
	v_add3_u32 v195, s24, v16, v195
	ds_read_b128 v[58:61], v216 offset:54016
	ds_read_b128 v[16:19], v195
	v_lshlrev_b32_e32 v36, 7, v217
	v_mov_b32_e32 v37, v69
	v_cmp_le_u32_e64 s[8:9], v178, v217
	v_lshl_add_u64 v[36:37], s[18:19], 0, v[36:37]
	v_lshl_add_u64 v[78:79], v[36:37], 0, v[6:7]
	v_cndmask_b32_e64 v24, 0, v24, s[8:9]
	v_cmp_lt_u32_e64 s[8:9], v178, v217
	v_bfe_u32 v212, v24, 16, 1
	global_store_dwordx2 v[78:79], v[38:39], off
	v_cndmask_b32_e64 v25, 0, v25, s[8:9]
	ds_read_b128 v[36:39], v195 offset:64
	v_add3_u32 v24, v24, v212, s35
	v_bfe_u32 v212, v25, 16, 1
	s_waitcnt lgkmcnt(1)
	v_mfma_f32_16x16x32_bf16 v[8:11], v[8:11], v[16:19], 0
	v_add3_u32 v25, v25, v212, s35
	ds_read_b128 v[212:215], v216 offset:54080
	v_lshrrev_b32_e32 v24, 16, v24
	v_mfma_f32_16x16x32_bf16 v[28:31], v[28:31], v[16:19], 0
	v_cmp_le_u32_e64 s[8:9], v179, v217
	v_mfma_f32_16x16x32_bf16 v[46:49], v[46:49], v[16:19], 0
	v_mfma_f32_16x16x32_bf16 v[16:19], v[58:61], v[16:19], 0
	v_and_or_b32 v58, v25, s58, v24
	v_cndmask_b32_e64 v24, 0, v26, s[8:9]
	v_cmp_le_u32_e64 s[8:9], v180, v217
	s_waitcnt lgkmcnt(1)
	v_mfma_f32_16x16x32_bf16 v[8:11], v[20:23], v[36:39], v[8:11]
	v_bfe_u32 v20, v24, 16, 1
	v_cndmask_b32_e64 v25, 0, v27, s[8:9]
	v_add3_u32 v24, v24, v20, s35
	v_mfma_f32_16x16x32_bf16 v[20:23], v[32:35], v[36:39], v[28:31]
	ds_read_b128 v[32:35], v195 offset:192
	v_cmp_le_u32_e64 s[8:9], v181, v217
	s_nop 0
	v_lshrrev_b32_e32 v28, 16, v24
	v_bfe_u32 v24, v25, 16, 1
	v_add3_u32 v29, v25, v24, s35
	v_and_or_b32 v59, v29, s58, v28
	ds_read_b128 v[28:31], v195 offset:128
	v_mfma_f32_16x16x32_bf16 v[24:27], v[50:53], v[36:39], v[46:49]
	v_cndmask_b32_e64 v12, 0, v12, s[8:9]
	v_cmp_lt_u32_e64 s[8:9], v181, v217
	global_store_dwordx2 v[78:79], v[58:59], off offset:32
	s_waitcnt lgkmcnt(2)
; #define LAS __attribute__((address_space(3)))
; #define LDS_BARRIER() do { asm volatile("s_waitcnt lgkmcnt(0)" ::: "memory"); __builtin_amdgcn_s_barrier(); asm volatile("" ::: "memory"); } while (0)
; __device__ __forceinline__ unsigned pk2(float lo, float hi) { return f2bf(lo) | (f2bf(hi) << 16); }
; __device__ __forceinline__ void prep_item(const Args& a, LAS unsigned char* lds, int tid, int dir, int b, int ch) {
;     ...
;         for (int t2 = 0; t2 < 2; ++t2) { const int ti = (wave & 1) * 2 + t2; f32x4 c[4];
; #pragma unroll
;             for (int tj = 0; tj < 4; ++tj) c[tj] = (f32x4){0.f, 0.f, 0.f, 0.f};
; #pragma unroll
;             for (int ks = 0; ks < 4; ++ks) { const int ko = hh * 128 + 32 * ks + 8 * l4;
;                 const bf16x8 bq = *(const LAS bf16x8*)(Qt + (16 * ti + l15) * TS + ko);
; #pragma unroll
;                 for (int tj = 0; tj < 4; ++tj) { const bf16x8 ak = *(const LAS bf16x8*)(Kt + (16 * tj + l15) * TS + ko);
;                     c[tj] = __builtin_amdgcn_mfma_f32_16x16x32_bf16(ak, bq, c[tj], 0, 0, 0); } }
;             const int i = 16 * ti + l15;
; #pragma unroll
;             for (int tj = 0; tj < 4; ++tj) { const int j0 = 16 * tj + 4 * l4;
;                 v2u p; p.x = pk2(j0 <= i ? c[tj][0] : 0.f, j0 + 1 <= i ? c[tj][1] : 0.f); p.y = pk2(j0 + 2 <= i ? c[tj][2] : 0.f, j0 + 3 <= i ? c[tj][3] : 0.f);
;                 *(v2u*)(amt + i * 64 + j0) = p; } }
;         LDS_BARRIER();
;         { const float eg = __builtin_amdgcn_exp2f(Gmid);
	v_mfma_f32_16x16x32_bf16 v[16:19], v[212:215], v[36:39], v[16:19]
	ds_read_b128 v[36:39], v216 offset:54144
	v_cndmask_b32_e64 v13, 0, v13, s[8:9]
	v_bfe_u32 v46, v12, 16, 1
	s_waitcnt lgkmcnt(1)
	v_mfma_f32_16x16x32_bf16 v[8:11], v[54:57], v[28:31], v[8:11]
	v_add3_u32 v12, v12, v46, s35
	v_bfe_u32 v46, v13, 16, 1
	v_lshrrev_b32_e32 v12, 16, v12
	v_mfma_f32_16x16x32_bf16 v[20:23], v[196:199], v[28:31], v[20:23]
	v_add3_u32 v13, v13, v46, s35
	v_cmp_le_u32_e64 s[8:9], v182, v217
	ds_read_b128 v[46:49], v216 offset:54208
	v_mfma_f32_16x16x32_bf16 v[24:27], v[204:207], v[28:31], v[24:27]
	v_mfma_f32_16x16x32_bf16 v[8:11], v[62:65], v[32:35], v[8:11]
	s_waitcnt lgkmcnt(1)
	v_mfma_f32_16x16x32_bf16 v[16:19], v[36:39], v[28:31], v[16:19]
	v_and_or_b32 v28, v13, s58, v12
	v_cndmask_b32_e64 v12, 0, v14, s[8:9]
	v_cmp_le_u32_e64 s[8:9], v183, v217
	v_bfe_u32 v13, v12, 16, 1
	v_add3_u32 v30, v12, v13, s35
	v_cndmask_b32_e64 v29, 0, v15, s[8:9]
	v_mfma_f32_16x16x32_bf16 v[12:15], v[200:203], v[32:35], v[20:23]
	v_lshrrev_b32_e32 v30, 16, v30
	s_nop 1
	v_bfe_u32 v20, v29, 16, 1
	v_add3_u32 v29, v29, v20, s35
	v_mfma_f32_16x16x32_bf16 v[20:23], v[208:211], v[32:35], v[24:27]
	v_and_or_b32 v29, v29, s58, v30
	global_store_dwordx2 v[78:79], v[28:29], off offset:64
	global_store_dwordx2 v[78:79], v[226:227], off offset:96
	v_bfe_u32 v26, v8, 16, 1
	v_add3_u32 v8, v8, v26, s35
	v_bfe_u32 v26, v9, 16, 1
	v_lshrrev_b32_e32 v8, 16, v8
	v_add3_u32 v9, v9, v26, s35
	v_and_or_b32 v8, v9, s58, v8
	v_bfe_u32 v9, v10, 16, 1
	v_lshlrev_b32_e32 v24, 7, v218
	v_mov_b32_e32 v25, v69
	v_add3_u32 v9, v10, v9, s35
	v_bfe_u32 v10, v11, 16, 1
	v_lshl_add_u64 v[24:25], s[18:19], 0, v[24:25]
	v_lshrrev_b32_e32 v9, 16, v9
	v_add3_u32 v10, v11, v10, s35
	v_and_or_b32 v9, v10, s58, v9
	v_lshl_add_u64 v[10:11], v[24:25], 0, v[6:7]
	global_store_dwordx2 v[10:11], v[8:9], off
	v_cndmask_b32_e64 v8, v12, 0, vcc
	v_cndmask_b32_e64 v9, 0, v13, s[4:5]
	v_bfe_u32 v12, v8, 16, 1
	v_add3_u32 v8, v8, v12, s35
	v_bfe_u32 v12, v9, 16, 1
	v_lshrrev_b32_e32 v8, 16, v8
	v_add3_u32 v9, v9, v12, s35
	v_cmp_le_u32_e32 vcc, v179, v218
	v_and_or_b32 v8, v9, s58, v8
	s_waitcnt lgkmcnt(0)
	v_mfma_f32_16x16x32_bf16 v[16:19], v[46:49], v[32:35], v[16:19]
	v_cndmask_b32_e32 v9, 0, v14, vcc
	v_cmp_le_u32_e32 vcc, v180, v218
	v_bfe_u32 v13, v9, 16, 1
	v_add3_u32 v9, v9, v13, s35
	v_cndmask_b32_e32 v12, 0, v15, vcc
	v_bfe_u32 v13, v12, 16, 1
	v_lshrrev_b32_e32 v9, 16, v9
	v_add3_u32 v12, v12, v13, s35
	v_and_or_b32 v9, v12, s58, v9
	v_cmp_le_u32_e32 vcc, v181, v218
	global_store_dwordx2 v[10:11], v[8:9], off offset:32
	s_nop 0
	v_cndmask_b32_e32 v8, 0, v20, vcc
	v_cmp_lt_u32_e32 vcc, v181, v218
	v_bfe_u32 v12, v8, 16, 1
	v_add3_u32 v8, v8, v12, s35
	v_cndmask_b32_e32 v9, 0, v21, vcc
	v_bfe_u32 v12, v9, 16, 1
	v_lshrrev_b32_e32 v8, 16, v8
	v_add3_u32 v9, v9, v12, s35
	v_cmp_le_u32_e32 vcc, v182, v218
	v_and_or_b32 v8, v9, s58, v8
	s_nop 0
	v_cndmask_b32_e32 v9, 0, v22, vcc
	v_cmp_le_u32_e32 vcc, v183, v218
	v_bfe_u32 v13, v9, 16, 1
	v_add3_u32 v9, v9, v13, s35
	v_cndmask_b32_e32 v12, 0, v23, vcc
	v_bfe_u32 v13, v12, 16, 1
	v_lshrrev_b32_e32 v9, 16, v9
	v_add3_u32 v12, v12, v13, s35
	v_and_or_b32 v9, v12, s58, v9
	v_cmp_le_u32_e32 vcc, v184, v218
	global_store_dwordx2 v[10:11], v[8:9], off offset:64
	s_nop 0
	v_cndmask_b32_e32 v8, 0, v16, vcc
	v_cmp_lt_u32_e32 vcc, v184, v218
	v_bfe_u32 v12, v8, 16, 1
	v_add3_u32 v8, v8, v12, s35
	v_cndmask_b32_e32 v9, 0, v17, vcc
	v_bfe_u32 v12, v9, 16, 1
	v_lshrrev_b32_e32 v8, 16, v8
	v_add3_u32 v9, v9, v12, s35
	v_cmp_le_u32_e32 vcc, v185, v218
	v_and_or_b32 v8, v9, s58, v8
	s_nop 0
	v_cndmask_b32_e32 v9, 0, v18, vcc
	v_cmp_le_u32_e32 vcc, v186, v218
	v_bfe_u32 v13, v9, 16, 1
	v_add3_u32 v9, v9, v13, s35
	v_cndmask_b32_e32 v12, 0, v19, vcc
	v_bfe_u32 v13, v12, 16, 1
	v_lshrrev_b32_e32 v9, 16, v9
	v_add3_u32 v12, v12, v13, s35
	v_and_or_b32 v9, v12, s58, v9
	global_store_dwordx2 v[10:11], v[8:9], off offset:96
	v_exp_f32_e32 v8, v45
	s_waitcnt lgkmcnt(0)
	s_barrier
